# v9 + nt (non-temporal) policy on the P2 background weight-conversion loads and stores (once-read / consumed-much-later streams no longer pollute L2)
# speedup vs baseline: 1.0351x; 1.0351x over previous
.LBB0_256:
	v_lshrrev_b32_e32 v131, 4, v196
	v_mul_u32_u24_e32 v2, s18, v131
	v_and_b32_e32 v130, 60, v204
	v_mov_b32_e32 v133, 0
	v_lshlrev_b32_e32 v132, 2, v2
	v_lshl_add_u64 v[2:3], s[16:17], 0, v[132:133]
	v_lshlrev_b32_e32 v132, 2, v130
	v_or_b32_e32 v135, 4, v131
	v_lshl_add_u64 v[10:11], v[2:3], 0, v[132:133]
	v_mul_u32_u24_e32 v2, s18, v135
	v_lshlrev_b32_e32 v2, 2, v2
	v_mov_b32_e32 v3, v133
	v_lshl_add_u64 v[2:3], s[16:17], 0, v[2:3]
	v_or_b32_e32 v139, 8, v131
	v_lshl_add_u64 v[12:13], v[2:3], 0, v[132:133]
	global_load_dwordx4 v[2:5], v[10:11], off nt
	global_load_dwordx4 v[6:9], v[12:13], off nt
	v_mul_u32_u24_e32 v10, s18, v139
	v_lshlrev_b32_e32 v10, 2, v10
	v_mov_b32_e32 v11, v133
	v_lshl_add_u64 v[10:11], s[16:17], 0, v[10:11]
	v_or_b32_e32 v141, 12, v131
	v_lshl_add_u64 v[18:19], v[10:11], 0, v[132:133]
	v_mul_u32_u24_e32 v10, s18, v141
	v_lshlrev_b32_e32 v10, 2, v10
	v_mov_b32_e32 v11, v133
	v_lshl_add_u64 v[10:11], s[16:17], 0, v[10:11]
	v_or_b32_e32 v143, 16, v131
	v_lshl_add_u64 v[20:21], v[10:11], 0, v[132:133]
	global_load_dwordx4 v[10:13], v[18:19], off nt
	global_load_dwordx4 v[14:17], v[20:21], off nt
	v_mul_u32_u24_e32 v18, s18, v143
	v_lshlrev_b32_e32 v18, 2, v18
	v_mov_b32_e32 v19, v133
	v_lshl_add_u64 v[18:19], s[16:17], 0, v[18:19]
	v_or_b32_e32 v145, 20, v131
	v_lshl_add_u64 v[26:27], v[18:19], 0, v[132:133]
	v_mul_u32_u24_e32 v18, s18, v145
	v_lshlrev_b32_e32 v18, 2, v18
	v_mov_b32_e32 v19, v133
	v_lshl_add_u64 v[18:19], s[16:17], 0, v[18:19]
	v_or_b32_e32 v147, 24, v131
	v_lshl_add_u64 v[28:29], v[18:19], 0, v[132:133]
	global_load_dwordx4 v[18:21], v[26:27], off nt
	global_load_dwordx4 v[22:25], v[28:29], off nt
	v_mul_u32_u24_e32 v26, s18, v147
	v_lshlrev_b32_e32 v26, 2, v26
	v_mov_b32_e32 v27, v133
	v_lshl_add_u64 v[26:27], s[16:17], 0, v[26:27]
	v_or_b32_e32 v149, 28, v131
	v_lshl_add_u64 v[34:35], v[26:27], 0, v[132:133]
	v_mul_u32_u24_e32 v26, s18, v149
	v_lshlrev_b32_e32 v26, 2, v26
	v_mov_b32_e32 v27, v133
	v_lshl_add_u64 v[26:27], s[16:17], 0, v[26:27]
	v_or_b32_e32 v151, 32, v131
	v_lshl_add_u64 v[36:37], v[26:27], 0, v[132:133]
	global_load_dwordx4 v[26:29], v[34:35], off nt
	global_load_dwordx4 v[30:33], v[36:37], off nt
	v_mul_u32_u24_e32 v34, s18, v151
	v_lshlrev_b32_e32 v34, 2, v34
	v_mov_b32_e32 v35, v133
	v_lshl_add_u64 v[34:35], s[16:17], 0, v[34:35]
	v_or_b32_e32 v163, 36, v131
	v_lshl_add_u64 v[42:43], v[34:35], 0, v[132:133]
	v_mul_u32_u24_e32 v34, s18, v163
	v_lshlrev_b32_e32 v34, 2, v34
	v_mov_b32_e32 v35, v133
	v_lshl_add_u64 v[34:35], s[16:17], 0, v[34:35]
	v_or_b32_e32 v165, 40, v131
	v_lshl_add_u64 v[44:45], v[34:35], 0, v[132:133]
	global_load_dwordx4 v[34:37], v[42:43], off nt
	global_load_dwordx4 v[38:41], v[44:45], off nt
	v_mul_u32_u24_e32 v42, s18, v165
	v_lshlrev_b32_e32 v42, 2, v42
	v_mov_b32_e32 v43, v133
	v_lshl_add_u64 v[42:43], s[16:17], 0, v[42:43]
	v_or_b32_e32 v167, 44, v131
	v_lshl_add_u64 v[50:51], v[42:43], 0, v[132:133]
	v_mul_u32_u24_e32 v42, s18, v167
	v_lshlrev_b32_e32 v42, 2, v42
	v_mov_b32_e32 v43, v133
	v_lshl_add_u64 v[42:43], s[16:17], 0, v[42:43]
	v_or_b32_e32 v169, 48, v131
	v_lshl_add_u64 v[52:53], v[42:43], 0, v[132:133]
	global_load_dwordx4 v[42:45], v[50:51], off nt
	global_load_dwordx4 v[46:49], v[52:53], off nt
	v_mul_u32_u24_e32 v50, s18, v169
	v_lshlrev_b32_e32 v50, 2, v50
	v_mov_b32_e32 v51, v133
	v_lshl_add_u64 v[50:51], s[16:17], 0, v[50:51]
	v_or_b32_e32 v171, 52, v131
	v_lshl_add_u64 v[58:59], v[50:51], 0, v[132:133]
	v_mul_u32_u24_e32 v50, s18, v171
	v_lshlrev_b32_e32 v50, 2, v50
	v_mov_b32_e32 v51, v133
	v_lshl_add_u64 v[50:51], s[16:17], 0, v[50:51]
	v_or_b32_e32 v182, 56, v131
	v_lshl_add_u64 v[60:61], v[50:51], 0, v[132:133]
	global_load_dwordx4 v[50:53], v[58:59], off nt
	global_load_dwordx4 v[54:57], v[60:61], off nt
	v_mul_u32_u24_e32 v58, s18, v182
	v_or_b32_e32 v183, 60, v131
	v_lshlrev_b32_e32 v58, 2, v58
	v_mov_b32_e32 v59, v133
	v_mul_u32_u24_e32 v60, s18, v183
	v_lshl_add_u64 v[58:59], s[16:17], 0, v[58:59]
	v_lshlrev_b32_e32 v60, 2, v60
	v_mov_b32_e32 v61, v133
	v_lshl_add_u64 v[58:59], v[58:59], 0, v[132:133]
	v_lshl_add_u64 v[60:61], s[16:17], 0, v[60:61]
	v_lshl_add_u64 v[60:61], v[60:61], 0, v[132:133]
	global_load_dwordx4 v[74:77], v[58:59], off nt
	global_load_dwordx4 v[78:81], v[60:61], off nt
	s_mul_i32 s16, s88, 0x4100
	s_lshl_b32 s27, s52, 3
	s_add_i32 s16, s16, 0
	s_bfe_u32 s28, s87, 0x10006
	s_add_u32 s29, s50, 0x14400000
	s_addc_u32 s30, s51, 0
	s_add_u32 s31, s50, 0x4000000
	s_addc_u32 s35, s51, 0
	s_add_u32 s36, s50, 0x1600000
	s_addc_u32 s37, s51, 0
	s_add_u32 s44, s50, 0xe00000
	s_addc_u32 s45, s51, 0
	v_and_b32_e32 v60, 7, v0
	v_lshrrev_b32_e32 v134, 3, v196
	v_add_u32_e32 v58, s16, v132
	v_mul_u32_u24_e32 v59, 0x104, v131
	s_add_u32 s46, s50, 0xa00000
	v_mul_u32_u24_e32 v61, 0x820, v60
	v_lshlrev_b32_e32 v62, 2, v134
	s_addc_u32 s47, s51, 0
	v_lshlrev_b32_e32 v136, 3, v60
	v_mov_b32_e32 v137, v133
	v_add3_u32 v184, s16, v61, v62
	v_or_b32_e32 v138, 8, v134
	v_or_b32_e32 v140, 16, v134
	v_or_b32_e32 v142, 24, v134
	v_or_b32_e32 v144, 32, v134
	v_or_b32_e32 v146, 40, v134
	v_or_b32_e32 v148, 48, v134
	v_or_b32_e32 v150, 56, v134
	v_lshlrev_b32_e32 v152, 4, v60
	v_mov_b32_e32 v153, v133
	s_lshl_b32 s53, s52, 4
	s_add_i32 s54, 0, 0x27ea8
	s_add_i32 s55, 0, 0x27e90
	s_movk_i32 s56, 0x98
	s_movk_i32 s57, 0x88
	s_add_i32 s58, 0, 0x27e60
	s_add_i32 s59, 0, 0x27e58
	s_add_i32 s60, 0, 0x27e50
	s_add_i32 s61, 0, 0x27e30
	s_mov_b32 s62, 0xc3e00000
	v_add_u32_e32 v185, v58, v59
	v_mov_b32_e32 v186, 0x43e00000
	s_mov_b32 s66, s34
	s_mov_b32 s65, s26
	s_mov_b64 s[16:17], s[0:1]
	s_branch .LBB0_260
.LBB0_257:
	ds_read2_b32 v[158:159], v188 offset0:56 offset1:65
	ds_read2_b32 v[160:161], v188 offset0:121 offset1:130
	ds_read2_b32 v[172:173], v188 offset0:186 offset1:195
	ds_read2_b32 v[174:175], v189 offset0:123 offset1:132
	ds_read2_b32 v[176:177], v187 offset0:60 offset1:69
	ds_read2_b32 v[178:179], v187 offset0:125 offset1:134
	ds_read2_b32 v[190:191], v187 offset0:190 offset1:199
	v_mov_b64_e32 v[192:193], s[16:17]
	ds_read2_b32 v[200:201], v188 offset0:8 offset1:16
	ds_read2_b32 v[206:207], v188 offset0:73 offset1:81
	ds_read2_b32 v[208:209], v188 offset0:138 offset1:146
	ds_read2_b32 v[210:211], v188 offset0:203 offset1:211
	ds_read2_b32 v[212:213], v187 offset0:12 offset1:20
	ds_read2_b32 v[214:215], v187 offset0:77 offset1:85
	ds_read2_b32 v[216:217], v187 offset0:142 offset1:150
	ds_read2_b32 v[218:219], v187 offset0:207 offset1:215
	v_mad_u64_u32 v[198:199], s[18:19], s65, v134, v[192:193]
	v_lshl_add_u64 v[198:199], v[198:199], 0, v[152:153]
	s_waitcnt lgkmcnt(14)
	v_cvt_pk_bf16_f32 v154, v132, v159
	s_waitcnt lgkmcnt(12)
	v_cvt_pk_bf16_f32 v155, v161, v173
	s_waitcnt lgkmcnt(10)
	v_cvt_pk_bf16_f32 v156, v175, v177
	s_waitcnt lgkmcnt(8)
	v_cvt_pk_bf16_f32 v157, v179, v191
	global_store_dwordx4 v[198:199], v[154:157], off nt
	v_mad_u64_u32 v[198:199], s[18:19], s65, v138, v[192:193]
	v_lshl_add_u64 v[198:199], v[198:199], 0, v[152:153]
	s_waitcnt lgkmcnt(6)
	v_cvt_pk_bf16_f32 v154, v200, v206
	s_waitcnt lgkmcnt(4)
	v_cvt_pk_bf16_f32 v155, v208, v210
	s_waitcnt lgkmcnt(2)
	v_cvt_pk_bf16_f32 v156, v212, v214
	s_waitcnt lgkmcnt(0)
	v_cvt_pk_bf16_f32 v157, v216, v218
	global_store_dwordx4 v[198:199], v[154:157], off nt
	v_mad_u64_u32 v[198:199], s[18:19], s65, v140, v[192:193]
	s_nop 0
	v_cvt_pk_bf16_f32 v154, v201, v207
	v_cvt_pk_bf16_f32 v155, v209, v211
	v_cvt_pk_bf16_f32 v156, v213, v215
	v_cvt_pk_bf16_f32 v157, v217, v219
	ds_read2_b32 v[200:201], v188 offset0:24 offset1:32
	ds_read2_b32 v[206:207], v188 offset0:89 offset1:97
	ds_read2_b32 v[208:209], v188 offset0:154 offset1:162
	ds_read2_b32 v[210:211], v188 offset0:219 offset1:227
	ds_read2_b32 v[212:213], v187 offset0:28 offset1:36
	ds_read2_b32 v[214:215], v187 offset0:93 offset1:101
	ds_read2_b32 v[216:217], v187 offset0:158 offset1:166
	ds_read2_b32 v[218:219], v187 offset0:223 offset1:231
	v_lshl_add_u64 v[198:199], v[198:199], 0, v[152:153]
	global_store_dwordx4 v[198:199], v[154:157], off nt
	v_mad_u64_u32 v[198:199], s[18:19], s65, v142, v[192:193]
	v_lshl_add_u64 v[198:199], v[198:199], 0, v[152:153]
	s_waitcnt lgkmcnt(6)
	v_cvt_pk_bf16_f32 v154, v200, v206
	s_waitcnt lgkmcnt(4)
	v_cvt_pk_bf16_f32 v155, v208, v210
	s_waitcnt lgkmcnt(2)
	v_cvt_pk_bf16_f32 v156, v212, v214
	s_waitcnt lgkmcnt(0)
	v_cvt_pk_bf16_f32 v157, v216, v218
	global_store_dwordx4 v[198:199], v[154:157], off nt
	v_mad_u64_u32 v[198:199], s[18:19], s65, v144, v[192:193]
	s_nop 0
	v_cvt_pk_bf16_f32 v154, v201, v207
	v_cvt_pk_bf16_f32 v155, v209, v211
	v_cvt_pk_bf16_f32 v156, v213, v215
	v_cvt_pk_bf16_f32 v157, v217, v219
	ds_read2_b32 v[200:201], v188 offset0:40 offset1:48
	ds_read2_b32 v[206:207], v188 offset0:105 offset1:113
	ds_read2_b32 v[208:209], v188 offset0:170 offset1:178
	ds_read2_b32 v[188:189], v188 offset0:235 offset1:243
	ds_read2_b32 v[210:211], v187 offset0:44 offset1:52
	ds_read2_b32 v[212:213], v187 offset0:109 offset1:117
	ds_read2_b32 v[214:215], v187 offset0:174 offset1:182
	ds_read2_b32 v[216:217], v187 offset0:239 offset1:247
	v_lshl_add_u64 v[198:199], v[198:199], 0, v[152:153]
	global_store_dwordx4 v[198:199], v[154:157], off nt
	v_mad_u64_u32 v[198:199], s[18:19], s65, v146, v[192:193]
	s_waitcnt lgkmcnt(4)
	v_cvt_pk_bf16_f32 v155, v208, v188
	v_lshl_add_u64 v[198:199], v[198:199], 0, v[152:153]
	v_cvt_pk_bf16_f32 v154, v200, v206
	s_waitcnt lgkmcnt(2)
	v_cvt_pk_bf16_f32 v156, v210, v212
	s_waitcnt lgkmcnt(0)
	v_cvt_pk_bf16_f32 v157, v214, v216
	global_store_dwordx4 v[198:199], v[154:157], off nt
	ds_read_b32 v132, v184 offset:18428
	s_nop 0
	v_cvt_pk_bf16_f32 v155, v209, v189
	v_mad_u64_u32 v[188:189], s[18:19], s65, v148, v[192:193]
	v_cvt_pk_bf16_f32 v154, v201, v207
	v_lshl_add_u64 v[188:189], v[188:189], 0, v[152:153]
	v_cvt_pk_bf16_f32 v156, v211, v213
	v_cvt_pk_bf16_f32 v157, v215, v217
	global_store_dwordx4 v[188:189], v[154:157], off nt
	s_nop 1
	v_cvt_pk_bf16_f32 v154, v158, v160
	v_mad_u64_u32 v[158:159], s[18:19], s65, v150, v[192:193]
	v_lshl_add_u64 v[158:159], v[158:159], 0, v[152:153]
	v_cvt_pk_bf16_f32 v155, v172, v174
	v_cvt_pk_bf16_f32 v156, v176, v178
	s_waitcnt lgkmcnt(0)
	v_cvt_pk_bf16_f32 v157, v190, v132
	global_store_dwordx4 v[158:159], v[154:157], off nt

.LBB0_288:
	v_mul_u32_u24_e32 v58, s22, v131
	v_mul_u32_u24_e32 v60, s22, v135
	v_mul_u32_u24_e32 v66, s22, v139
	v_mul_u32_u24_e32 v68, s22, v141
	v_mul_u32_u24_e32 v82, s22, v143
	v_mul_u32_u24_e32 v84, s22, v145
	v_mul_u32_u24_e32 v90, s22, v147
	v_mul_u32_u24_e32 v92, s22, v149
	v_mul_u32_u24_e32 v98, s22, v151
	v_mul_u32_u24_e32 v100, s22, v163
	v_mul_u32_u24_e32 v106, s22, v165
	v_mul_u32_u24_e32 v108, s22, v167
	v_mul_u32_u24_e32 v114, s22, v169
	v_mul_u32_u24_e32 v116, s22, v171
	v_mul_u32_u24_e32 v122, s22, v182
	v_mul_u32_u24_e32 v124, s22, v183
	s_waitcnt lgkmcnt(0)
	v_lshlrev_b32_e32 v132, 2, v58
	v_lshlrev_b32_e32 v60, 2, v60
	v_mov_b32_e32 v61, v133
	v_lshlrev_b32_e32 v66, 2, v66
	v_mov_b32_e32 v67, v133
	v_lshlrev_b32_e32 v68, 2, v68
	v_mov_b32_e32 v69, v133
	v_lshlrev_b32_e32 v82, 2, v82
	v_mov_b32_e32 v83, v133
	v_lshlrev_b32_e32 v84, 2, v84
	v_mov_b32_e32 v85, v133
	v_lshlrev_b32_e32 v90, 2, v90
	v_mov_b32_e32 v91, v133
	v_lshlrev_b32_e32 v92, 2, v92
	v_mov_b32_e32 v93, v133
	v_lshlrev_b32_e32 v98, 2, v98
	v_mov_b32_e32 v99, v133
	v_lshlrev_b32_e32 v100, 2, v100
	v_mov_b32_e32 v101, v133
	v_lshlrev_b32_e32 v106, 2, v106
	v_mov_b32_e32 v107, v133
	v_lshlrev_b32_e32 v108, 2, v108
	v_mov_b32_e32 v109, v133
	v_lshlrev_b32_e32 v114, 2, v114
	v_mov_b32_e32 v115, v133
	v_lshlrev_b32_e32 v116, 2, v116
	v_mov_b32_e32 v117, v133
	v_lshlrev_b32_e32 v122, 2, v122
	v_mov_b32_e32 v123, v133
	v_lshlrev_b32_e32 v124, 2, v124
	v_mov_b32_e32 v125, v133
	v_lshl_add_u64 v[58:59], s[20:21], 0, v[132:133]
	v_lshlrev_b32_e32 v132, 2, v130
	v_lshl_add_u64 v[60:61], s[20:21], 0, v[60:61]
	v_lshl_add_u64 v[66:67], s[20:21], 0, v[66:67]
	v_lshl_add_u64 v[68:69], s[20:21], 0, v[68:69]
	v_lshl_add_u64 v[82:83], s[20:21], 0, v[82:83]
	v_lshl_add_u64 v[84:85], s[20:21], 0, v[84:85]
	v_lshl_add_u64 v[90:91], s[20:21], 0, v[90:91]
	v_lshl_add_u64 v[92:93], s[20:21], 0, v[92:93]
	v_lshl_add_u64 v[98:99], s[20:21], 0, v[98:99]
	v_lshl_add_u64 v[100:101], s[20:21], 0, v[100:101]
	v_lshl_add_u64 v[106:107], s[20:21], 0, v[106:107]
	v_lshl_add_u64 v[108:109], s[20:21], 0, v[108:109]
	v_lshl_add_u64 v[114:115], s[20:21], 0, v[114:115]
	v_lshl_add_u64 v[116:117], s[20:21], 0, v[116:117]
	v_lshl_add_u64 v[122:123], s[20:21], 0, v[122:123]
	v_lshl_add_u64 v[124:125], s[20:21], 0, v[124:125]
	v_lshl_add_u64 v[58:59], v[58:59], 0, v[132:133]
	v_lshl_add_u64 v[60:61], v[60:61], 0, v[132:133]
	v_lshl_add_u64 v[66:67], v[66:67], 0, v[132:133]
	v_lshl_add_u64 v[68:69], v[68:69], 0, v[132:133]
	v_lshl_add_u64 v[82:83], v[82:83], 0, v[132:133]
	v_lshl_add_u64 v[84:85], v[84:85], 0, v[132:133]
	v_lshl_add_u64 v[90:91], v[90:91], 0, v[132:133]
	v_lshl_add_u64 v[92:93], v[92:93], 0, v[132:133]
	v_lshl_add_u64 v[98:99], v[98:99], 0, v[132:133]
	v_lshl_add_u64 v[100:101], v[100:101], 0, v[132:133]
	v_lshl_add_u64 v[106:107], v[106:107], 0, v[132:133]
	v_lshl_add_u64 v[108:109], v[108:109], 0, v[132:133]
	v_lshl_add_u64 v[114:115], v[114:115], 0, v[132:133]
	v_lshl_add_u64 v[116:117], v[116:117], 0, v[132:133]
	v_lshl_add_u64 v[122:123], v[122:123], 0, v[132:133]
	v_lshl_add_u64 v[124:125], v[124:125], 0, v[132:133]
	global_load_dwordx4 v[62:65], v[58:59], off nt
	s_nop 0
	global_load_dwordx4 v[58:61], v[60:61], off nt
	s_nop 0
	global_load_dwordx4 v[70:73], v[66:67], off nt
	s_nop 0
	global_load_dwordx4 v[66:69], v[68:69], off nt
	s_nop 0
	global_load_dwordx4 v[86:89], v[82:83], off nt
	s_nop 0
	global_load_dwordx4 v[82:85], v[84:85], off nt
	s_nop 0
	global_load_dwordx4 v[94:97], v[90:91], off nt
	s_nop 0
	global_load_dwordx4 v[90:93], v[92:93], off nt
	s_nop 0
	global_load_dwordx4 v[102:105], v[98:99], off nt
	s_nop 0
	global_load_dwordx4 v[98:101], v[100:101], off nt
	s_nop 0
	global_load_dwordx4 v[110:113], v[106:107], off nt
	s_nop 0
	global_load_dwordx4 v[106:109], v[108:109], off nt
	s_nop 0
	global_load_dwordx4 v[118:121], v[114:115], off nt
	s_nop 0
	global_load_dwordx4 v[114:117], v[116:117], off nt
	s_nop 0
	global_load_dwordx4 v[126:129], v[122:123], off nt
	s_nop 0
	global_load_dwordx4 v[122:125], v[124:125], off nt
.LBB0_289:
	v_add_u32_e32 v190, 0x4000, v185
	v_add_u32_e32 v191, 0x4008, v185
	v_add_u32_e32 v192, 0x4410, v185
	v_add_u32_e32 v193, 0x4418, v185
	v_add_u32_e32 v198, 0x4820, v185
	v_add_u32_e32 v199, 0x4828, v185
	v_add_u32_e32 v200, 0x4c30, v185
	v_add_u32_e32 v201, 0x4c38, v185
	v_add_u32_e32 v205, 0x5040, v185
	v_add_u32_e32 v206, 0x5048, v185
	v_add_u32_e32 v207, 0x5450, v185
	v_add_u32_e32 v208, 0x5458, v185
	v_add_u32_e32 v209, 0x5860, v185
	v_add_u32_e32 v210, 0x5868, v185
	v_add_u32_e32 v211, 0x5c70, v185
	v_add_u32_e32 v212, 0x5c78, v185
	v_add_u32_e32 v213, 0x6080, v185
	v_add_u32_e32 v214, 0x6088, v185
	v_add_u32_e32 v215, 0x6490, v185
	v_add_u32_e32 v216, 0x6498, v185
	v_add_u32_e32 v217, 0x68a0, v185
	v_add_u32_e32 v218, 0x68a8, v185
	v_add_u32_e32 v219, 0x6cb0, v185
	v_add_u32_e32 v220, 0x6cb8, v185
	v_add_u32_e32 v221, 0x70c0, v185
	v_add_u32_e32 v222, 0x70c8, v185
	v_add_u32_e32 v223, 0x74d0, v185
	v_add_u32_e32 v224, 0x74d8, v185
	v_add_u32_e32 v225, 0x78e0, v185
	v_add_u32_e32 v226, 0x78e8, v185
	v_add_u32_e32 v227, 0x7cf0, v185
	v_add_u32_e32 v228, 0x7cf8, v185
	s_waitcnt vmcnt(15)
	ds_write2_b32 v190, v2, v3 offset1:1
	ds_write2_b32 v191, v4, v5 offset1:1
	s_waitcnt vmcnt(14)
	ds_write2_b32 v192, v6, v7 offset1:1
	ds_write2_b32 v193, v8, v9 offset1:1
	s_waitcnt vmcnt(13)
	ds_write2_b32 v198, v10, v11 offset1:1
	ds_write2_b32 v199, v12, v13 offset1:1
	s_waitcnt vmcnt(12)
	ds_write2_b32 v200, v14, v15 offset1:1
	ds_write2_b32 v201, v16, v17 offset1:1
	s_waitcnt vmcnt(11)
	ds_write2_b32 v205, v18, v19 offset1:1
	ds_write2_b32 v206, v20, v21 offset1:1
	s_waitcnt vmcnt(10)
	ds_write2_b32 v207, v22, v23 offset1:1
	ds_write2_b32 v208, v24, v25 offset1:1
	s_waitcnt vmcnt(9)
	ds_write2_b32 v209, v26, v27 offset1:1
	ds_write2_b32 v210, v28, v29 offset1:1
	s_waitcnt vmcnt(8)
	ds_write2_b32 v211, v30, v31 offset1:1
	ds_write2_b32 v212, v32, v33 offset1:1
	s_waitcnt vmcnt(7)
	ds_write2_b32 v213, v34, v35 offset1:1
	ds_write2_b32 v214, v36, v37 offset1:1
	s_waitcnt vmcnt(6)
	ds_write2_b32 v215, v38, v39 offset1:1
	ds_write2_b32 v216, v40, v41 offset1:1
	s_waitcnt vmcnt(5)
	ds_write2_b32 v217, v42, v43 offset1:1
	ds_write2_b32 v218, v44, v45 offset1:1
	s_waitcnt vmcnt(4)
	ds_write2_b32 v219, v46, v47 offset1:1
	ds_write2_b32 v220, v48, v49 offset1:1
	s_waitcnt vmcnt(3)
	ds_write2_b32 v221, v50, v51 offset1:1
	ds_write2_b32 v222, v52, v53 offset1:1
	s_waitcnt vmcnt(2)
	ds_write2_b32 v223, v54, v55 offset1:1
	ds_write2_b32 v224, v56, v57 offset1:1
	s_waitcnt vmcnt(1)
	ds_write2_b32 v225, v74, v75 offset1:1
	ds_write2_b32 v226, v76, v77 offset1:1
	s_waitcnt vmcnt(0)
	ds_write2_b32 v227, v78, v79 offset1:1
	ds_write2_b32 v228, v80, v81 offset1:1
	s_waitcnt lgkmcnt(0)
	ds_read_b32 v132, v184 offset:16384
	v_cmp_eq_f32_e64 s[20:21], s34, 0
	s_and_b64 vcc, exec, s[20:21]
	v_add_u32_e32 v188, 0x4000, v184
	v_add_u32_e32 v189, 0x4200, v184
	v_add_u32_e32 v187, 0x4400, v184
	s_cbranch_vccnz .LBB0_310
	ds_read2_b32 v[154:155], v188 offset0:56 offset1:65
	ds_read2_b32 v[156:157], v188 offset0:121 offset1:130
	ds_read2_b32 v[158:159], v188 offset0:186 offset1:195
	s_waitcnt lgkmcnt(3)
	v_mul_f32_e32 v160, s34, v132
	v_med3_f32 v160, v160, s62, v186
	s_waitcnt lgkmcnt(2)
	v_mul_f32_e32 v155, s34, v155
	v_med3_f32 v155, v155, s62, v186
	v_mov_b32_e32 v230, v133
	v_cvt_pk_fp8_f32 v230, v160, v155
	ds_read2_b32 v[174:175], v189 offset0:123 offset1:132
	ds_read2_b32 v[160:161], v187 offset0:60 offset1:69
	ds_read2_b32 v[172:173], v187 offset0:125 offset1:134
	s_waitcnt lgkmcnt(4)
	v_mul_f32_e32 v157, s34, v157
	s_waitcnt lgkmcnt(3)
	v_mul_f32_e32 v159, s34, v159
	v_med3_f32 v157, v157, s62, v186
	v_med3_f32 v155, v159, s62, v186
	ds_read2_b32 v[178:179], v187 offset0:190 offset1:199
	v_cvt_pk_fp8_f32 v230, v157, v155 op_sel:[0,0,1]
	s_waitcnt lgkmcnt(3)
	v_mul_f32_e32 v155, s34, v175
	s_waitcnt lgkmcnt(2)
	v_mul_f32_e32 v157, s34, v161
	v_med3_f32 v155, v155, s62, v186
	v_med3_f32 v157, v157, s62, v186
	v_mov_b32_e32 v231, v133
	v_cvt_pk_fp8_f32 v231, v155, v157
	s_waitcnt lgkmcnt(1)
	v_mul_f32_e32 v159, s34, v173
	s_waitcnt lgkmcnt(0)
	v_mul_f32_e32 v155, s34, v179
	v_med3_f32 v157, v159, s62, v186
	v_med3_f32 v155, v155, s62, v186
	v_cvt_pk_fp8_f32 v231, v157, v155 op_sel:[0,0,1]
	ds_read2_b32 v[234:235], v188 offset0:8 offset1:16
	ds_read2_b32 v[236:237], v188 offset0:73 offset1:81
	ds_read2_b32 v[238:239], v188 offset0:138 offset1:146
	ds_read2_b32 v[240:241], v188 offset0:203 offset1:211
	v_mov_b64_e32 v[176:177], s[0:1]
	v_mad_u64_u32 v[232:233], s[20:21], s26, v134, v[176:177]
	v_lshl_add_u64 v[232:233], v[232:233], 0, v[136:137]
	s_waitcnt lgkmcnt(3)
	v_mul_f32_e32 v155, s34, v234
	s_waitcnt lgkmcnt(2)
	v_mul_f32_e32 v157, s34, v236
	global_store_dwordx2 v[232:233], v[230:231], off nt
	v_med3_f32 v155, v155, s62, v186
	v_med3_f32 v157, v157, s62, v186
	v_mov_b32_e32 v230, v133
	v_cvt_pk_fp8_f32 v230, v155, v157
	ds_read2_b32 v[232:233], v187 offset0:12 offset1:20
	ds_read2_b32 v[242:243], v187 offset0:77 offset1:85
	ds_read2_b32 v[244:245], v187 offset0:142 offset1:150
	s_waitcnt lgkmcnt(4)
	v_mul_f32_e32 v159, s34, v238
	s_waitcnt lgkmcnt(3)
	v_mul_f32_e32 v161, s34, v240
	v_med3_f32 v159, v159, s62, v186
	v_med3_f32 v155, v161, s62, v186
	ds_read2_b32 v[246:247], v187 offset0:207 offset1:215
	v_cvt_pk_fp8_f32 v230, v159, v155 op_sel:[0,0,1]
	s_waitcnt lgkmcnt(3)
	v_mul_f32_e32 v155, s34, v232
	s_waitcnt lgkmcnt(2)
	v_mul_f32_e32 v157, s34, v242
	v_med3_f32 v155, v155, s62, v186
	v_med3_f32 v157, v157, s62, v186
	v_mov_b32_e32 v231, v133
	v_cvt_pk_fp8_f32 v231, v155, v157
	s_waitcnt lgkmcnt(1)
	v_mul_f32_e32 v159, s34, v244
	s_waitcnt lgkmcnt(0)
	v_mul_f32_e32 v155, s34, v246
	v_med3_f32 v157, v159, s62, v186
	v_med3_f32 v155, v155, s62, v186
	v_cvt_pk_fp8_f32 v231, v157, v155 op_sel:[0,0,1]
	v_mad_u64_u32 v[248:249], s[20:21], s26, v138, v[176:177]
	v_lshl_add_u64 v[248:249], v[248:249], 0, v[136:137]
	v_mul_f32_e32 v155, s34, v235
	v_mul_f32_e32 v157, s34, v237
	global_store_dwordx2 v[248:249], v[230:231], off nt
	v_med3_f32 v155, v155, s62, v186
	v_med3_f32 v157, v157, s62, v186
	v_mov_b32_e32 v230, v133
	v_cvt_pk_fp8_f32 v230, v155, v157
	v_mul_f32_e32 v159, s34, v239
	v_mul_f32_e32 v155, s34, v241
	v_med3_f32 v157, v159, s62, v186
	v_med3_f32 v155, v155, s62, v186
	v_cvt_pk_fp8_f32 v230, v157, v155 op_sel:[0,0,1]
	v_mul_f32_e32 v155, s34, v233
	v_mul_f32_e32 v157, s34, v243
	v_med3_f32 v155, v155, s62, v186
	v_med3_f32 v157, v157, s62, v186
	v_mov_b32_e32 v231, v133
	v_cvt_pk_fp8_f32 v231, v155, v157
	v_mul_f32_e32 v159, s34, v245
	v_mul_f32_e32 v155, s34, v247
	v_med3_f32 v157, v159, s62, v186
	v_med3_f32 v155, v155, s62, v186
	v_cvt_pk_fp8_f32 v231, v157, v155 op_sel:[0,0,1]
	ds_read2_b32 v[234:235], v188 offset0:24 offset1:32
	ds_read2_b32 v[236:237], v188 offset0:89 offset1:97
	ds_read2_b32 v[238:239], v188 offset0:154 offset1:162
	ds_read2_b32 v[240:241], v188 offset0:219 offset1:227
	v_mad_u64_u32 v[232:233], s[20:21], s26, v140, v[176:177]
	v_lshl_add_u64 v[232:233], v[232:233], 0, v[136:137]
	s_waitcnt lgkmcnt(3)
	v_mul_f32_e32 v155, s34, v234
	s_waitcnt lgkmcnt(2)
	v_mul_f32_e32 v157, s34, v236
	global_store_dwordx2 v[232:233], v[230:231], off nt
	v_med3_f32 v155, v155, s62, v186
	v_med3_f32 v157, v157, s62, v186
	v_mov_b32_e32 v230, v133
	v_cvt_pk_fp8_f32 v230, v155, v157
	ds_read2_b32 v[232:233], v187 offset0:28 offset1:36
	ds_read2_b32 v[242:243], v187 offset0:93 offset1:101
	ds_read2_b32 v[244:245], v187 offset0:158 offset1:166
	s_waitcnt lgkmcnt(4)
	v_mul_f32_e32 v159, s34, v238
	s_waitcnt lgkmcnt(3)
	v_mul_f32_e32 v161, s34, v240
	v_med3_f32 v159, v159, s62, v186
	v_med3_f32 v155, v161, s62, v186
	ds_read2_b32 v[246:247], v187 offset0:223 offset1:231
	v_cvt_pk_fp8_f32 v230, v159, v155 op_sel:[0,0,1]
	s_waitcnt lgkmcnt(3)
	v_mul_f32_e32 v155, s34, v232
	s_waitcnt lgkmcnt(2)
	v_mul_f32_e32 v157, s34, v242
	v_med3_f32 v155, v155, s62, v186
	v_med3_f32 v157, v157, s62, v186
	v_mov_b32_e32 v231, v133
	v_cvt_pk_fp8_f32 v231, v155, v157
	s_waitcnt lgkmcnt(1)
	v_mul_f32_e32 v159, s34, v244
	s_waitcnt lgkmcnt(0)
	v_mul_f32_e32 v155, s34, v246
	v_med3_f32 v157, v159, s62, v186
	v_med3_f32 v155, v155, s62, v186
	v_cvt_pk_fp8_f32 v231, v157, v155 op_sel:[0,0,1]
	v_mad_u64_u32 v[248:249], s[20:21], s26, v142, v[176:177]
	v_lshl_add_u64 v[248:249], v[248:249], 0, v[136:137]
	v_mul_f32_e32 v155, s34, v235
	v_mul_f32_e32 v157, s34, v237
	global_store_dwordx2 v[248:249], v[230:231], off nt
	v_med3_f32 v155, v155, s62, v186
	v_med3_f32 v157, v157, s62, v186
	v_mov_b32_e32 v230, v133
	v_cvt_pk_fp8_f32 v230, v155, v157
	v_mul_f32_e32 v159, s34, v239
	v_mul_f32_e32 v155, s34, v241
	v_med3_f32 v157, v159, s62, v186
	v_med3_f32 v155, v155, s62, v186
	v_cvt_pk_fp8_f32 v230, v157, v155 op_sel:[0,0,1]
	v_mul_f32_e32 v155, s34, v233
	v_mul_f32_e32 v157, s34, v243
	v_med3_f32 v155, v155, s62, v186
	v_med3_f32 v157, v157, s62, v186
	v_mov_b32_e32 v231, v133
	v_cvt_pk_fp8_f32 v231, v155, v157
	v_mul_f32_e32 v159, s34, v245
	v_mul_f32_e32 v155, s34, v247
	v_med3_f32 v157, v159, s62, v186
	v_med3_f32 v155, v155, s62, v186
	v_cvt_pk_fp8_f32 v231, v157, v155 op_sel:[0,0,1]
	ds_read2_b32 v[234:235], v188 offset0:40 offset1:48
	ds_read2_b32 v[236:237], v188 offset0:105 offset1:113
	ds_read2_b32 v[238:239], v188 offset0:170 offset1:178
	ds_read2_b32 v[240:241], v188 offset0:235 offset1:243
	v_mad_u64_u32 v[232:233], s[20:21], s26, v144, v[176:177]
	v_lshl_add_u64 v[232:233], v[232:233], 0, v[136:137]
	s_waitcnt lgkmcnt(3)
	v_mul_f32_e32 v155, s34, v234
	s_waitcnt lgkmcnt(2)
	v_mul_f32_e32 v157, s34, v236
	global_store_dwordx2 v[232:233], v[230:231], off nt
	v_med3_f32 v155, v155, s62, v186
	v_med3_f32 v157, v157, s62, v186
	v_mov_b32_e32 v230, v133
	v_cvt_pk_fp8_f32 v230, v155, v157
	ds_read2_b32 v[232:233], v187 offset0:44 offset1:52
	ds_read2_b32 v[242:243], v187 offset0:109 offset1:117
	ds_read2_b32 v[244:245], v187 offset0:174 offset1:182
	s_waitcnt lgkmcnt(4)
	v_mul_f32_e32 v159, s34, v238
	s_waitcnt lgkmcnt(3)
	v_mul_f32_e32 v161, s34, v240
	v_med3_f32 v159, v159, s62, v186
	v_med3_f32 v155, v161, s62, v186
	ds_read2_b32 v[246:247], v187 offset0:239 offset1:247
	v_cvt_pk_fp8_f32 v230, v159, v155 op_sel:[0,0,1]
	s_waitcnt lgkmcnt(3)
	v_mul_f32_e32 v155, s34, v232
	s_waitcnt lgkmcnt(2)
	v_mul_f32_e32 v157, s34, v242
	v_med3_f32 v155, v155, s62, v186
	v_med3_f32 v157, v157, s62, v186
	v_mov_b32_e32 v231, v133
	v_cvt_pk_fp8_f32 v231, v155, v157
	s_waitcnt lgkmcnt(1)
	v_mul_f32_e32 v159, s34, v244
	s_waitcnt lgkmcnt(0)
	v_mul_f32_e32 v155, s34, v246
	v_med3_f32 v157, v159, s62, v186
	v_med3_f32 v155, v155, s62, v186
	v_cvt_pk_fp8_f32 v231, v157, v155 op_sel:[0,0,1]
	v_mad_u64_u32 v[248:249], s[20:21], s26, v146, v[176:177]
	v_lshl_add_u64 v[248:249], v[248:249], 0, v[136:137]
	v_mul_f32_e32 v155, s34, v235
	v_mul_f32_e32 v157, s34, v237
	global_store_dwordx2 v[248:249], v[230:231], off nt
	v_med3_f32 v155, v155, s62, v186
	v_med3_f32 v157, v157, s62, v186
	v_mov_b32_e32 v230, v133
	v_cvt_pk_fp8_f32 v230, v155, v157
	v_mul_f32_e32 v159, s34, v239
	v_mul_f32_e32 v155, s34, v241
	v_med3_f32 v157, v159, s62, v186
	v_med3_f32 v155, v155, s62, v186
	v_cvt_pk_fp8_f32 v230, v157, v155 op_sel:[0,0,1]
	v_mul_f32_e32 v155, s34, v233
	v_mul_f32_e32 v157, s34, v243
	v_med3_f32 v155, v155, s62, v186
	v_med3_f32 v157, v157, s62, v186
	v_mov_b32_e32 v231, v133
	v_cvt_pk_fp8_f32 v231, v155, v157
	v_mul_f32_e32 v159, s34, v245
	v_mul_f32_e32 v155, s34, v247
	v_med3_f32 v157, v159, s62, v186
	v_med3_f32 v155, v155, s62, v186
	v_cvt_pk_fp8_f32 v231, v157, v155 op_sel:[0,0,1]
	v_mul_f32_e32 v154, s34, v154
	v_mul_f32_e32 v155, s34, v156
	v_med3_f32 v157, v154, s62, v186
	v_med3_f32 v155, v155, s62, v186
	v_mov_b32_e32 v154, v133
	v_cvt_pk_fp8_f32 v154, v157, v155
	v_mul_f32_e32 v156, s34, v158
	v_mul_f32_e32 v155, s34, v174
	v_med3_f32 v156, v156, s62, v186
	v_med3_f32 v155, v155, s62, v186
	ds_read_b32 v158, v184 offset:18428
	v_cvt_pk_fp8_f32 v154, v156, v155 op_sel:[0,0,1]
	v_mul_f32_e32 v155, s34, v160
	v_mul_f32_e32 v156, s34, v172
	v_med3_f32 v159, v155, s62, v186
	v_med3_f32 v156, v156, s62, v186
	v_mov_b32_e32 v155, v133
	v_cvt_pk_fp8_f32 v155, v159, v156
	v_mul_f32_e32 v157, s34, v178
	s_waitcnt lgkmcnt(0)
	v_mul_f32_e32 v156, s34, v158
	v_med3_f32 v157, v157, s62, v186
	v_med3_f32 v156, v156, s62, v186
	v_cvt_pk_fp8_f32 v155, v157, v156 op_sel:[0,0,1]
	v_mad_u64_u32 v[232:233], s[20:21], s26, v148, v[176:177]
	v_mad_u64_u32 v[156:157], s[20:21], s26, v150, v[176:177]
	v_lshl_add_u64 v[232:233], v[232:233], 0, v[136:137]
	v_lshl_add_u64 v[156:157], v[156:157], 0, v[136:137]
	global_store_dwordx2 v[232:233], v[230:231], off nt
	global_store_dwordx2 v[156:157], v[154:155], off nt
	s_cbranch_execnz .LBB0_292
.LBB0_291:
	ds_read2_b32 v[158:159], v188 offset0:56 offset1:65
	ds_read2_b32 v[160:161], v188 offset0:121 offset1:130
	ds_read2_b32 v[172:173], v188 offset0:186 offset1:195
	ds_read2_b32 v[174:175], v189 offset0:123 offset1:132
	ds_read2_b32 v[176:177], v187 offset0:60 offset1:69
	ds_read2_b32 v[178:179], v187 offset0:125 offset1:134
	ds_read2_b32 v[230:231], v187 offset0:190 offset1:199
	v_mov_b64_e32 v[232:233], s[0:1]
	ds_read2_b32 v[236:237], v188 offset0:8 offset1:16
	ds_read2_b32 v[238:239], v188 offset0:73 offset1:81
	ds_read2_b32 v[240:241], v188 offset0:138 offset1:146
	ds_read2_b32 v[242:243], v188 offset0:203 offset1:211
	ds_read2_b32 v[244:245], v187 offset0:12 offset1:20
	ds_read2_b32 v[246:247], v187 offset0:77 offset1:85
	ds_read2_b32 v[248:249], v187 offset0:142 offset1:150
	ds_read2_b32 v[250:251], v187 offset0:207 offset1:215
	v_mad_u64_u32 v[234:235], s[20:21], s26, v134, v[232:233]
	v_lshl_add_u64 v[234:235], v[234:235], 0, v[152:153]
	s_waitcnt lgkmcnt(14)
	v_cvt_pk_bf16_f32 v154, v132, v159
	s_waitcnt lgkmcnt(12)
	v_cvt_pk_bf16_f32 v155, v161, v173
	s_waitcnt lgkmcnt(10)
	v_cvt_pk_bf16_f32 v156, v175, v177
	s_waitcnt lgkmcnt(8)
	v_cvt_pk_bf16_f32 v157, v179, v231
	global_store_dwordx4 v[234:235], v[154:157], off nt
	v_mad_u64_u32 v[234:235], s[20:21], s26, v138, v[232:233]
	v_lshl_add_u64 v[234:235], v[234:235], 0, v[152:153]
	s_waitcnt lgkmcnt(6)
	v_cvt_pk_bf16_f32 v154, v236, v238
	s_waitcnt lgkmcnt(4)
	v_cvt_pk_bf16_f32 v155, v240, v242
	s_waitcnt lgkmcnt(2)
	v_cvt_pk_bf16_f32 v156, v244, v246
	s_waitcnt lgkmcnt(0)
	v_cvt_pk_bf16_f32 v157, v248, v250
	global_store_dwordx4 v[234:235], v[154:157], off nt
	v_mad_u64_u32 v[234:235], s[20:21], s26, v140, v[232:233]
	s_nop 0
	v_cvt_pk_bf16_f32 v154, v237, v239
	v_cvt_pk_bf16_f32 v155, v241, v243
	v_cvt_pk_bf16_f32 v156, v245, v247
	v_cvt_pk_bf16_f32 v157, v249, v251
	ds_read2_b32 v[236:237], v188 offset0:24 offset1:32
	ds_read2_b32 v[238:239], v188 offset0:89 offset1:97
	ds_read2_b32 v[240:241], v188 offset0:154 offset1:162
	ds_read2_b32 v[242:243], v188 offset0:219 offset1:227
	ds_read2_b32 v[244:245], v187 offset0:28 offset1:36
	ds_read2_b32 v[246:247], v187 offset0:93 offset1:101
	ds_read2_b32 v[248:249], v187 offset0:158 offset1:166
	ds_read2_b32 v[250:251], v187 offset0:223 offset1:231
	v_lshl_add_u64 v[234:235], v[234:235], 0, v[152:153]
	global_store_dwordx4 v[234:235], v[154:157], off nt
	v_mad_u64_u32 v[234:235], s[20:21], s26, v142, v[232:233]
	v_lshl_add_u64 v[234:235], v[234:235], 0, v[152:153]
	s_waitcnt lgkmcnt(6)
	v_cvt_pk_bf16_f32 v154, v236, v238
	s_waitcnt lgkmcnt(4)
	v_cvt_pk_bf16_f32 v155, v240, v242
	s_waitcnt lgkmcnt(2)
	v_cvt_pk_bf16_f32 v156, v244, v246
	s_waitcnt lgkmcnt(0)
	v_cvt_pk_bf16_f32 v157, v248, v250
	global_store_dwordx4 v[234:235], v[154:157], off nt
	v_mad_u64_u32 v[234:235], s[20:21], s26, v144, v[232:233]
	s_nop 0
	v_cvt_pk_bf16_f32 v154, v237, v239
	v_cvt_pk_bf16_f32 v155, v241, v243
	v_cvt_pk_bf16_f32 v156, v245, v247
	v_cvt_pk_bf16_f32 v157, v249, v251
	ds_read2_b32 v[236:237], v188 offset0:40 offset1:48
	ds_read2_b32 v[238:239], v188 offset0:105 offset1:113
	ds_read2_b32 v[240:241], v188 offset0:170 offset1:178
	ds_read2_b32 v[242:243], v188 offset0:235 offset1:243
	ds_read2_b32 v[244:245], v187 offset0:44 offset1:52
	ds_read2_b32 v[246:247], v187 offset0:109 offset1:117
	ds_read2_b32 v[248:249], v187 offset0:174 offset1:182
	ds_read2_b32 v[250:251], v187 offset0:239 offset1:247
	v_lshl_add_u64 v[234:235], v[234:235], 0, v[152:153]
	global_store_dwordx4 v[234:235], v[154:157], off nt
	v_mad_u64_u32 v[234:235], s[20:21], s26, v146, v[232:233]
	v_lshl_add_u64 v[234:235], v[234:235], 0, v[152:153]
	s_waitcnt lgkmcnt(6)
	v_cvt_pk_bf16_f32 v154, v236, v238
	s_waitcnt lgkmcnt(4)
	v_cvt_pk_bf16_f32 v155, v240, v242
	s_waitcnt lgkmcnt(2)
	v_cvt_pk_bf16_f32 v156, v244, v246
	s_waitcnt lgkmcnt(0)
	v_cvt_pk_bf16_f32 v157, v248, v250
	global_store_dwordx4 v[234:235], v[154:157], off nt
	v_mad_u64_u32 v[234:235], s[20:21], s26, v148, v[232:233]
	s_nop 0
	v_cvt_pk_bf16_f32 v154, v237, v239
	v_lshl_add_u64 v[234:235], v[234:235], 0, v[152:153]
	v_cvt_pk_bf16_f32 v155, v241, v243
	v_cvt_pk_bf16_f32 v156, v245, v247
	v_cvt_pk_bf16_f32 v157, v249, v251
	global_store_dwordx4 v[234:235], v[154:157], off nt
	ds_read_b32 v132, v184 offset:18428
	s_nop 0
	v_cvt_pk_bf16_f32 v154, v158, v160
	v_mad_u64_u32 v[158:159], s[20:21], s26, v150, v[232:233]
	v_lshl_add_u64 v[158:159], v[158:159], 0, v[152:153]
	v_cvt_pk_bf16_f32 v155, v172, v174
	v_cvt_pk_bf16_f32 v156, v176, v178
	s_waitcnt lgkmcnt(0)
	v_cvt_pk_bf16_f32 v157, v230, v132
	global_store_dwordx4 v[158:159], v[154:157], off nt

.LBB0_325:
	v_mul_u32_u24_e32 v2, s20, v131
	v_mul_u32_u24_e32 v4, s20, v135
	v_mul_u32_u24_e32 v10, s20, v139
	v_mul_u32_u24_e32 v12, s20, v141
	v_mul_u32_u24_e32 v18, s20, v143
	v_mul_u32_u24_e32 v20, s20, v145
	v_mul_u32_u24_e32 v26, s20, v147
	v_mul_u32_u24_e32 v28, s20, v149
	v_mul_u32_u24_e32 v34, s20, v151
	v_mul_u32_u24_e32 v36, s20, v163
	v_mul_u32_u24_e32 v42, s20, v165
	v_mul_u32_u24_e32 v44, s20, v167
	v_mul_u32_u24_e32 v50, s20, v169
	v_mul_u32_u24_e32 v52, s20, v171
	v_mul_u32_u24_e32 v74, s20, v182
	v_mul_u32_u24_e32 v76, s20, v183
	s_waitcnt lgkmcnt(0)
	v_lshlrev_b32_e32 v132, 2, v2
	v_lshlrev_b32_e32 v4, 2, v4
	v_mov_b32_e32 v5, v133
	v_lshlrev_b32_e32 v10, 2, v10
	v_mov_b32_e32 v11, v133
	v_lshlrev_b32_e32 v12, 2, v12
	v_mov_b32_e32 v13, v133
	v_lshlrev_b32_e32 v18, 2, v18
	v_mov_b32_e32 v19, v133
	v_lshlrev_b32_e32 v20, 2, v20
	v_mov_b32_e32 v21, v133
	v_lshlrev_b32_e32 v26, 2, v26
	v_mov_b32_e32 v27, v133
	v_lshlrev_b32_e32 v28, 2, v28
	v_mov_b32_e32 v29, v133
	v_lshlrev_b32_e32 v34, 2, v34
	v_mov_b32_e32 v35, v133
	v_lshlrev_b32_e32 v36, 2, v36
	v_mov_b32_e32 v37, v133
	v_lshlrev_b32_e32 v42, 2, v42
	v_mov_b32_e32 v43, v133
	v_lshlrev_b32_e32 v44, 2, v44
	v_mov_b32_e32 v45, v133
	v_lshlrev_b32_e32 v50, 2, v50
	v_mov_b32_e32 v51, v133
	v_lshlrev_b32_e32 v52, 2, v52
	v_mov_b32_e32 v53, v133
	v_lshlrev_b32_e32 v74, 2, v74
	v_mov_b32_e32 v75, v133
	v_lshlrev_b32_e32 v76, 2, v76
	v_mov_b32_e32 v77, v133
	v_lshl_add_u64 v[2:3], s[18:19], 0, v[132:133]
	v_lshlrev_b32_e32 v132, 2, v130
	v_lshl_add_u64 v[4:5], s[18:19], 0, v[4:5]
	v_lshl_add_u64 v[10:11], s[18:19], 0, v[10:11]
	v_lshl_add_u64 v[12:13], s[18:19], 0, v[12:13]
	v_lshl_add_u64 v[18:19], s[18:19], 0, v[18:19]
	v_lshl_add_u64 v[20:21], s[18:19], 0, v[20:21]
	v_lshl_add_u64 v[26:27], s[18:19], 0, v[26:27]
	v_lshl_add_u64 v[28:29], s[18:19], 0, v[28:29]
	v_lshl_add_u64 v[34:35], s[18:19], 0, v[34:35]
	v_lshl_add_u64 v[36:37], s[18:19], 0, v[36:37]
	v_lshl_add_u64 v[42:43], s[18:19], 0, v[42:43]
	v_lshl_add_u64 v[44:45], s[18:19], 0, v[44:45]
	v_lshl_add_u64 v[50:51], s[18:19], 0, v[50:51]
	v_lshl_add_u64 v[52:53], s[18:19], 0, v[52:53]
	v_lshl_add_u64 v[74:75], s[18:19], 0, v[74:75]
	v_lshl_add_u64 v[76:77], s[18:19], 0, v[76:77]
	v_lshl_add_u64 v[2:3], v[2:3], 0, v[132:133]
	v_lshl_add_u64 v[6:7], v[4:5], 0, v[132:133]
	v_lshl_add_u64 v[10:11], v[10:11], 0, v[132:133]
	v_lshl_add_u64 v[14:15], v[12:13], 0, v[132:133]
	v_lshl_add_u64 v[18:19], v[18:19], 0, v[132:133]
	v_lshl_add_u64 v[22:23], v[20:21], 0, v[132:133]
	v_lshl_add_u64 v[26:27], v[26:27], 0, v[132:133]
	v_lshl_add_u64 v[30:31], v[28:29], 0, v[132:133]
	v_lshl_add_u64 v[34:35], v[34:35], 0, v[132:133]
	v_lshl_add_u64 v[38:39], v[36:37], 0, v[132:133]
	v_lshl_add_u64 v[42:43], v[42:43], 0, v[132:133]
	v_lshl_add_u64 v[46:47], v[44:45], 0, v[132:133]
	v_lshl_add_u64 v[50:51], v[50:51], 0, v[132:133]
	v_lshl_add_u64 v[54:55], v[52:53], 0, v[132:133]
	v_lshl_add_u64 v[74:75], v[74:75], 0, v[132:133]
	v_lshl_add_u64 v[78:79], v[76:77], 0, v[132:133]
	global_load_dwordx4 v[2:5], v[2:3], off nt
	s_nop 0
	global_load_dwordx4 v[6:9], v[6:7], off nt
	s_nop 0
	global_load_dwordx4 v[10:13], v[10:11], off nt
	s_nop 0
	global_load_dwordx4 v[14:17], v[14:15], off nt
	s_nop 0
	global_load_dwordx4 v[18:21], v[18:19], off nt
	s_nop 0
	global_load_dwordx4 v[22:25], v[22:23], off nt
	s_nop 0
	global_load_dwordx4 v[26:29], v[26:27], off nt
	s_nop 0
	global_load_dwordx4 v[30:33], v[30:31], off nt
	s_nop 0
	global_load_dwordx4 v[34:37], v[34:35], off nt
	s_nop 0
	global_load_dwordx4 v[38:41], v[38:39], off nt
	s_nop 0
	global_load_dwordx4 v[42:45], v[42:43], off nt
	s_nop 0
	global_load_dwordx4 v[46:49], v[46:47], off nt
	s_nop 0
	global_load_dwordx4 v[50:53], v[50:51], off nt
	s_nop 0
	global_load_dwordx4 v[54:57], v[54:55], off nt
	s_nop 0
	global_load_dwordx4 v[74:77], v[74:75], off nt
	s_nop 0
	global_load_dwordx4 v[78:81], v[78:79], off nt
.LBB0_326:
	ds_write2_b32 v190, v62, v63 offset1:1
	ds_write2_b32 v191, v64, v65 offset1:1
	ds_write2_b32 v192, v58, v59 offset1:1
	ds_write2_b32 v193, v60, v61 offset1:1
	ds_write2_b32 v198, v70, v71 offset1:1
	ds_write2_b32 v199, v72, v73 offset1:1
	ds_write2_b32 v200, v66, v67 offset1:1
	ds_write2_b32 v201, v68, v69 offset1:1
	ds_write2_b32 v205, v86, v87 offset1:1
	ds_write2_b32 v206, v88, v89 offset1:1
	ds_write2_b32 v207, v82, v83 offset1:1
	ds_write2_b32 v208, v84, v85 offset1:1
	ds_write2_b32 v209, v94, v95 offset1:1
	ds_write2_b32 v210, v96, v97 offset1:1
	ds_write2_b32 v211, v90, v91 offset1:1
	ds_write2_b32 v212, v92, v93 offset1:1
	ds_write2_b32 v213, v102, v103 offset1:1
	ds_write2_b32 v214, v104, v105 offset1:1
	ds_write2_b32 v215, v98, v99 offset1:1
	ds_write2_b32 v216, v100, v101 offset1:1
	ds_write2_b32 v217, v110, v111 offset1:1
	ds_write2_b32 v218, v112, v113 offset1:1
	ds_write2_b32 v219, v106, v107 offset1:1
	ds_write2_b32 v220, v108, v109 offset1:1
	ds_write2_b32 v221, v118, v119 offset1:1
	ds_write2_b32 v222, v120, v121 offset1:1
	ds_write2_b32 v223, v114, v115 offset1:1
	ds_write2_b32 v224, v116, v117 offset1:1
	ds_write2_b32 v225, v126, v127 offset1:1
	ds_write2_b32 v226, v128, v129 offset1:1
	ds_write2_b32 v227, v122, v123 offset1:1
	ds_write2_b32 v228, v124, v125 offset1:1
	s_waitcnt lgkmcnt(0)
	s_waitcnt lgkmcnt(14)
	ds_read_b32 v132, v184 offset:16384
	v_cmp_eq_f32_e64 s[18:19], s66, 0
	s_and_b64 vcc, exec, s[18:19]
	s_cbranch_vccnz .LBB0_328
	ds_read2_b32 v[154:155], v188 offset0:56 offset1:65
	ds_read2_b32 v[156:157], v188 offset0:121 offset1:130
	ds_read2_b32 v[158:159], v188 offset0:186 offset1:195
	s_waitcnt lgkmcnt(3)
	v_mul_f32_e32 v160, s66, v132
	v_med3_f32 v160, v160, s62, v186
	s_waitcnt lgkmcnt(2)
	v_mul_f32_e32 v155, s66, v155
	v_med3_f32 v155, v155, s62, v186
	v_mov_b32_e32 v190, v133
	v_cvt_pk_fp8_f32 v190, v160, v155
	ds_read2_b32 v[174:175], v189 offset0:123 offset1:132
	ds_read2_b32 v[160:161], v187 offset0:60 offset1:69
	ds_read2_b32 v[172:173], v187 offset0:125 offset1:134
	s_waitcnt lgkmcnt(4)
	v_mul_f32_e32 v157, s66, v157
	s_waitcnt lgkmcnt(3)
	v_mul_f32_e32 v159, s66, v159
	v_med3_f32 v157, v157, s62, v186
	v_med3_f32 v155, v159, s62, v186
	ds_read2_b32 v[178:179], v187 offset0:190 offset1:199
	v_cvt_pk_fp8_f32 v190, v157, v155 op_sel:[0,0,1]
	s_waitcnt lgkmcnt(3)
	v_mul_f32_e32 v155, s66, v175
	s_waitcnt lgkmcnt(2)
	v_mul_f32_e32 v157, s66, v161
	v_med3_f32 v155, v155, s62, v186
	v_med3_f32 v157, v157, s62, v186
	v_mov_b32_e32 v191, v133
	v_cvt_pk_fp8_f32 v191, v155, v157
	s_waitcnt lgkmcnt(1)
	v_mul_f32_e32 v159, s66, v173
	s_waitcnt lgkmcnt(0)
	v_mul_f32_e32 v155, s66, v179
	v_med3_f32 v157, v159, s62, v186
	v_med3_f32 v155, v155, s62, v186
	v_cvt_pk_fp8_f32 v191, v157, v155 op_sel:[0,0,1]
	ds_read2_b32 v[198:199], v188 offset0:8 offset1:16
	ds_read2_b32 v[200:201], v188 offset0:73 offset1:81
	ds_read2_b32 v[206:207], v188 offset0:138 offset1:146
	ds_read2_b32 v[208:209], v188 offset0:203 offset1:211
	v_mov_b64_e32 v[176:177], s[16:17]
	v_mad_u64_u32 v[192:193], s[18:19], s65, v134, v[176:177]
	v_lshl_add_u64 v[192:193], v[192:193], 0, v[136:137]
	s_waitcnt lgkmcnt(3)
	v_mul_f32_e32 v155, s66, v198
	s_waitcnt lgkmcnt(2)
	v_mul_f32_e32 v157, s66, v200
	global_store_dwordx2 v[192:193], v[190:191], off nt
	v_med3_f32 v155, v155, s62, v186
	v_med3_f32 v157, v157, s62, v186
	v_mov_b32_e32 v190, v133
	v_cvt_pk_fp8_f32 v190, v155, v157
	ds_read2_b32 v[192:193], v187 offset0:12 offset1:20
	ds_read2_b32 v[210:211], v187 offset0:77 offset1:85
	ds_read2_b32 v[212:213], v187 offset0:142 offset1:150
	s_waitcnt lgkmcnt(4)
	v_mul_f32_e32 v159, s66, v206
	s_waitcnt lgkmcnt(3)
	v_mul_f32_e32 v161, s66, v208
	v_med3_f32 v159, v159, s62, v186
	v_med3_f32 v155, v161, s62, v186
	ds_read2_b32 v[214:215], v187 offset0:207 offset1:215
	v_cvt_pk_fp8_f32 v190, v159, v155 op_sel:[0,0,1]
	s_waitcnt lgkmcnt(3)
	v_mul_f32_e32 v155, s66, v192
	s_waitcnt lgkmcnt(2)
	v_mul_f32_e32 v157, s66, v210
	v_med3_f32 v155, v155, s62, v186
	v_med3_f32 v157, v157, s62, v186
	v_mov_b32_e32 v191, v133
	v_cvt_pk_fp8_f32 v191, v155, v157
	s_waitcnt lgkmcnt(1)
	v_mul_f32_e32 v159, s66, v212
	s_waitcnt lgkmcnt(0)
	v_mul_f32_e32 v155, s66, v214
	v_med3_f32 v157, v159, s62, v186
	v_med3_f32 v155, v155, s62, v186
	v_cvt_pk_fp8_f32 v191, v157, v155 op_sel:[0,0,1]
	v_mad_u64_u32 v[216:217], s[18:19], s65, v138, v[176:177]
	v_lshl_add_u64 v[216:217], v[216:217], 0, v[136:137]
	v_mul_f32_e32 v155, s66, v199
	v_mul_f32_e32 v157, s66, v201
	global_store_dwordx2 v[216:217], v[190:191], off nt
	v_med3_f32 v155, v155, s62, v186
	v_med3_f32 v157, v157, s62, v186
	v_mov_b32_e32 v190, v133
	v_cvt_pk_fp8_f32 v190, v155, v157
	v_mul_f32_e32 v159, s66, v207
	v_mul_f32_e32 v155, s66, v209
	v_med3_f32 v157, v159, s62, v186
	v_med3_f32 v155, v155, s62, v186
	v_cvt_pk_fp8_f32 v190, v157, v155 op_sel:[0,0,1]
	v_mul_f32_e32 v155, s66, v193
	v_mul_f32_e32 v157, s66, v211
	v_med3_f32 v155, v155, s62, v186
	v_med3_f32 v157, v157, s62, v186
	v_mov_b32_e32 v191, v133
	v_cvt_pk_fp8_f32 v191, v155, v157
	v_mul_f32_e32 v159, s66, v213
	v_mul_f32_e32 v155, s66, v215
	v_med3_f32 v157, v159, s62, v186
	v_med3_f32 v155, v155, s62, v186
	v_cvt_pk_fp8_f32 v191, v157, v155 op_sel:[0,0,1]
	ds_read2_b32 v[198:199], v188 offset0:24 offset1:32
	ds_read2_b32 v[200:201], v188 offset0:89 offset1:97
	ds_read2_b32 v[206:207], v188 offset0:154 offset1:162
	ds_read2_b32 v[208:209], v188 offset0:219 offset1:227
	v_mad_u64_u32 v[192:193], s[18:19], s65, v140, v[176:177]
	v_lshl_add_u64 v[192:193], v[192:193], 0, v[136:137]
	s_waitcnt lgkmcnt(3)
	v_mul_f32_e32 v155, s66, v198
	s_waitcnt lgkmcnt(2)
	v_mul_f32_e32 v157, s66, v200
	global_store_dwordx2 v[192:193], v[190:191], off nt
	v_med3_f32 v155, v155, s62, v186
	v_med3_f32 v157, v157, s62, v186
	v_mov_b32_e32 v190, v133
	v_cvt_pk_fp8_f32 v190, v155, v157
	ds_read2_b32 v[192:193], v187 offset0:28 offset1:36
	ds_read2_b32 v[210:211], v187 offset0:93 offset1:101
	ds_read2_b32 v[212:213], v187 offset0:158 offset1:166
	s_waitcnt lgkmcnt(4)
	v_mul_f32_e32 v159, s66, v206
	s_waitcnt lgkmcnt(3)
	v_mul_f32_e32 v161, s66, v208
	v_med3_f32 v159, v159, s62, v186
	v_med3_f32 v155, v161, s62, v186
	ds_read2_b32 v[214:215], v187 offset0:223 offset1:231
	v_cvt_pk_fp8_f32 v190, v159, v155 op_sel:[0,0,1]
	s_waitcnt lgkmcnt(3)
	v_mul_f32_e32 v155, s66, v192
	s_waitcnt lgkmcnt(2)
	v_mul_f32_e32 v157, s66, v210
	v_med3_f32 v155, v155, s62, v186
	v_med3_f32 v157, v157, s62, v186
	v_mov_b32_e32 v191, v133
	v_cvt_pk_fp8_f32 v191, v155, v157
	s_waitcnt lgkmcnt(1)
	v_mul_f32_e32 v159, s66, v212
	s_waitcnt lgkmcnt(0)
	v_mul_f32_e32 v155, s66, v214
	v_med3_f32 v157, v159, s62, v186
	v_med3_f32 v155, v155, s62, v186
	v_cvt_pk_fp8_f32 v191, v157, v155 op_sel:[0,0,1]
	v_mad_u64_u32 v[216:217], s[18:19], s65, v142, v[176:177]
	v_lshl_add_u64 v[216:217], v[216:217], 0, v[136:137]
	v_mul_f32_e32 v155, s66, v199
	v_mul_f32_e32 v157, s66, v201
	global_store_dwordx2 v[216:217], v[190:191], off nt
	v_med3_f32 v155, v155, s62, v186
	v_med3_f32 v157, v157, s62, v186
	v_mov_b32_e32 v190, v133
	v_cvt_pk_fp8_f32 v190, v155, v157
	v_mul_f32_e32 v159, s66, v207
	v_mul_f32_e32 v155, s66, v209
	v_med3_f32 v157, v159, s62, v186
	v_med3_f32 v155, v155, s62, v186
	v_cvt_pk_fp8_f32 v190, v157, v155 op_sel:[0,0,1]
	v_mul_f32_e32 v155, s66, v193
	v_mul_f32_e32 v157, s66, v211
	v_med3_f32 v155, v155, s62, v186
	v_med3_f32 v157, v157, s62, v186
	v_mov_b32_e32 v191, v133
	v_cvt_pk_fp8_f32 v191, v155, v157
	v_mul_f32_e32 v159, s66, v213
	v_mul_f32_e32 v155, s66, v215
	v_med3_f32 v157, v159, s62, v186
	v_med3_f32 v155, v155, s62, v186
	v_cvt_pk_fp8_f32 v191, v157, v155 op_sel:[0,0,1]
	ds_read2_b32 v[198:199], v188 offset0:40 offset1:48
	ds_read2_b32 v[200:201], v188 offset0:105 offset1:113
	ds_read2_b32 v[206:207], v188 offset0:170 offset1:178
	ds_read2_b32 v[208:209], v188 offset0:235 offset1:243
	v_mad_u64_u32 v[192:193], s[18:19], s65, v144, v[176:177]
	v_lshl_add_u64 v[192:193], v[192:193], 0, v[136:137]
	s_waitcnt lgkmcnt(3)
	v_mul_f32_e32 v155, s66, v198
	s_waitcnt lgkmcnt(2)
	v_mul_f32_e32 v157, s66, v200
	global_store_dwordx2 v[192:193], v[190:191], off nt
	v_med3_f32 v155, v155, s62, v186
	v_med3_f32 v157, v157, s62, v186
	v_mov_b32_e32 v190, v133
	v_cvt_pk_fp8_f32 v190, v155, v157
	ds_read2_b32 v[192:193], v187 offset0:44 offset1:52
	ds_read2_b32 v[210:211], v187 offset0:109 offset1:117
	ds_read2_b32 v[212:213], v187 offset0:174 offset1:182
	s_waitcnt lgkmcnt(4)
	v_mul_f32_e32 v159, s66, v206
	s_waitcnt lgkmcnt(3)
	v_mul_f32_e32 v161, s66, v208
	v_med3_f32 v159, v159, s62, v186
	v_med3_f32 v155, v161, s62, v186
	ds_read2_b32 v[214:215], v187 offset0:239 offset1:247
	v_cvt_pk_fp8_f32 v190, v159, v155 op_sel:[0,0,1]
	s_waitcnt lgkmcnt(3)
	v_mul_f32_e32 v155, s66, v192
	s_waitcnt lgkmcnt(2)
	v_mul_f32_e32 v157, s66, v210
	v_med3_f32 v155, v155, s62, v186
	v_med3_f32 v157, v157, s62, v186
	v_mov_b32_e32 v191, v133
	v_cvt_pk_fp8_f32 v191, v155, v157
	s_waitcnt lgkmcnt(1)
	v_mul_f32_e32 v159, s66, v212
	s_waitcnt lgkmcnt(0)
	v_mul_f32_e32 v155, s66, v214
	v_med3_f32 v157, v159, s62, v186
	v_med3_f32 v155, v155, s62, v186
	v_cvt_pk_fp8_f32 v191, v157, v155 op_sel:[0,0,1]
	v_mad_u64_u32 v[216:217], s[18:19], s65, v146, v[176:177]
	v_lshl_add_u64 v[216:217], v[216:217], 0, v[136:137]
	v_mul_f32_e32 v155, s66, v199
	v_mul_f32_e32 v157, s66, v201
	global_store_dwordx2 v[216:217], v[190:191], off nt
	v_med3_f32 v155, v155, s62, v186
	v_med3_f32 v157, v157, s62, v186
	v_mov_b32_e32 v190, v133
	v_cvt_pk_fp8_f32 v190, v155, v157
	v_mul_f32_e32 v159, s66, v207
	v_mul_f32_e32 v155, s66, v209
	v_med3_f32 v157, v159, s62, v186
	v_med3_f32 v155, v155, s62, v186
	v_cvt_pk_fp8_f32 v190, v157, v155 op_sel:[0,0,1]
	v_mul_f32_e32 v155, s66, v193
	v_mul_f32_e32 v157, s66, v211
	v_med3_f32 v155, v155, s62, v186
	v_med3_f32 v157, v157, s62, v186
	v_mov_b32_e32 v191, v133
	v_cvt_pk_fp8_f32 v191, v155, v157
	v_mul_f32_e32 v159, s66, v213
	v_mul_f32_e32 v155, s66, v215
	v_med3_f32 v157, v159, s62, v186
	v_med3_f32 v155, v155, s62, v186
	v_cvt_pk_fp8_f32 v191, v157, v155 op_sel:[0,0,1]
	v_mul_f32_e32 v154, s66, v154
	v_mul_f32_e32 v155, s66, v156
	v_med3_f32 v157, v154, s62, v186
	v_med3_f32 v155, v155, s62, v186
	v_mov_b32_e32 v154, v133
	v_cvt_pk_fp8_f32 v154, v157, v155
	v_mul_f32_e32 v156, s66, v158
	v_mul_f32_e32 v155, s66, v174
	v_med3_f32 v156, v156, s62, v186
	v_med3_f32 v155, v155, s62, v186
	ds_read_b32 v158, v184 offset:18428
	v_cvt_pk_fp8_f32 v154, v156, v155 op_sel:[0,0,1]
	v_mul_f32_e32 v155, s66, v160
	v_mul_f32_e32 v156, s66, v172
	v_med3_f32 v159, v155, s62, v186
	v_med3_f32 v156, v156, s62, v186
	v_mov_b32_e32 v155, v133
	v_cvt_pk_fp8_f32 v155, v159, v156
	v_mul_f32_e32 v157, s66, v178
	s_waitcnt lgkmcnt(0)
	v_mul_f32_e32 v156, s66, v158
	v_med3_f32 v157, v157, s62, v186
	v_med3_f32 v156, v156, s62, v186
	v_cvt_pk_fp8_f32 v155, v157, v156 op_sel:[0,0,1]
	v_mad_u64_u32 v[192:193], s[18:19], s65, v148, v[176:177]
	v_mad_u64_u32 v[156:157], s[18:19], s65, v150, v[176:177]
	v_lshl_add_u64 v[192:193], v[192:193], 0, v[136:137]
	v_lshl_add_u64 v[156:157], v[156:157], 0, v[136:137]
	global_store_dwordx2 v[192:193], v[190:191], off nt
	global_store_dwordx2 v[156:157], v[154:155], off nt
	s_cbranch_execnz .LBB0_258
	s_branch .LBB0_257

.LBB0_413:
	v_lshrrev_b32_e32 v131, 4, v196
	v_mul_u32_u24_e32 v2, s12, v131
	v_and_b32_e32 v130, 60, v204
	v_mov_b32_e32 v133, 0
	v_lshlrev_b32_e32 v132, 2, v2
	v_lshl_add_u64 v[2:3], s[10:11], 0, v[132:133]
	v_lshlrev_b32_e32 v132, 2, v130
	v_or_b32_e32 v135, 4, v131
	v_lshl_add_u64 v[10:11], v[2:3], 0, v[132:133]
	v_mul_u32_u24_e32 v2, s12, v135
	v_lshlrev_b32_e32 v2, 2, v2
	v_mov_b32_e32 v3, v133
	v_lshl_add_u64 v[2:3], s[10:11], 0, v[2:3]
	v_or_b32_e32 v139, 8, v131
	v_lshl_add_u64 v[12:13], v[2:3], 0, v[132:133]
	global_load_dwordx4 v[2:5], v[10:11], off nt
	global_load_dwordx4 v[6:9], v[12:13], off nt
	v_mul_u32_u24_e32 v10, s12, v139
	v_lshlrev_b32_e32 v10, 2, v10
	v_mov_b32_e32 v11, v133
	v_lshl_add_u64 v[10:11], s[10:11], 0, v[10:11]
	v_or_b32_e32 v141, 12, v131
	v_lshl_add_u64 v[18:19], v[10:11], 0, v[132:133]
	v_mul_u32_u24_e32 v10, s12, v141
	v_lshlrev_b32_e32 v10, 2, v10
	v_mov_b32_e32 v11, v133
	v_lshl_add_u64 v[10:11], s[10:11], 0, v[10:11]
	v_or_b32_e32 v143, 16, v131
	v_lshl_add_u64 v[20:21], v[10:11], 0, v[132:133]
	global_load_dwordx4 v[10:13], v[18:19], off nt
	global_load_dwordx4 v[14:17], v[20:21], off nt
	v_mul_u32_u24_e32 v18, s12, v143
	v_lshlrev_b32_e32 v18, 2, v18
	v_mov_b32_e32 v19, v133
	v_lshl_add_u64 v[18:19], s[10:11], 0, v[18:19]
	v_or_b32_e32 v145, 20, v131
	v_lshl_add_u64 v[26:27], v[18:19], 0, v[132:133]
	v_mul_u32_u24_e32 v18, s12, v145
	v_lshlrev_b32_e32 v18, 2, v18
	v_mov_b32_e32 v19, v133
	v_lshl_add_u64 v[18:19], s[10:11], 0, v[18:19]
	v_or_b32_e32 v147, 24, v131
	v_lshl_add_u64 v[28:29], v[18:19], 0, v[132:133]
	global_load_dwordx4 v[18:21], v[26:27], off nt
	global_load_dwordx4 v[22:25], v[28:29], off nt
	v_mul_u32_u24_e32 v26, s12, v147
	v_lshlrev_b32_e32 v26, 2, v26
	v_mov_b32_e32 v27, v133
	v_lshl_add_u64 v[26:27], s[10:11], 0, v[26:27]
	v_or_b32_e32 v149, 28, v131
	v_lshl_add_u64 v[34:35], v[26:27], 0, v[132:133]
	v_mul_u32_u24_e32 v26, s12, v149
	v_lshlrev_b32_e32 v26, 2, v26
	v_mov_b32_e32 v27, v133
	v_lshl_add_u64 v[26:27], s[10:11], 0, v[26:27]
	v_or_b32_e32 v151, 32, v131
	v_lshl_add_u64 v[36:37], v[26:27], 0, v[132:133]
	global_load_dwordx4 v[26:29], v[34:35], off nt
	global_load_dwordx4 v[30:33], v[36:37], off nt
	v_mul_u32_u24_e32 v34, s12, v151
	v_lshlrev_b32_e32 v34, 2, v34
	v_mov_b32_e32 v35, v133
	v_lshl_add_u64 v[34:35], s[10:11], 0, v[34:35]
	v_or_b32_e32 v163, 36, v131
	v_lshl_add_u64 v[42:43], v[34:35], 0, v[132:133]
	v_mul_u32_u24_e32 v34, s12, v163
	v_lshlrev_b32_e32 v34, 2, v34
	v_mov_b32_e32 v35, v133
	v_lshl_add_u64 v[34:35], s[10:11], 0, v[34:35]
	v_or_b32_e32 v165, 40, v131
	v_lshl_add_u64 v[44:45], v[34:35], 0, v[132:133]
	global_load_dwordx4 v[34:37], v[42:43], off nt
	global_load_dwordx4 v[38:41], v[44:45], off nt
	v_mul_u32_u24_e32 v42, s12, v165
	v_lshlrev_b32_e32 v42, 2, v42
	v_mov_b32_e32 v43, v133
	v_lshl_add_u64 v[42:43], s[10:11], 0, v[42:43]
	v_or_b32_e32 v167, 44, v131
	v_lshl_add_u64 v[50:51], v[42:43], 0, v[132:133]
	v_mul_u32_u24_e32 v42, s12, v167
	v_lshlrev_b32_e32 v42, 2, v42
	v_mov_b32_e32 v43, v133
	v_lshl_add_u64 v[42:43], s[10:11], 0, v[42:43]
	v_or_b32_e32 v169, 48, v131
	v_lshl_add_u64 v[52:53], v[42:43], 0, v[132:133]
	global_load_dwordx4 v[42:45], v[50:51], off nt
	global_load_dwordx4 v[46:49], v[52:53], off nt
	v_mul_u32_u24_e32 v50, s12, v169
	v_lshlrev_b32_e32 v50, 2, v50
	v_mov_b32_e32 v51, v133
	v_lshl_add_u64 v[50:51], s[10:11], 0, v[50:51]
	v_or_b32_e32 v171, 52, v131
	v_lshl_add_u64 v[58:59], v[50:51], 0, v[132:133]
	v_mul_u32_u24_e32 v50, s12, v171
	v_lshlrev_b32_e32 v50, 2, v50
	v_mov_b32_e32 v51, v133
	v_lshl_add_u64 v[50:51], s[10:11], 0, v[50:51]
	v_or_b32_e32 v180, 56, v131
	v_lshl_add_u64 v[60:61], v[50:51], 0, v[132:133]
	global_load_dwordx4 v[50:53], v[58:59], off nt
	global_load_dwordx4 v[54:57], v[60:61], off nt
	v_mul_u32_u24_e32 v58, s12, v180
	v_or_b32_e32 v181, 60, v131
	v_lshlrev_b32_e32 v58, 2, v58
	v_mov_b32_e32 v59, v133
	v_mul_u32_u24_e32 v60, s12, v181
	v_lshl_add_u64 v[58:59], s[10:11], 0, v[58:59]
	v_lshlrev_b32_e32 v60, 2, v60
	v_mov_b32_e32 v61, v133
	v_lshl_add_u64 v[58:59], v[58:59], 0, v[132:133]
	v_lshl_add_u64 v[60:61], s[10:11], 0, v[60:61]
	v_lshl_add_u64 v[60:61], v[60:61], 0, v[132:133]
	global_load_dwordx4 v[74:77], v[58:59], off nt
	global_load_dwordx4 v[78:81], v[60:61], off nt
	s_lshl_b32 s23, s52, 3
	s_bfe_u32 s24, s87, 0x10006
	s_add_u32 s25, s50, 0x14400000
	s_addc_u32 s26, s51, 0
	s_add_u32 s27, s50, 0x4000000
	s_addc_u32 s28, s51, 0
	s_add_u32 s29, s50, 0x1600000
	s_addc_u32 s30, s51, 0
	s_add_u32 s31, s50, 0xe00000
	s_addc_u32 s34, s51, 0
	v_and_b32_e32 v60, 7, v0
	v_lshrrev_b32_e32 v134, 3, v196
	v_add_u32_e32 v58, s20, v132
	v_mul_u32_u24_e32 v59, 0x104, v131
	s_add_u32 s35, s50, 0xa00000
	v_mul_u32_u24_e32 v61, 0x820, v60
	v_lshlrev_b32_e32 v62, 2, v134
	s_addc_u32 s37, s51, 0
	v_lshlrev_b32_e32 v136, 3, v60
	v_mov_b32_e32 v137, v133
	v_add3_u32 v182, s20, v61, v62
	v_or_b32_e32 v138, 8, v134
	v_or_b32_e32 v140, 16, v134
	v_or_b32_e32 v142, 24, v134
	v_or_b32_e32 v144, 32, v134
	v_or_b32_e32 v146, 40, v134
	v_or_b32_e32 v148, 48, v134
	v_or_b32_e32 v150, 56, v134
	v_lshlrev_b32_e32 v152, 4, v60
	v_mov_b32_e32 v153, v133
	s_lshl_b32 s42, s52, 4
	s_add_i32 s43, 0, 0x27ea8
	s_add_i32 s44, 0, 0x27e90
	s_movk_i32 s45, 0x98
	s_movk_i32 s46, 0x88
	s_add_i32 s47, 0, 0x27e60
	s_add_i32 s53, 0, 0x27e58
	s_add_i32 s54, 0, 0x27e50
	s_add_i32 s55, 0, 0x27e30
	s_mov_b32 s56, 0xc3e00000
	v_add_u32_e32 v183, v58, v59
	v_mov_b32_e32 v184, 0x43e00000
	s_mov_b32 s60, s33
	s_mov_b32 s59, s22
	s_mov_b64 s[10:11], s[8:9]
	s_branch .LBB0_417
.LBB0_414:
	ds_read2_b32 v[158:159], v186 offset0:56 offset1:65
	ds_read2_b32 v[160:161], v186 offset0:121 offset1:130
	ds_read2_b32 v[172:173], v186 offset0:186 offset1:195
	ds_read2_b32 v[174:175], v187 offset0:123 offset1:132
	ds_read2_b32 v[176:177], v185 offset0:60 offset1:69
	ds_read2_b32 v[178:179], v185 offset0:125 offset1:134
	ds_read2_b32 v[188:189], v185 offset0:190 offset1:199
	v_mov_b64_e32 v[190:191], s[10:11]
	ds_read2_b32 v[198:199], v186 offset0:8 offset1:16
	ds_read2_b32 v[200:201], v186 offset0:73 offset1:81
	ds_read2_b32 v[206:207], v186 offset0:138 offset1:146
	ds_read2_b32 v[208:209], v186 offset0:203 offset1:211
	ds_read2_b32 v[210:211], v185 offset0:12 offset1:20
	ds_read2_b32 v[212:213], v185 offset0:77 offset1:85
	ds_read2_b32 v[214:215], v185 offset0:142 offset1:150
	ds_read2_b32 v[216:217], v185 offset0:207 offset1:215
	v_mad_u64_u32 v[192:193], s[12:13], s59, v134, v[190:191]
	v_lshl_add_u64 v[192:193], v[192:193], 0, v[152:153]
	s_waitcnt lgkmcnt(14)
	v_cvt_pk_bf16_f32 v154, v132, v159
	s_waitcnt lgkmcnt(12)
	v_cvt_pk_bf16_f32 v155, v161, v173
	s_waitcnt lgkmcnt(10)
	v_cvt_pk_bf16_f32 v156, v175, v177
	s_waitcnt lgkmcnt(8)
	v_cvt_pk_bf16_f32 v157, v179, v189
	global_store_dwordx4 v[192:193], v[154:157], off nt
	v_mad_u64_u32 v[192:193], s[12:13], s59, v138, v[190:191]
	v_lshl_add_u64 v[192:193], v[192:193], 0, v[152:153]
	s_waitcnt lgkmcnt(6)
	v_cvt_pk_bf16_f32 v154, v198, v200
	s_waitcnt lgkmcnt(4)
	v_cvt_pk_bf16_f32 v155, v206, v208
	s_waitcnt lgkmcnt(2)
	v_cvt_pk_bf16_f32 v156, v210, v212
	s_waitcnt lgkmcnt(0)
	v_cvt_pk_bf16_f32 v157, v214, v216
	global_store_dwordx4 v[192:193], v[154:157], off nt
	v_mad_u64_u32 v[192:193], s[12:13], s59, v140, v[190:191]
	s_nop 0
	v_cvt_pk_bf16_f32 v154, v199, v201
	v_cvt_pk_bf16_f32 v155, v207, v209
	v_cvt_pk_bf16_f32 v156, v211, v213
	v_cvt_pk_bf16_f32 v157, v215, v217
	ds_read2_b32 v[198:199], v186 offset0:24 offset1:32
	ds_read2_b32 v[200:201], v186 offset0:89 offset1:97
	ds_read2_b32 v[206:207], v186 offset0:154 offset1:162
	ds_read2_b32 v[208:209], v186 offset0:219 offset1:227
	ds_read2_b32 v[210:211], v185 offset0:28 offset1:36
	ds_read2_b32 v[212:213], v185 offset0:93 offset1:101
	ds_read2_b32 v[214:215], v185 offset0:158 offset1:166
	ds_read2_b32 v[216:217], v185 offset0:223 offset1:231
	v_lshl_add_u64 v[192:193], v[192:193], 0, v[152:153]
	global_store_dwordx4 v[192:193], v[154:157], off nt
	v_mad_u64_u32 v[192:193], s[12:13], s59, v142, v[190:191]
	v_lshl_add_u64 v[192:193], v[192:193], 0, v[152:153]
	s_waitcnt lgkmcnt(6)
	v_cvt_pk_bf16_f32 v154, v198, v200
	s_waitcnt lgkmcnt(4)
	v_cvt_pk_bf16_f32 v155, v206, v208
	s_waitcnt lgkmcnt(2)
	v_cvt_pk_bf16_f32 v156, v210, v212
	s_waitcnt lgkmcnt(0)
	v_cvt_pk_bf16_f32 v157, v214, v216
	global_store_dwordx4 v[192:193], v[154:157], off nt
	v_mad_u64_u32 v[192:193], s[12:13], s59, v144, v[190:191]
	s_nop 0
	v_cvt_pk_bf16_f32 v154, v199, v201
	v_cvt_pk_bf16_f32 v155, v207, v209
	v_cvt_pk_bf16_f32 v156, v211, v213
	v_cvt_pk_bf16_f32 v157, v215, v217
	ds_read2_b32 v[198:199], v186 offset0:40 offset1:48
	ds_read2_b32 v[200:201], v186 offset0:105 offset1:113
	ds_read2_b32 v[206:207], v186 offset0:170 offset1:178
	ds_read2_b32 v[186:187], v186 offset0:235 offset1:243
	ds_read2_b32 v[208:209], v185 offset0:44 offset1:52
	ds_read2_b32 v[210:211], v185 offset0:109 offset1:117
	ds_read2_b32 v[212:213], v185 offset0:174 offset1:182
	ds_read2_b32 v[214:215], v185 offset0:239 offset1:247
	v_lshl_add_u64 v[192:193], v[192:193], 0, v[152:153]
	global_store_dwordx4 v[192:193], v[154:157], off nt
	v_mad_u64_u32 v[192:193], s[12:13], s59, v146, v[190:191]
	s_waitcnt lgkmcnt(4)
	v_cvt_pk_bf16_f32 v155, v206, v186
	v_lshl_add_u64 v[192:193], v[192:193], 0, v[152:153]
	v_cvt_pk_bf16_f32 v154, v198, v200
	s_waitcnt lgkmcnt(2)
	v_cvt_pk_bf16_f32 v156, v208, v210
	s_waitcnt lgkmcnt(0)
	v_cvt_pk_bf16_f32 v157, v212, v214
	global_store_dwordx4 v[192:193], v[154:157], off nt
	ds_read_b32 v132, v182 offset:18428
	s_nop 0
	v_cvt_pk_bf16_f32 v155, v207, v187
	v_mad_u64_u32 v[186:187], s[12:13], s59, v148, v[190:191]
	v_cvt_pk_bf16_f32 v154, v199, v201
	v_lshl_add_u64 v[186:187], v[186:187], 0, v[152:153]
	v_cvt_pk_bf16_f32 v156, v209, v211
	v_cvt_pk_bf16_f32 v157, v213, v215
	global_store_dwordx4 v[186:187], v[154:157], off nt
	s_nop 1
	v_cvt_pk_bf16_f32 v154, v158, v160
	v_mad_u64_u32 v[158:159], s[12:13], s59, v150, v[190:191]
	v_lshl_add_u64 v[158:159], v[158:159], 0, v[152:153]
	v_cvt_pk_bf16_f32 v155, v172, v174
	v_cvt_pk_bf16_f32 v156, v176, v178
	s_waitcnt lgkmcnt(0)
	v_cvt_pk_bf16_f32 v157, v188, v132
	global_store_dwordx4 v[158:159], v[154:157], off nt

.LBB0_445:
	v_mul_u32_u24_e32 v58, s16, v131
	v_mul_u32_u24_e32 v60, s16, v135
	v_mul_u32_u24_e32 v66, s16, v139
	v_mul_u32_u24_e32 v68, s16, v141
	v_mul_u32_u24_e32 v82, s16, v143
	v_mul_u32_u24_e32 v84, s16, v145
	v_mul_u32_u24_e32 v90, s16, v147
	v_mul_u32_u24_e32 v92, s16, v149
	v_mul_u32_u24_e32 v98, s16, v151
	v_mul_u32_u24_e32 v100, s16, v163
	v_mul_u32_u24_e32 v106, s16, v165
	v_mul_u32_u24_e32 v108, s16, v167
	v_mul_u32_u24_e32 v114, s16, v169
	v_mul_u32_u24_e32 v116, s16, v171
	v_mul_u32_u24_e32 v122, s16, v180
	v_mul_u32_u24_e32 v124, s16, v181
	s_waitcnt lgkmcnt(0)
	v_lshlrev_b32_e32 v132, 2, v58
	v_lshlrev_b32_e32 v60, 2, v60
	v_mov_b32_e32 v61, v133
	v_lshlrev_b32_e32 v66, 2, v66
	v_mov_b32_e32 v67, v133
	v_lshlrev_b32_e32 v68, 2, v68
	v_mov_b32_e32 v69, v133
	v_lshlrev_b32_e32 v82, 2, v82
	v_mov_b32_e32 v83, v133
	v_lshlrev_b32_e32 v84, 2, v84
	v_mov_b32_e32 v85, v133
	v_lshlrev_b32_e32 v90, 2, v90
	v_mov_b32_e32 v91, v133
	v_lshlrev_b32_e32 v92, 2, v92
	v_mov_b32_e32 v93, v133
	v_lshlrev_b32_e32 v98, 2, v98
	v_mov_b32_e32 v99, v133
	v_lshlrev_b32_e32 v100, 2, v100
	v_mov_b32_e32 v101, v133
	v_lshlrev_b32_e32 v106, 2, v106
	v_mov_b32_e32 v107, v133
	v_lshlrev_b32_e32 v108, 2, v108
	v_mov_b32_e32 v109, v133
	v_lshlrev_b32_e32 v114, 2, v114
	v_mov_b32_e32 v115, v133
	v_lshlrev_b32_e32 v116, 2, v116
	v_mov_b32_e32 v117, v133
	v_lshlrev_b32_e32 v122, 2, v122
	v_mov_b32_e32 v123, v133
	v_lshlrev_b32_e32 v124, 2, v124
	v_mov_b32_e32 v125, v133
	v_lshl_add_u64 v[58:59], s[14:15], 0, v[132:133]
	v_lshlrev_b32_e32 v132, 2, v130
	v_lshl_add_u64 v[60:61], s[14:15], 0, v[60:61]
	v_lshl_add_u64 v[66:67], s[14:15], 0, v[66:67]
	v_lshl_add_u64 v[68:69], s[14:15], 0, v[68:69]
	v_lshl_add_u64 v[82:83], s[14:15], 0, v[82:83]
	v_lshl_add_u64 v[84:85], s[14:15], 0, v[84:85]
	v_lshl_add_u64 v[90:91], s[14:15], 0, v[90:91]
	v_lshl_add_u64 v[92:93], s[14:15], 0, v[92:93]
	v_lshl_add_u64 v[98:99], s[14:15], 0, v[98:99]
	v_lshl_add_u64 v[100:101], s[14:15], 0, v[100:101]
	v_lshl_add_u64 v[106:107], s[14:15], 0, v[106:107]
	v_lshl_add_u64 v[108:109], s[14:15], 0, v[108:109]
	v_lshl_add_u64 v[114:115], s[14:15], 0, v[114:115]
	v_lshl_add_u64 v[116:117], s[14:15], 0, v[116:117]
	v_lshl_add_u64 v[122:123], s[14:15], 0, v[122:123]
	v_lshl_add_u64 v[124:125], s[14:15], 0, v[124:125]
	v_lshl_add_u64 v[58:59], v[58:59], 0, v[132:133]
	v_lshl_add_u64 v[60:61], v[60:61], 0, v[132:133]
	v_lshl_add_u64 v[66:67], v[66:67], 0, v[132:133]
	v_lshl_add_u64 v[68:69], v[68:69], 0, v[132:133]
	v_lshl_add_u64 v[82:83], v[82:83], 0, v[132:133]
	v_lshl_add_u64 v[84:85], v[84:85], 0, v[132:133]
	v_lshl_add_u64 v[90:91], v[90:91], 0, v[132:133]
	v_lshl_add_u64 v[92:93], v[92:93], 0, v[132:133]
	v_lshl_add_u64 v[98:99], v[98:99], 0, v[132:133]
	v_lshl_add_u64 v[100:101], v[100:101], 0, v[132:133]
	v_lshl_add_u64 v[106:107], v[106:107], 0, v[132:133]
	v_lshl_add_u64 v[108:109], v[108:109], 0, v[132:133]
	v_lshl_add_u64 v[114:115], v[114:115], 0, v[132:133]
	v_lshl_add_u64 v[116:117], v[116:117], 0, v[132:133]
	v_lshl_add_u64 v[122:123], v[122:123], 0, v[132:133]
	v_lshl_add_u64 v[124:125], v[124:125], 0, v[132:133]
	global_load_dwordx4 v[62:65], v[58:59], off nt
	s_nop 0
	global_load_dwordx4 v[58:61], v[60:61], off nt
	s_nop 0
	global_load_dwordx4 v[70:73], v[66:67], off nt
	s_nop 0
	global_load_dwordx4 v[66:69], v[68:69], off nt
	s_nop 0
	global_load_dwordx4 v[86:89], v[82:83], off nt
	s_nop 0
	global_load_dwordx4 v[82:85], v[84:85], off nt
	s_nop 0
	global_load_dwordx4 v[94:97], v[90:91], off nt
	s_nop 0
	global_load_dwordx4 v[90:93], v[92:93], off nt
	s_nop 0
	global_load_dwordx4 v[102:105], v[98:99], off nt
	s_nop 0
	global_load_dwordx4 v[98:101], v[100:101], off nt
	s_nop 0
	global_load_dwordx4 v[110:113], v[106:107], off nt
	s_nop 0
	global_load_dwordx4 v[106:109], v[108:109], off nt
	s_nop 0
	global_load_dwordx4 v[118:121], v[114:115], off nt
	s_nop 0
	global_load_dwordx4 v[114:117], v[116:117], off nt
	s_nop 0
	global_load_dwordx4 v[126:129], v[122:123], off nt
	s_nop 0
	global_load_dwordx4 v[122:125], v[124:125], off nt
.LBB0_446:
	v_add_u32_e32 v188, 0x4000, v183
	v_add_u32_e32 v189, 0x4008, v183
	v_add_u32_e32 v190, 0x4410, v183
	v_add_u32_e32 v191, 0x4418, v183
	v_add_u32_e32 v192, 0x4820, v183
	v_add_u32_e32 v193, 0x4828, v183
	v_add_u32_e32 v198, 0x4c30, v183
	v_add_u32_e32 v199, 0x4c38, v183
	v_add_u32_e32 v200, 0x5040, v183
	v_add_u32_e32 v201, 0x5048, v183
	v_add_u32_e32 v205, 0x5450, v183
	v_add_u32_e32 v206, 0x5458, v183
	v_add_u32_e32 v207, 0x5860, v183
	v_add_u32_e32 v208, 0x5868, v183
	v_add_u32_e32 v209, 0x5c70, v183
	v_add_u32_e32 v210, 0x5c78, v183
	v_add_u32_e32 v211, 0x6080, v183
	v_add_u32_e32 v212, 0x6088, v183
	v_add_u32_e32 v213, 0x6490, v183
	v_add_u32_e32 v214, 0x6498, v183
	v_add_u32_e32 v215, 0x68a0, v183
	v_add_u32_e32 v216, 0x68a8, v183
	v_add_u32_e32 v217, 0x6cb0, v183
	v_add_u32_e32 v218, 0x6cb8, v183
	v_add_u32_e32 v219, 0x70c0, v183
	v_add_u32_e32 v220, 0x70c8, v183
	v_add_u32_e32 v221, 0x74d0, v183
	v_add_u32_e32 v222, 0x74d8, v183
	v_add_u32_e32 v223, 0x78e0, v183
	v_add_u32_e32 v224, 0x78e8, v183
	v_add_u32_e32 v225, 0x7cf0, v183
	v_add_u32_e32 v226, 0x7cf8, v183
	s_waitcnt vmcnt(15)
	ds_write2_b32 v188, v2, v3 offset1:1
	ds_write2_b32 v189, v4, v5 offset1:1
	s_waitcnt vmcnt(14)
	ds_write2_b32 v190, v6, v7 offset1:1
	ds_write2_b32 v191, v8, v9 offset1:1
	s_waitcnt vmcnt(13)
	ds_write2_b32 v192, v10, v11 offset1:1
	ds_write2_b32 v193, v12, v13 offset1:1
	s_waitcnt vmcnt(12)
	ds_write2_b32 v198, v14, v15 offset1:1
	ds_write2_b32 v199, v16, v17 offset1:1
	s_waitcnt vmcnt(11)
	ds_write2_b32 v200, v18, v19 offset1:1
	ds_write2_b32 v201, v20, v21 offset1:1
	s_waitcnt vmcnt(10)
	ds_write2_b32 v205, v22, v23 offset1:1
	ds_write2_b32 v206, v24, v25 offset1:1
	s_waitcnt vmcnt(9)
	ds_write2_b32 v207, v26, v27 offset1:1
	ds_write2_b32 v208, v28, v29 offset1:1
	s_waitcnt vmcnt(8)
	ds_write2_b32 v209, v30, v31 offset1:1
	ds_write2_b32 v210, v32, v33 offset1:1
	s_waitcnt vmcnt(7)
	ds_write2_b32 v211, v34, v35 offset1:1
	ds_write2_b32 v212, v36, v37 offset1:1
	s_waitcnt vmcnt(6)
	ds_write2_b32 v213, v38, v39 offset1:1
	ds_write2_b32 v214, v40, v41 offset1:1
	s_waitcnt vmcnt(5)
	ds_write2_b32 v215, v42, v43 offset1:1
	ds_write2_b32 v216, v44, v45 offset1:1
	s_waitcnt vmcnt(4)
	ds_write2_b32 v217, v46, v47 offset1:1
	ds_write2_b32 v218, v48, v49 offset1:1
	s_waitcnt vmcnt(3)
	ds_write2_b32 v219, v50, v51 offset1:1
	ds_write2_b32 v220, v52, v53 offset1:1
	s_waitcnt vmcnt(2)
	ds_write2_b32 v221, v54, v55 offset1:1
	ds_write2_b32 v222, v56, v57 offset1:1
	s_waitcnt vmcnt(1)
	ds_write2_b32 v223, v74, v75 offset1:1
	ds_write2_b32 v224, v76, v77 offset1:1
	s_waitcnt vmcnt(0)
	ds_write2_b32 v225, v78, v79 offset1:1
	ds_write2_b32 v226, v80, v81 offset1:1
	s_waitcnt lgkmcnt(0)
	ds_read_b32 v132, v182 offset:16384
	v_cmp_eq_f32_e64 s[14:15], s33, 0
	s_and_b64 vcc, exec, s[14:15]
	v_add_u32_e32 v186, 0x4000, v182
	v_add_u32_e32 v187, 0x4200, v182
	v_add_u32_e32 v185, 0x4400, v182
	s_cbranch_vccnz .LBB0_467
	ds_read2_b32 v[154:155], v186 offset0:56 offset1:65
	ds_read2_b32 v[156:157], v186 offset0:121 offset1:130
	ds_read2_b32 v[158:159], v186 offset0:186 offset1:195
	s_waitcnt lgkmcnt(3)
	v_mul_f32_e32 v160, s33, v132
	v_med3_f32 v160, v160, s56, v184
	s_waitcnt lgkmcnt(2)
	v_mul_f32_e32 v155, s33, v155
	v_med3_f32 v155, v155, s56, v184
	v_mov_b32_e32 v228, v133
	v_cvt_pk_fp8_f32 v228, v160, v155
	ds_read2_b32 v[174:175], v187 offset0:123 offset1:132
	ds_read2_b32 v[160:161], v185 offset0:60 offset1:69
	ds_read2_b32 v[172:173], v185 offset0:125 offset1:134
	s_waitcnt lgkmcnt(4)
	v_mul_f32_e32 v157, s33, v157
	s_waitcnt lgkmcnt(3)
	v_mul_f32_e32 v159, s33, v159
	v_med3_f32 v157, v157, s56, v184
	v_med3_f32 v155, v159, s56, v184
	ds_read2_b32 v[178:179], v185 offset0:190 offset1:199
	v_cvt_pk_fp8_f32 v228, v157, v155 op_sel:[0,0,1]
	s_waitcnt lgkmcnt(3)
	v_mul_f32_e32 v155, s33, v175
	s_waitcnt lgkmcnt(2)
	v_mul_f32_e32 v157, s33, v161
	v_med3_f32 v155, v155, s56, v184
	v_med3_f32 v157, v157, s56, v184
	v_mov_b32_e32 v229, v133
	v_cvt_pk_fp8_f32 v229, v155, v157
	s_waitcnt lgkmcnt(1)
	v_mul_f32_e32 v159, s33, v173
	s_waitcnt lgkmcnt(0)
	v_mul_f32_e32 v155, s33, v179
	v_med3_f32 v157, v159, s56, v184
	v_med3_f32 v155, v155, s56, v184
	v_cvt_pk_fp8_f32 v229, v157, v155 op_sel:[0,0,1]
	ds_read2_b32 v[232:233], v186 offset0:8 offset1:16
	ds_read2_b32 v[234:235], v186 offset0:73 offset1:81
	ds_read2_b32 v[236:237], v186 offset0:138 offset1:146
	ds_read2_b32 v[238:239], v186 offset0:203 offset1:211
	v_mov_b64_e32 v[176:177], s[8:9]
	v_mad_u64_u32 v[230:231], s[14:15], s22, v134, v[176:177]
	v_lshl_add_u64 v[230:231], v[230:231], 0, v[136:137]
	s_waitcnt lgkmcnt(3)
	v_mul_f32_e32 v155, s33, v232
	s_waitcnt lgkmcnt(2)
	v_mul_f32_e32 v157, s33, v234
	global_store_dwordx2 v[230:231], v[228:229], off nt
	v_med3_f32 v155, v155, s56, v184
	v_med3_f32 v157, v157, s56, v184
	v_mov_b32_e32 v228, v133
	v_cvt_pk_fp8_f32 v228, v155, v157
	ds_read2_b32 v[230:231], v185 offset0:12 offset1:20
	ds_read2_b32 v[240:241], v185 offset0:77 offset1:85
	ds_read2_b32 v[242:243], v185 offset0:142 offset1:150
	s_waitcnt lgkmcnt(4)
	v_mul_f32_e32 v159, s33, v236
	s_waitcnt lgkmcnt(3)
	v_mul_f32_e32 v161, s33, v238
	v_med3_f32 v159, v159, s56, v184
	v_med3_f32 v155, v161, s56, v184
	ds_read2_b32 v[244:245], v185 offset0:207 offset1:215
	v_cvt_pk_fp8_f32 v228, v159, v155 op_sel:[0,0,1]
	s_waitcnt lgkmcnt(3)
	v_mul_f32_e32 v155, s33, v230
	s_waitcnt lgkmcnt(2)
	v_mul_f32_e32 v157, s33, v240
	v_med3_f32 v155, v155, s56, v184
	v_med3_f32 v157, v157, s56, v184
	v_mov_b32_e32 v229, v133
	v_cvt_pk_fp8_f32 v229, v155, v157
	s_waitcnt lgkmcnt(1)
	v_mul_f32_e32 v159, s33, v242
	s_waitcnt lgkmcnt(0)
	v_mul_f32_e32 v155, s33, v244
	v_med3_f32 v157, v159, s56, v184
	v_med3_f32 v155, v155, s56, v184
	v_cvt_pk_fp8_f32 v229, v157, v155 op_sel:[0,0,1]
	v_mad_u64_u32 v[246:247], s[14:15], s22, v138, v[176:177]
	v_lshl_add_u64 v[246:247], v[246:247], 0, v[136:137]
	v_mul_f32_e32 v155, s33, v233
	v_mul_f32_e32 v157, s33, v235
	global_store_dwordx2 v[246:247], v[228:229], off nt
	v_med3_f32 v155, v155, s56, v184
	v_med3_f32 v157, v157, s56, v184
	v_mov_b32_e32 v228, v133
	v_cvt_pk_fp8_f32 v228, v155, v157
	v_mul_f32_e32 v159, s33, v237
	v_mul_f32_e32 v155, s33, v239
	v_med3_f32 v157, v159, s56, v184
	v_med3_f32 v155, v155, s56, v184
	v_cvt_pk_fp8_f32 v228, v157, v155 op_sel:[0,0,1]
	v_mul_f32_e32 v155, s33, v231
	v_mul_f32_e32 v157, s33, v241
	v_med3_f32 v155, v155, s56, v184
	v_med3_f32 v157, v157, s56, v184
	v_mov_b32_e32 v229, v133
	v_cvt_pk_fp8_f32 v229, v155, v157
	v_mul_f32_e32 v159, s33, v243
	v_mul_f32_e32 v155, s33, v245
	v_med3_f32 v157, v159, s56, v184
	v_med3_f32 v155, v155, s56, v184
	v_cvt_pk_fp8_f32 v229, v157, v155 op_sel:[0,0,1]
	ds_read2_b32 v[232:233], v186 offset0:24 offset1:32
	ds_read2_b32 v[234:235], v186 offset0:89 offset1:97
	ds_read2_b32 v[236:237], v186 offset0:154 offset1:162
	ds_read2_b32 v[238:239], v186 offset0:219 offset1:227
	v_mad_u64_u32 v[230:231], s[14:15], s22, v140, v[176:177]
	v_lshl_add_u64 v[230:231], v[230:231], 0, v[136:137]
	s_waitcnt lgkmcnt(3)
	v_mul_f32_e32 v155, s33, v232
	s_waitcnt lgkmcnt(2)
	v_mul_f32_e32 v157, s33, v234
	global_store_dwordx2 v[230:231], v[228:229], off nt
	v_med3_f32 v155, v155, s56, v184
	v_med3_f32 v157, v157, s56, v184
	v_mov_b32_e32 v228, v133
	v_cvt_pk_fp8_f32 v228, v155, v157
	ds_read2_b32 v[230:231], v185 offset0:28 offset1:36
	ds_read2_b32 v[240:241], v185 offset0:93 offset1:101
	ds_read2_b32 v[242:243], v185 offset0:158 offset1:166
	s_waitcnt lgkmcnt(4)
	v_mul_f32_e32 v159, s33, v236
	s_waitcnt lgkmcnt(3)
	v_mul_f32_e32 v161, s33, v238
	v_med3_f32 v159, v159, s56, v184
	v_med3_f32 v155, v161, s56, v184
	ds_read2_b32 v[244:245], v185 offset0:223 offset1:231
	v_cvt_pk_fp8_f32 v228, v159, v155 op_sel:[0,0,1]
	s_waitcnt lgkmcnt(3)
	v_mul_f32_e32 v155, s33, v230
	s_waitcnt lgkmcnt(2)
	v_mul_f32_e32 v157, s33, v240
	v_med3_f32 v155, v155, s56, v184
	v_med3_f32 v157, v157, s56, v184
	v_mov_b32_e32 v229, v133
	v_cvt_pk_fp8_f32 v229, v155, v157
	s_waitcnt lgkmcnt(1)
	v_mul_f32_e32 v159, s33, v242
	s_waitcnt lgkmcnt(0)
	v_mul_f32_e32 v155, s33, v244
	v_med3_f32 v157, v159, s56, v184
	v_med3_f32 v155, v155, s56, v184
	v_cvt_pk_fp8_f32 v229, v157, v155 op_sel:[0,0,1]
	v_mad_u64_u32 v[246:247], s[14:15], s22, v142, v[176:177]
	v_lshl_add_u64 v[246:247], v[246:247], 0, v[136:137]
	v_mul_f32_e32 v155, s33, v233
	v_mul_f32_e32 v157, s33, v235
	global_store_dwordx2 v[246:247], v[228:229], off nt
	v_med3_f32 v155, v155, s56, v184
	v_med3_f32 v157, v157, s56, v184
	v_mov_b32_e32 v228, v133
	v_cvt_pk_fp8_f32 v228, v155, v157
	v_mul_f32_e32 v159, s33, v237
	v_mul_f32_e32 v155, s33, v239
	v_med3_f32 v157, v159, s56, v184
	v_med3_f32 v155, v155, s56, v184
	v_cvt_pk_fp8_f32 v228, v157, v155 op_sel:[0,0,1]
	v_mul_f32_e32 v155, s33, v231
	v_mul_f32_e32 v157, s33, v241
	v_med3_f32 v155, v155, s56, v184
	v_med3_f32 v157, v157, s56, v184
	v_mov_b32_e32 v229, v133
	v_cvt_pk_fp8_f32 v229, v155, v157
	v_mul_f32_e32 v159, s33, v243
	v_mul_f32_e32 v155, s33, v245
	v_med3_f32 v157, v159, s56, v184
	v_med3_f32 v155, v155, s56, v184
	v_cvt_pk_fp8_f32 v229, v157, v155 op_sel:[0,0,1]
	ds_read2_b32 v[232:233], v186 offset0:40 offset1:48
	ds_read2_b32 v[234:235], v186 offset0:105 offset1:113
	ds_read2_b32 v[236:237], v186 offset0:170 offset1:178
	ds_read2_b32 v[238:239], v186 offset0:235 offset1:243
	v_mad_u64_u32 v[230:231], s[14:15], s22, v144, v[176:177]
	v_lshl_add_u64 v[230:231], v[230:231], 0, v[136:137]
	s_waitcnt lgkmcnt(3)
	v_mul_f32_e32 v155, s33, v232
	s_waitcnt lgkmcnt(2)
	v_mul_f32_e32 v157, s33, v234
	global_store_dwordx2 v[230:231], v[228:229], off nt
	v_med3_f32 v155, v155, s56, v184
	v_med3_f32 v157, v157, s56, v184
	v_mov_b32_e32 v228, v133
	v_cvt_pk_fp8_f32 v228, v155, v157
	ds_read2_b32 v[230:231], v185 offset0:44 offset1:52
	ds_read2_b32 v[240:241], v185 offset0:109 offset1:117
	ds_read2_b32 v[242:243], v185 offset0:174 offset1:182
	s_waitcnt lgkmcnt(4)
	v_mul_f32_e32 v159, s33, v236
	s_waitcnt lgkmcnt(3)
	v_mul_f32_e32 v161, s33, v238
	v_med3_f32 v159, v159, s56, v184
	v_med3_f32 v155, v161, s56, v184
	ds_read2_b32 v[244:245], v185 offset0:239 offset1:247
	v_cvt_pk_fp8_f32 v228, v159, v155 op_sel:[0,0,1]
	s_waitcnt lgkmcnt(3)
	v_mul_f32_e32 v155, s33, v230
	s_waitcnt lgkmcnt(2)
	v_mul_f32_e32 v157, s33, v240
	v_med3_f32 v155, v155, s56, v184
	v_med3_f32 v157, v157, s56, v184
	v_mov_b32_e32 v229, v133
	v_cvt_pk_fp8_f32 v229, v155, v157
	s_waitcnt lgkmcnt(1)
	v_mul_f32_e32 v159, s33, v242
	s_waitcnt lgkmcnt(0)
	v_mul_f32_e32 v155, s33, v244
	v_med3_f32 v157, v159, s56, v184
	v_med3_f32 v155, v155, s56, v184
	v_cvt_pk_fp8_f32 v229, v157, v155 op_sel:[0,0,1]
	v_mad_u64_u32 v[246:247], s[14:15], s22, v146, v[176:177]
	v_lshl_add_u64 v[246:247], v[246:247], 0, v[136:137]
	v_mul_f32_e32 v155, s33, v233
	v_mul_f32_e32 v157, s33, v235
	global_store_dwordx2 v[246:247], v[228:229], off nt
	v_med3_f32 v155, v155, s56, v184
	v_med3_f32 v157, v157, s56, v184
	v_mov_b32_e32 v228, v133
	v_cvt_pk_fp8_f32 v228, v155, v157
	v_mul_f32_e32 v159, s33, v237
	v_mul_f32_e32 v155, s33, v239
	v_med3_f32 v157, v159, s56, v184
	v_med3_f32 v155, v155, s56, v184
	v_cvt_pk_fp8_f32 v228, v157, v155 op_sel:[0,0,1]
	v_mul_f32_e32 v155, s33, v231
	v_mul_f32_e32 v157, s33, v241
	v_med3_f32 v155, v155, s56, v184
	v_med3_f32 v157, v157, s56, v184
	v_mov_b32_e32 v229, v133
	v_cvt_pk_fp8_f32 v229, v155, v157
	v_mul_f32_e32 v159, s33, v243
	v_mul_f32_e32 v155, s33, v245
	v_med3_f32 v157, v159, s56, v184
	v_med3_f32 v155, v155, s56, v184
	v_cvt_pk_fp8_f32 v229, v157, v155 op_sel:[0,0,1]
	v_mul_f32_e32 v154, s33, v154
	v_mul_f32_e32 v155, s33, v156
	v_med3_f32 v157, v154, s56, v184
	v_med3_f32 v155, v155, s56, v184
	v_mov_b32_e32 v154, v133
	v_cvt_pk_fp8_f32 v154, v157, v155
	v_mul_f32_e32 v156, s33, v158
	v_mul_f32_e32 v155, s33, v174
	v_med3_f32 v156, v156, s56, v184
	v_med3_f32 v155, v155, s56, v184
	ds_read_b32 v158, v182 offset:18428
	v_cvt_pk_fp8_f32 v154, v156, v155 op_sel:[0,0,1]
	v_mul_f32_e32 v155, s33, v160
	v_mul_f32_e32 v156, s33, v172
	v_med3_f32 v159, v155, s56, v184
	v_med3_f32 v156, v156, s56, v184
	v_mov_b32_e32 v155, v133
	v_cvt_pk_fp8_f32 v155, v159, v156
	v_mul_f32_e32 v157, s33, v178
	s_waitcnt lgkmcnt(0)
	v_mul_f32_e32 v156, s33, v158
	v_med3_f32 v157, v157, s56, v184
	v_med3_f32 v156, v156, s56, v184
	v_cvt_pk_fp8_f32 v155, v157, v156 op_sel:[0,0,1]
	v_mad_u64_u32 v[230:231], s[14:15], s22, v148, v[176:177]
	v_mad_u64_u32 v[156:157], s[14:15], s22, v150, v[176:177]
	v_lshl_add_u64 v[230:231], v[230:231], 0, v[136:137]
	v_lshl_add_u64 v[156:157], v[156:157], 0, v[136:137]
	global_store_dwordx2 v[230:231], v[228:229], off nt
	global_store_dwordx2 v[156:157], v[154:155], off nt
	s_cbranch_execnz .LBB0_449
.LBB0_448:
	ds_read2_b32 v[158:159], v186 offset0:56 offset1:65
	ds_read2_b32 v[160:161], v186 offset0:121 offset1:130
	ds_read2_b32 v[172:173], v186 offset0:186 offset1:195
	ds_read2_b32 v[174:175], v187 offset0:123 offset1:132
	ds_read2_b32 v[176:177], v185 offset0:60 offset1:69
	ds_read2_b32 v[178:179], v185 offset0:125 offset1:134
	ds_read2_b32 v[228:229], v185 offset0:190 offset1:199
	v_mov_b64_e32 v[230:231], s[8:9]
	ds_read2_b32 v[234:235], v186 offset0:8 offset1:16
	ds_read2_b32 v[236:237], v186 offset0:73 offset1:81
	ds_read2_b32 v[238:239], v186 offset0:138 offset1:146
	ds_read2_b32 v[240:241], v186 offset0:203 offset1:211
	ds_read2_b32 v[242:243], v185 offset0:12 offset1:20
	ds_read2_b32 v[244:245], v185 offset0:77 offset1:85
	ds_read2_b32 v[246:247], v185 offset0:142 offset1:150
	ds_read2_b32 v[248:249], v185 offset0:207 offset1:215
	v_mad_u64_u32 v[232:233], s[14:15], s22, v134, v[230:231]
	v_lshl_add_u64 v[232:233], v[232:233], 0, v[152:153]
	s_waitcnt lgkmcnt(14)
	v_cvt_pk_bf16_f32 v154, v132, v159
	s_waitcnt lgkmcnt(12)
	v_cvt_pk_bf16_f32 v155, v161, v173
	s_waitcnt lgkmcnt(10)
	v_cvt_pk_bf16_f32 v156, v175, v177
	s_waitcnt lgkmcnt(8)
	v_cvt_pk_bf16_f32 v157, v179, v229
	global_store_dwordx4 v[232:233], v[154:157], off nt
	v_mad_u64_u32 v[232:233], s[14:15], s22, v138, v[230:231]
	v_lshl_add_u64 v[232:233], v[232:233], 0, v[152:153]
	s_waitcnt lgkmcnt(6)
	v_cvt_pk_bf16_f32 v154, v234, v236
	s_waitcnt lgkmcnt(4)
	v_cvt_pk_bf16_f32 v155, v238, v240
	s_waitcnt lgkmcnt(2)
	v_cvt_pk_bf16_f32 v156, v242, v244
	s_waitcnt lgkmcnt(0)
	v_cvt_pk_bf16_f32 v157, v246, v248
	global_store_dwordx4 v[232:233], v[154:157], off nt
	v_mad_u64_u32 v[232:233], s[14:15], s22, v140, v[230:231]
	s_nop 0
	v_cvt_pk_bf16_f32 v154, v235, v237
	v_cvt_pk_bf16_f32 v155, v239, v241
	v_cvt_pk_bf16_f32 v156, v243, v245
	v_cvt_pk_bf16_f32 v157, v247, v249
	ds_read2_b32 v[234:235], v186 offset0:24 offset1:32
	ds_read2_b32 v[236:237], v186 offset0:89 offset1:97
	ds_read2_b32 v[238:239], v186 offset0:154 offset1:162
	ds_read2_b32 v[240:241], v186 offset0:219 offset1:227
	ds_read2_b32 v[242:243], v185 offset0:28 offset1:36
	ds_read2_b32 v[244:245], v185 offset0:93 offset1:101
	ds_read2_b32 v[246:247], v185 offset0:158 offset1:166
	ds_read2_b32 v[248:249], v185 offset0:223 offset1:231
	v_lshl_add_u64 v[232:233], v[232:233], 0, v[152:153]
	global_store_dwordx4 v[232:233], v[154:157], off nt
	v_mad_u64_u32 v[232:233], s[14:15], s22, v142, v[230:231]
	v_lshl_add_u64 v[232:233], v[232:233], 0, v[152:153]
	s_waitcnt lgkmcnt(6)
	v_cvt_pk_bf16_f32 v154, v234, v236
	s_waitcnt lgkmcnt(4)
	v_cvt_pk_bf16_f32 v155, v238, v240
	s_waitcnt lgkmcnt(2)
	v_cvt_pk_bf16_f32 v156, v242, v244
	s_waitcnt lgkmcnt(0)
	v_cvt_pk_bf16_f32 v157, v246, v248
	global_store_dwordx4 v[232:233], v[154:157], off nt
	v_mad_u64_u32 v[232:233], s[14:15], s22, v144, v[230:231]
	s_nop 0
	v_cvt_pk_bf16_f32 v154, v235, v237
	v_cvt_pk_bf16_f32 v155, v239, v241
	v_cvt_pk_bf16_f32 v156, v243, v245
	v_cvt_pk_bf16_f32 v157, v247, v249
	ds_read2_b32 v[234:235], v186 offset0:40 offset1:48
	ds_read2_b32 v[236:237], v186 offset0:105 offset1:113
	ds_read2_b32 v[238:239], v186 offset0:170 offset1:178
	ds_read2_b32 v[240:241], v186 offset0:235 offset1:243
	ds_read2_b32 v[242:243], v185 offset0:44 offset1:52
	ds_read2_b32 v[244:245], v185 offset0:109 offset1:117
	ds_read2_b32 v[246:247], v185 offset0:174 offset1:182
	ds_read2_b32 v[248:249], v185 offset0:239 offset1:247
	v_lshl_add_u64 v[232:233], v[232:233], 0, v[152:153]
	global_store_dwordx4 v[232:233], v[154:157], off nt
	v_mad_u64_u32 v[232:233], s[14:15], s22, v146, v[230:231]
	v_lshl_add_u64 v[232:233], v[232:233], 0, v[152:153]
	s_waitcnt lgkmcnt(6)
	v_cvt_pk_bf16_f32 v154, v234, v236
	s_waitcnt lgkmcnt(4)
	v_cvt_pk_bf16_f32 v155, v238, v240
	s_waitcnt lgkmcnt(2)
	v_cvt_pk_bf16_f32 v156, v242, v244
	s_waitcnt lgkmcnt(0)
	v_cvt_pk_bf16_f32 v157, v246, v248
	global_store_dwordx4 v[232:233], v[154:157], off nt
	v_mad_u64_u32 v[232:233], s[14:15], s22, v148, v[230:231]
	s_nop 0
	v_cvt_pk_bf16_f32 v154, v235, v237
	v_lshl_add_u64 v[232:233], v[232:233], 0, v[152:153]
	v_cvt_pk_bf16_f32 v155, v239, v241
	v_cvt_pk_bf16_f32 v156, v243, v245
	v_cvt_pk_bf16_f32 v157, v247, v249
	global_store_dwordx4 v[232:233], v[154:157], off nt
	ds_read_b32 v132, v182 offset:18428
	s_nop 0
	v_cvt_pk_bf16_f32 v154, v158, v160
	v_mad_u64_u32 v[158:159], s[14:15], s22, v150, v[230:231]
	v_lshl_add_u64 v[158:159], v[158:159], 0, v[152:153]
	v_cvt_pk_bf16_f32 v155, v172, v174
	v_cvt_pk_bf16_f32 v156, v176, v178
	s_waitcnt lgkmcnt(0)
	v_cvt_pk_bf16_f32 v157, v228, v132
	global_store_dwordx4 v[158:159], v[154:157], off nt

.LBB0_482:
	v_mul_u32_u24_e32 v2, s14, v131
	v_mul_u32_u24_e32 v4, s14, v135
	v_mul_u32_u24_e32 v10, s14, v139
	v_mul_u32_u24_e32 v12, s14, v141
	v_mul_u32_u24_e32 v18, s14, v143
	v_mul_u32_u24_e32 v20, s14, v145
	v_mul_u32_u24_e32 v26, s14, v147
	v_mul_u32_u24_e32 v28, s14, v149
	v_mul_u32_u24_e32 v34, s14, v151
	v_mul_u32_u24_e32 v36, s14, v163
	v_mul_u32_u24_e32 v42, s14, v165
	v_mul_u32_u24_e32 v44, s14, v167
	v_mul_u32_u24_e32 v50, s14, v169
	v_mul_u32_u24_e32 v52, s14, v171
	v_mul_u32_u24_e32 v74, s14, v180
	v_mul_u32_u24_e32 v76, s14, v181
	s_waitcnt lgkmcnt(0)
	v_lshlrev_b32_e32 v132, 2, v2
	v_lshlrev_b32_e32 v4, 2, v4
	v_mov_b32_e32 v5, v133
	v_lshlrev_b32_e32 v10, 2, v10
	v_mov_b32_e32 v11, v133
	v_lshlrev_b32_e32 v12, 2, v12
	v_mov_b32_e32 v13, v133
	v_lshlrev_b32_e32 v18, 2, v18
	v_mov_b32_e32 v19, v133
	v_lshlrev_b32_e32 v20, 2, v20
	v_mov_b32_e32 v21, v133
	v_lshlrev_b32_e32 v26, 2, v26
	v_mov_b32_e32 v27, v133
	v_lshlrev_b32_e32 v28, 2, v28
	v_mov_b32_e32 v29, v133
	v_lshlrev_b32_e32 v34, 2, v34
	v_mov_b32_e32 v35, v133
	v_lshlrev_b32_e32 v36, 2, v36
	v_mov_b32_e32 v37, v133
	v_lshlrev_b32_e32 v42, 2, v42
	v_mov_b32_e32 v43, v133
	v_lshlrev_b32_e32 v44, 2, v44
	v_mov_b32_e32 v45, v133
	v_lshlrev_b32_e32 v50, 2, v50
	v_mov_b32_e32 v51, v133
	v_lshlrev_b32_e32 v52, 2, v52
	v_mov_b32_e32 v53, v133
	v_lshlrev_b32_e32 v74, 2, v74
	v_mov_b32_e32 v75, v133
	v_lshlrev_b32_e32 v76, 2, v76
	v_mov_b32_e32 v77, v133
	v_lshl_add_u64 v[2:3], s[12:13], 0, v[132:133]
	v_lshlrev_b32_e32 v132, 2, v130
	v_lshl_add_u64 v[4:5], s[12:13], 0, v[4:5]
	v_lshl_add_u64 v[10:11], s[12:13], 0, v[10:11]
	v_lshl_add_u64 v[12:13], s[12:13], 0, v[12:13]
	v_lshl_add_u64 v[18:19], s[12:13], 0, v[18:19]
	v_lshl_add_u64 v[20:21], s[12:13], 0, v[20:21]
	v_lshl_add_u64 v[26:27], s[12:13], 0, v[26:27]
	v_lshl_add_u64 v[28:29], s[12:13], 0, v[28:29]
	v_lshl_add_u64 v[34:35], s[12:13], 0, v[34:35]
	v_lshl_add_u64 v[36:37], s[12:13], 0, v[36:37]
	v_lshl_add_u64 v[42:43], s[12:13], 0, v[42:43]
	v_lshl_add_u64 v[44:45], s[12:13], 0, v[44:45]
	v_lshl_add_u64 v[50:51], s[12:13], 0, v[50:51]
	v_lshl_add_u64 v[52:53], s[12:13], 0, v[52:53]
	v_lshl_add_u64 v[74:75], s[12:13], 0, v[74:75]
	v_lshl_add_u64 v[76:77], s[12:13], 0, v[76:77]
	v_lshl_add_u64 v[2:3], v[2:3], 0, v[132:133]
	v_lshl_add_u64 v[6:7], v[4:5], 0, v[132:133]
	v_lshl_add_u64 v[10:11], v[10:11], 0, v[132:133]
	v_lshl_add_u64 v[14:15], v[12:13], 0, v[132:133]
	v_lshl_add_u64 v[18:19], v[18:19], 0, v[132:133]
	v_lshl_add_u64 v[22:23], v[20:21], 0, v[132:133]
	v_lshl_add_u64 v[26:27], v[26:27], 0, v[132:133]
	v_lshl_add_u64 v[30:31], v[28:29], 0, v[132:133]
	v_lshl_add_u64 v[34:35], v[34:35], 0, v[132:133]
	v_lshl_add_u64 v[38:39], v[36:37], 0, v[132:133]
	v_lshl_add_u64 v[42:43], v[42:43], 0, v[132:133]
	v_lshl_add_u64 v[46:47], v[44:45], 0, v[132:133]
	v_lshl_add_u64 v[50:51], v[50:51], 0, v[132:133]
	v_lshl_add_u64 v[54:55], v[52:53], 0, v[132:133]
	v_lshl_add_u64 v[74:75], v[74:75], 0, v[132:133]
	v_lshl_add_u64 v[78:79], v[76:77], 0, v[132:133]
	global_load_dwordx4 v[2:5], v[2:3], off nt
	s_nop 0
	global_load_dwordx4 v[6:9], v[6:7], off nt
	s_nop 0
	global_load_dwordx4 v[10:13], v[10:11], off nt
	s_nop 0
	global_load_dwordx4 v[14:17], v[14:15], off nt
	s_nop 0
	global_load_dwordx4 v[18:21], v[18:19], off nt
	s_nop 0
	global_load_dwordx4 v[22:25], v[22:23], off nt
	s_nop 0
	global_load_dwordx4 v[26:29], v[26:27], off nt
	s_nop 0
	global_load_dwordx4 v[30:33], v[30:31], off nt
	s_nop 0
	global_load_dwordx4 v[34:37], v[34:35], off nt
	s_nop 0
	global_load_dwordx4 v[38:41], v[38:39], off nt
	s_nop 0
	global_load_dwordx4 v[42:45], v[42:43], off nt
	s_nop 0
	global_load_dwordx4 v[46:49], v[46:47], off nt
	s_nop 0
	global_load_dwordx4 v[50:53], v[50:51], off nt
	s_nop 0
	global_load_dwordx4 v[54:57], v[54:55], off nt
	s_nop 0
	global_load_dwordx4 v[74:77], v[74:75], off nt
	s_nop 0
	global_load_dwordx4 v[78:81], v[78:79], off nt
.LBB0_483:
	ds_write2_b32 v188, v62, v63 offset1:1
	ds_write2_b32 v189, v64, v65 offset1:1
	ds_write2_b32 v190, v58, v59 offset1:1
	ds_write2_b32 v191, v60, v61 offset1:1
	ds_write2_b32 v192, v70, v71 offset1:1
	ds_write2_b32 v193, v72, v73 offset1:1
	ds_write2_b32 v198, v66, v67 offset1:1
	ds_write2_b32 v199, v68, v69 offset1:1
	ds_write2_b32 v200, v86, v87 offset1:1
	ds_write2_b32 v201, v88, v89 offset1:1
	ds_write2_b32 v205, v82, v83 offset1:1
	ds_write2_b32 v206, v84, v85 offset1:1
	ds_write2_b32 v207, v94, v95 offset1:1
	ds_write2_b32 v208, v96, v97 offset1:1
	ds_write2_b32 v209, v90, v91 offset1:1
	ds_write2_b32 v210, v92, v93 offset1:1
	ds_write2_b32 v211, v102, v103 offset1:1
	ds_write2_b32 v212, v104, v105 offset1:1
	ds_write2_b32 v213, v98, v99 offset1:1
	ds_write2_b32 v214, v100, v101 offset1:1
	ds_write2_b32 v215, v110, v111 offset1:1
	ds_write2_b32 v216, v112, v113 offset1:1
	ds_write2_b32 v217, v106, v107 offset1:1
	ds_write2_b32 v218, v108, v109 offset1:1
	ds_write2_b32 v219, v118, v119 offset1:1
	ds_write2_b32 v220, v120, v121 offset1:1
	ds_write2_b32 v221, v114, v115 offset1:1
	ds_write2_b32 v222, v116, v117 offset1:1
	ds_write2_b32 v223, v126, v127 offset1:1
	ds_write2_b32 v224, v128, v129 offset1:1
	ds_write2_b32 v225, v122, v123 offset1:1
	ds_write2_b32 v226, v124, v125 offset1:1
	s_waitcnt lgkmcnt(0)
	s_waitcnt lgkmcnt(14)
	ds_read_b32 v132, v182 offset:16384
	v_cmp_eq_f32_e64 s[12:13], s60, 0
	s_and_b64 vcc, exec, s[12:13]
	s_cbranch_vccnz .LBB0_485
	ds_read2_b32 v[154:155], v186 offset0:56 offset1:65
	ds_read2_b32 v[156:157], v186 offset0:121 offset1:130
	ds_read2_b32 v[158:159], v186 offset0:186 offset1:195
	s_waitcnt lgkmcnt(3)
	v_mul_f32_e32 v160, s60, v132
	v_med3_f32 v160, v160, s56, v184
	s_waitcnt lgkmcnt(2)
	v_mul_f32_e32 v155, s60, v155
	v_med3_f32 v155, v155, s56, v184
	v_mov_b32_e32 v188, v133
	v_cvt_pk_fp8_f32 v188, v160, v155
	ds_read2_b32 v[174:175], v187 offset0:123 offset1:132
	ds_read2_b32 v[160:161], v185 offset0:60 offset1:69
	ds_read2_b32 v[172:173], v185 offset0:125 offset1:134
	s_waitcnt lgkmcnt(4)
	v_mul_f32_e32 v157, s60, v157
	s_waitcnt lgkmcnt(3)
	v_mul_f32_e32 v159, s60, v159
	v_med3_f32 v157, v157, s56, v184
	v_med3_f32 v155, v159, s56, v184
	ds_read2_b32 v[178:179], v185 offset0:190 offset1:199
	v_cvt_pk_fp8_f32 v188, v157, v155 op_sel:[0,0,1]
	s_waitcnt lgkmcnt(3)
	v_mul_f32_e32 v155, s60, v175
	s_waitcnt lgkmcnt(2)
	v_mul_f32_e32 v157, s60, v161
	v_med3_f32 v155, v155, s56, v184
	v_med3_f32 v157, v157, s56, v184
	v_mov_b32_e32 v189, v133
	v_cvt_pk_fp8_f32 v189, v155, v157
	s_waitcnt lgkmcnt(1)
	v_mul_f32_e32 v159, s60, v173
	s_waitcnt lgkmcnt(0)
	v_mul_f32_e32 v155, s60, v179
	v_med3_f32 v157, v159, s56, v184
	v_med3_f32 v155, v155, s56, v184
	v_cvt_pk_fp8_f32 v189, v157, v155 op_sel:[0,0,1]
	ds_read2_b32 v[192:193], v186 offset0:8 offset1:16
	ds_read2_b32 v[198:199], v186 offset0:73 offset1:81
	ds_read2_b32 v[200:201], v186 offset0:138 offset1:146
	ds_read2_b32 v[206:207], v186 offset0:203 offset1:211
	v_mov_b64_e32 v[176:177], s[10:11]
	v_mad_u64_u32 v[190:191], s[12:13], s59, v134, v[176:177]
	v_lshl_add_u64 v[190:191], v[190:191], 0, v[136:137]
	s_waitcnt lgkmcnt(3)
	v_mul_f32_e32 v155, s60, v192
	s_waitcnt lgkmcnt(2)
	v_mul_f32_e32 v157, s60, v198
	global_store_dwordx2 v[190:191], v[188:189], off nt
	v_med3_f32 v155, v155, s56, v184
	v_med3_f32 v157, v157, s56, v184
	v_mov_b32_e32 v188, v133
	v_cvt_pk_fp8_f32 v188, v155, v157
	ds_read2_b32 v[190:191], v185 offset0:12 offset1:20
	ds_read2_b32 v[208:209], v185 offset0:77 offset1:85
	ds_read2_b32 v[210:211], v185 offset0:142 offset1:150
	s_waitcnt lgkmcnt(4)
	v_mul_f32_e32 v159, s60, v200
	s_waitcnt lgkmcnt(3)
	v_mul_f32_e32 v161, s60, v206
	v_med3_f32 v159, v159, s56, v184
	v_med3_f32 v155, v161, s56, v184
	ds_read2_b32 v[212:213], v185 offset0:207 offset1:215
	v_cvt_pk_fp8_f32 v188, v159, v155 op_sel:[0,0,1]
	s_waitcnt lgkmcnt(3)
	v_mul_f32_e32 v155, s60, v190
	s_waitcnt lgkmcnt(2)
	v_mul_f32_e32 v157, s60, v208
	v_med3_f32 v155, v155, s56, v184
	v_med3_f32 v157, v157, s56, v184
	v_mov_b32_e32 v189, v133
	v_cvt_pk_fp8_f32 v189, v155, v157
	s_waitcnt lgkmcnt(1)
	v_mul_f32_e32 v159, s60, v210
	s_waitcnt lgkmcnt(0)
	v_mul_f32_e32 v155, s60, v212
	v_med3_f32 v157, v159, s56, v184
	v_med3_f32 v155, v155, s56, v184
	v_cvt_pk_fp8_f32 v189, v157, v155 op_sel:[0,0,1]
	v_mad_u64_u32 v[214:215], s[12:13], s59, v138, v[176:177]
	v_lshl_add_u64 v[214:215], v[214:215], 0, v[136:137]
	v_mul_f32_e32 v155, s60, v193
	v_mul_f32_e32 v157, s60, v199
	global_store_dwordx2 v[214:215], v[188:189], off nt
	v_med3_f32 v155, v155, s56, v184
	v_med3_f32 v157, v157, s56, v184
	v_mov_b32_e32 v188, v133
	v_cvt_pk_fp8_f32 v188, v155, v157
	v_mul_f32_e32 v159, s60, v201
	v_mul_f32_e32 v155, s60, v207
	v_med3_f32 v157, v159, s56, v184
	v_med3_f32 v155, v155, s56, v184
	v_cvt_pk_fp8_f32 v188, v157, v155 op_sel:[0,0,1]
	v_mul_f32_e32 v155, s60, v191
	v_mul_f32_e32 v157, s60, v209
	v_med3_f32 v155, v155, s56, v184
	v_med3_f32 v157, v157, s56, v184
	v_mov_b32_e32 v189, v133
	v_cvt_pk_fp8_f32 v189, v155, v157
	v_mul_f32_e32 v159, s60, v211
	v_mul_f32_e32 v155, s60, v213
	v_med3_f32 v157, v159, s56, v184
	v_med3_f32 v155, v155, s56, v184
	v_cvt_pk_fp8_f32 v189, v157, v155 op_sel:[0,0,1]
	ds_read2_b32 v[192:193], v186 offset0:24 offset1:32
	ds_read2_b32 v[198:199], v186 offset0:89 offset1:97
	ds_read2_b32 v[200:201], v186 offset0:154 offset1:162
	ds_read2_b32 v[206:207], v186 offset0:219 offset1:227
	v_mad_u64_u32 v[190:191], s[12:13], s59, v140, v[176:177]
	v_lshl_add_u64 v[190:191], v[190:191], 0, v[136:137]
	s_waitcnt lgkmcnt(3)
	v_mul_f32_e32 v155, s60, v192
	s_waitcnt lgkmcnt(2)
	v_mul_f32_e32 v157, s60, v198
	global_store_dwordx2 v[190:191], v[188:189], off nt
	v_med3_f32 v155, v155, s56, v184
	v_med3_f32 v157, v157, s56, v184
	v_mov_b32_e32 v188, v133
	v_cvt_pk_fp8_f32 v188, v155, v157
	ds_read2_b32 v[190:191], v185 offset0:28 offset1:36
	ds_read2_b32 v[208:209], v185 offset0:93 offset1:101
	ds_read2_b32 v[210:211], v185 offset0:158 offset1:166
	s_waitcnt lgkmcnt(4)
	v_mul_f32_e32 v159, s60, v200
	s_waitcnt lgkmcnt(3)
	v_mul_f32_e32 v161, s60, v206
	v_med3_f32 v159, v159, s56, v184
	v_med3_f32 v155, v161, s56, v184
	ds_read2_b32 v[212:213], v185 offset0:223 offset1:231
	v_cvt_pk_fp8_f32 v188, v159, v155 op_sel:[0,0,1]
	s_waitcnt lgkmcnt(3)
	v_mul_f32_e32 v155, s60, v190
	s_waitcnt lgkmcnt(2)
	v_mul_f32_e32 v157, s60, v208
	v_med3_f32 v155, v155, s56, v184
	v_med3_f32 v157, v157, s56, v184
	v_mov_b32_e32 v189, v133
	v_cvt_pk_fp8_f32 v189, v155, v157
	s_waitcnt lgkmcnt(1)
	v_mul_f32_e32 v159, s60, v210
	s_waitcnt lgkmcnt(0)
	v_mul_f32_e32 v155, s60, v212
	v_med3_f32 v157, v159, s56, v184
	v_med3_f32 v155, v155, s56, v184
	v_cvt_pk_fp8_f32 v189, v157, v155 op_sel:[0,0,1]
	v_mad_u64_u32 v[214:215], s[12:13], s59, v142, v[176:177]
	v_lshl_add_u64 v[214:215], v[214:215], 0, v[136:137]
	v_mul_f32_e32 v155, s60, v193
	v_mul_f32_e32 v157, s60, v199
	global_store_dwordx2 v[214:215], v[188:189], off nt
	v_med3_f32 v155, v155, s56, v184
	v_med3_f32 v157, v157, s56, v184
	v_mov_b32_e32 v188, v133
	v_cvt_pk_fp8_f32 v188, v155, v157
	v_mul_f32_e32 v159, s60, v201
	v_mul_f32_e32 v155, s60, v207
	v_med3_f32 v157, v159, s56, v184
	v_med3_f32 v155, v155, s56, v184
	v_cvt_pk_fp8_f32 v188, v157, v155 op_sel:[0,0,1]
	v_mul_f32_e32 v155, s60, v191
	v_mul_f32_e32 v157, s60, v209
	v_med3_f32 v155, v155, s56, v184
	v_med3_f32 v157, v157, s56, v184
	v_mov_b32_e32 v189, v133
	v_cvt_pk_fp8_f32 v189, v155, v157
	v_mul_f32_e32 v159, s60, v211
	v_mul_f32_e32 v155, s60, v213
	v_med3_f32 v157, v159, s56, v184
	v_med3_f32 v155, v155, s56, v184
	v_cvt_pk_fp8_f32 v189, v157, v155 op_sel:[0,0,1]
	ds_read2_b32 v[192:193], v186 offset0:40 offset1:48
	ds_read2_b32 v[198:199], v186 offset0:105 offset1:113
	ds_read2_b32 v[200:201], v186 offset0:170 offset1:178
	ds_read2_b32 v[206:207], v186 offset0:235 offset1:243
	v_mad_u64_u32 v[190:191], s[12:13], s59, v144, v[176:177]
	v_lshl_add_u64 v[190:191], v[190:191], 0, v[136:137]
	s_waitcnt lgkmcnt(3)
	v_mul_f32_e32 v155, s60, v192
	s_waitcnt lgkmcnt(2)
	v_mul_f32_e32 v157, s60, v198
	global_store_dwordx2 v[190:191], v[188:189], off nt
	v_med3_f32 v155, v155, s56, v184
	v_med3_f32 v157, v157, s56, v184
	v_mov_b32_e32 v188, v133
	v_cvt_pk_fp8_f32 v188, v155, v157
	ds_read2_b32 v[190:191], v185 offset0:44 offset1:52
	ds_read2_b32 v[208:209], v185 offset0:109 offset1:117
	ds_read2_b32 v[210:211], v185 offset0:174 offset1:182
	s_waitcnt lgkmcnt(4)
	v_mul_f32_e32 v159, s60, v200
	s_waitcnt lgkmcnt(3)
	v_mul_f32_e32 v161, s60, v206
	v_med3_f32 v159, v159, s56, v184
	v_med3_f32 v155, v161, s56, v184
	ds_read2_b32 v[212:213], v185 offset0:239 offset1:247
	v_cvt_pk_fp8_f32 v188, v159, v155 op_sel:[0,0,1]
	s_waitcnt lgkmcnt(3)
	v_mul_f32_e32 v155, s60, v190
	s_waitcnt lgkmcnt(2)
	v_mul_f32_e32 v157, s60, v208
	v_med3_f32 v155, v155, s56, v184
	v_med3_f32 v157, v157, s56, v184
	v_mov_b32_e32 v189, v133
	v_cvt_pk_fp8_f32 v189, v155, v157
	s_waitcnt lgkmcnt(1)
	v_mul_f32_e32 v159, s60, v210
	s_waitcnt lgkmcnt(0)
	v_mul_f32_e32 v155, s60, v212
	v_med3_f32 v157, v159, s56, v184
	v_med3_f32 v155, v155, s56, v184
	v_cvt_pk_fp8_f32 v189, v157, v155 op_sel:[0,0,1]
	v_mad_u64_u32 v[214:215], s[12:13], s59, v146, v[176:177]
	v_lshl_add_u64 v[214:215], v[214:215], 0, v[136:137]
	v_mul_f32_e32 v155, s60, v193
	v_mul_f32_e32 v157, s60, v199
	global_store_dwordx2 v[214:215], v[188:189], off nt
	v_med3_f32 v155, v155, s56, v184
	v_med3_f32 v157, v157, s56, v184
	v_mov_b32_e32 v188, v133
	v_cvt_pk_fp8_f32 v188, v155, v157
	v_mul_f32_e32 v159, s60, v201
	v_mul_f32_e32 v155, s60, v207
	v_med3_f32 v157, v159, s56, v184
	v_med3_f32 v155, v155, s56, v184
	v_cvt_pk_fp8_f32 v188, v157, v155 op_sel:[0,0,1]
	v_mul_f32_e32 v155, s60, v191
	v_mul_f32_e32 v157, s60, v209
	v_med3_f32 v155, v155, s56, v184
	v_med3_f32 v157, v157, s56, v184
	v_mov_b32_e32 v189, v133
	v_cvt_pk_fp8_f32 v189, v155, v157
	v_mul_f32_e32 v159, s60, v211
	v_mul_f32_e32 v155, s60, v213
	v_med3_f32 v157, v159, s56, v184
	v_med3_f32 v155, v155, s56, v184
	v_cvt_pk_fp8_f32 v189, v157, v155 op_sel:[0,0,1]
	v_mul_f32_e32 v154, s60, v154
	v_mul_f32_e32 v155, s60, v156
	v_med3_f32 v157, v154, s56, v184
	v_med3_f32 v155, v155, s56, v184
	v_mov_b32_e32 v154, v133
	v_cvt_pk_fp8_f32 v154, v157, v155
	v_mul_f32_e32 v156, s60, v158
	v_mul_f32_e32 v155, s60, v174
	v_med3_f32 v156, v156, s56, v184
	v_med3_f32 v155, v155, s56, v184
	ds_read_b32 v158, v182 offset:18428
	v_cvt_pk_fp8_f32 v154, v156, v155 op_sel:[0,0,1]
	v_mul_f32_e32 v155, s60, v160
	v_mul_f32_e32 v156, s60, v172
	v_med3_f32 v159, v155, s56, v184
	v_med3_f32 v156, v156, s56, v184
	v_mov_b32_e32 v155, v133
	v_cvt_pk_fp8_f32 v155, v159, v156
	v_mul_f32_e32 v157, s60, v178
	s_waitcnt lgkmcnt(0)
	v_mul_f32_e32 v156, s60, v158
	v_med3_f32 v157, v157, s56, v184
	v_med3_f32 v156, v156, s56, v184
	v_cvt_pk_fp8_f32 v155, v157, v156 op_sel:[0,0,1]
	v_mad_u64_u32 v[190:191], s[12:13], s59, v148, v[176:177]
	v_mad_u64_u32 v[156:157], s[12:13], s59, v150, v[176:177]
	v_lshl_add_u64 v[190:191], v[190:191], 0, v[136:137]
	v_lshl_add_u64 v[156:157], v[156:157], 0, v[136:137]
	global_store_dwordx2 v[190:191], v[188:189], off nt
	global_store_dwordx2 v[156:157], v[154:155], off nt
	s_cbranch_execnz .LBB0_415
	s_branch .LBB0_414

.LBB0_524:
	v_lshrrev_b32_e32 v131, 4, v196
	s_waitcnt vmcnt(15)
	v_mul_u32_u24_e32 v2, s10, v131
	v_and_b32_e32 v130, 60, v204
	v_mov_b32_e32 v133, 0
	s_waitcnt lgkmcnt(0)
	v_lshlrev_b32_e32 v132, 2, v2
	v_lshl_add_u64 v[2:3], s[8:9], 0, v[132:133]
	v_lshlrev_b32_e32 v132, 2, v130
	v_or_b32_e32 v135, 4, v131
	s_waitcnt vmcnt(13)
	v_lshl_add_u64 v[10:11], v[2:3], 0, v[132:133]
	v_mul_u32_u24_e32 v2, s10, v135
	v_lshlrev_b32_e32 v2, 2, v2
	v_mov_b32_e32 v3, v133
	v_lshl_add_u64 v[2:3], s[8:9], 0, v[2:3]
	v_or_b32_e32 v139, 8, v131
	v_lshl_add_u64 v[12:13], v[2:3], 0, v[132:133]
	global_load_dwordx4 v[2:5], v[10:11], off nt
	global_load_dwordx4 v[6:9], v[12:13], off nt
	v_mul_u32_u24_e32 v10, s10, v139
	v_lshlrev_b32_e32 v10, 2, v10
	v_mov_b32_e32 v11, v133
	v_lshl_add_u64 v[10:11], s[8:9], 0, v[10:11]
	v_or_b32_e32 v141, 12, v131
	s_waitcnt vmcnt(13)
	v_lshl_add_u64 v[18:19], v[10:11], 0, v[132:133]
	v_mul_u32_u24_e32 v10, s10, v141
	v_lshlrev_b32_e32 v10, 2, v10
	v_mov_b32_e32 v11, v133
	v_lshl_add_u64 v[10:11], s[8:9], 0, v[10:11]
	v_or_b32_e32 v143, 16, v131
	v_lshl_add_u64 v[20:21], v[10:11], 0, v[132:133]
	global_load_dwordx4 v[10:13], v[18:19], off nt
	global_load_dwordx4 v[14:17], v[20:21], off nt
	v_mul_u32_u24_e32 v18, s10, v143
	v_lshlrev_b32_e32 v18, 2, v18
	v_mov_b32_e32 v19, v133
	v_lshl_add_u64 v[18:19], s[8:9], 0, v[18:19]
	v_or_b32_e32 v145, 20, v131
	s_waitcnt vmcnt(13)
	v_lshl_add_u64 v[26:27], v[18:19], 0, v[132:133]
	v_mul_u32_u24_e32 v18, s10, v145
	v_lshlrev_b32_e32 v18, 2, v18
	v_mov_b32_e32 v19, v133
	v_lshl_add_u64 v[18:19], s[8:9], 0, v[18:19]
	v_or_b32_e32 v147, 24, v131
	v_lshl_add_u64 v[28:29], v[18:19], 0, v[132:133]
	global_load_dwordx4 v[18:21], v[26:27], off nt
	global_load_dwordx4 v[22:25], v[28:29], off nt
	v_mul_u32_u24_e32 v26, s10, v147
	v_lshlrev_b32_e32 v26, 2, v26
	v_mov_b32_e32 v27, v133
	v_lshl_add_u64 v[26:27], s[8:9], 0, v[26:27]
	v_or_b32_e32 v149, 28, v131
	s_waitcnt vmcnt(13)
	v_lshl_add_u64 v[34:35], v[26:27], 0, v[132:133]
	v_mul_u32_u24_e32 v26, s10, v149
	v_lshlrev_b32_e32 v26, 2, v26
	v_mov_b32_e32 v27, v133
	v_lshl_add_u64 v[26:27], s[8:9], 0, v[26:27]
	v_or_b32_e32 v151, 32, v131
	v_lshl_add_u64 v[36:37], v[26:27], 0, v[132:133]
	global_load_dwordx4 v[26:29], v[34:35], off nt
	global_load_dwordx4 v[30:33], v[36:37], off nt
	v_mul_u32_u24_e32 v34, s10, v151
	v_lshlrev_b32_e32 v34, 2, v34
	v_mov_b32_e32 v35, v133
	v_lshl_add_u64 v[34:35], s[8:9], 0, v[34:35]
	v_or_b32_e32 v163, 36, v131
	s_waitcnt vmcnt(13)
	v_lshl_add_u64 v[42:43], v[34:35], 0, v[132:133]
	v_mul_u32_u24_e32 v34, s10, v163
	v_lshlrev_b32_e32 v34, 2, v34
	v_mov_b32_e32 v35, v133
	v_lshl_add_u64 v[34:35], s[8:9], 0, v[34:35]
	v_or_b32_e32 v165, 40, v131
	v_lshl_add_u64 v[44:45], v[34:35], 0, v[132:133]
	global_load_dwordx4 v[34:37], v[42:43], off nt
	global_load_dwordx4 v[38:41], v[44:45], off nt
	v_mul_u32_u24_e32 v42, s10, v165
	v_lshlrev_b32_e32 v42, 2, v42
	v_mov_b32_e32 v43, v133
	v_lshl_add_u64 v[42:43], s[8:9], 0, v[42:43]
	v_or_b32_e32 v167, 44, v131
	s_waitcnt vmcnt(13)
	v_lshl_add_u64 v[50:51], v[42:43], 0, v[132:133]
	v_mul_u32_u24_e32 v42, s10, v167
	v_lshlrev_b32_e32 v42, 2, v42
	v_mov_b32_e32 v43, v133
	v_lshl_add_u64 v[42:43], s[8:9], 0, v[42:43]
	v_or_b32_e32 v169, 48, v131
	v_lshl_add_u64 v[52:53], v[42:43], 0, v[132:133]
	global_load_dwordx4 v[42:45], v[50:51], off nt
	global_load_dwordx4 v[46:49], v[52:53], off nt
	v_mul_u32_u24_e32 v50, s10, v169
	v_lshlrev_b32_e32 v50, 2, v50
	v_mov_b32_e32 v51, v133
	v_lshl_add_u64 v[50:51], s[8:9], 0, v[50:51]
	v_or_b32_e32 v171, 52, v131
	v_lshl_add_u64 v[58:59], v[50:51], 0, v[132:133]
	v_mul_u32_u24_e32 v50, s10, v171
	v_lshlrev_b32_e32 v50, 2, v50
	v_mov_b32_e32 v51, v133
	v_lshl_add_u64 v[50:51], s[8:9], 0, v[50:51]
	v_or_b32_e32 v180, 56, v131
	v_lshl_add_u64 v[60:61], v[50:51], 0, v[132:133]
	global_load_dwordx4 v[50:53], v[58:59], off nt
	global_load_dwordx4 v[54:57], v[60:61], off nt
	v_mul_u32_u24_e32 v58, s10, v180
	v_or_b32_e32 v181, 60, v131
	v_lshlrev_b32_e32 v58, 2, v58
	v_mov_b32_e32 v59, v133
	v_mul_u32_u24_e32 v60, s10, v181
	v_lshl_add_u64 v[58:59], s[8:9], 0, v[58:59]
	v_lshlrev_b32_e32 v60, 2, v60
	v_mov_b32_e32 v61, v133
	v_lshl_add_u64 v[58:59], v[58:59], 0, v[132:133]
	v_lshl_add_u64 v[60:61], s[8:9], 0, v[60:61]
	v_lshl_add_u64 v[60:61], v[60:61], 0, v[132:133]
	global_load_dwordx4 v[74:77], v[58:59], off nt
	global_load_dwordx4 v[78:81], v[60:61], off nt
	s_lshl_b32 s8, s15, 5
	s_and_b32 s22, s8, 0xc0
	s_lshl_b32 s8, s15, 6
	s_bfe_u32 s21, s87, 0x10006
	s_and_b32 s23, s8, 64
	s_add_u32 s25, s50, 0x14400000
	s_addc_u32 s26, s51, 0
	s_add_u32 s27, s50, 0x4000000
	s_addc_u32 s28, s51, 0
	s_add_u32 s29, s50, 0x1600000
	s_addc_u32 s30, s51, 0
	s_add_u32 s31, s50, 0xe00000
	s_addc_u32 s33, s51, 0
	v_and_b32_e32 v60, 7, v0
	v_lshrrev_b32_e32 v134, 3, v196
	v_add_u32_e32 v58, s20, v132
	v_mul_u32_u24_e32 v59, 0x104, v131
	s_add_u32 s34, s50, 0xa00000
	v_mul_u32_u24_e32 v61, 0x820, v60
	v_lshlrev_b32_e32 v62, 2, v134
	s_addc_u32 s35, s51, 0
	v_lshlrev_b32_e32 v136, 3, v60
	v_mov_b32_e32 v137, v133
	v_add3_u32 v182, s20, v61, v62
	v_or_b32_e32 v138, 8, v134
	v_or_b32_e32 v140, 16, v134
	v_or_b32_e32 v142, 24, v134
	v_or_b32_e32 v144, 32, v134
	v_or_b32_e32 v146, 40, v134
	v_or_b32_e32 v148, 48, v134
	v_or_b32_e32 v150, 56, v134
	v_lshlrev_b32_e32 v152, 4, v60
	v_mov_b32_e32 v153, v133
	s_add_i32 s57, s14, 0x6c00
	s_add_i32 s20, 0, 0x27ea8
	s_add_i32 s37, 0, 0x27e90
	s_movk_i32 s42, 0x98
	s_movk_i32 s43, 0x88
	s_add_i32 s44, 0, 0x27e60
	s_add_i32 s45, 0, 0x27e58
	s_add_i32 s46, 0, 0x27e50
	s_add_i32 s47, 0, 0x27e30
	s_mov_b32 s53, 0xc3e00000
	v_add_u32_e32 v183, v58, v59
	v_mov_b32_e32 v184, 0x43e00000
	s_mov_b32 s56, s24
	s_mov_b32 s55, s19
	s_mov_b64 s[8:9], s[0:1]
	s_branch .LBB0_528
.LBB0_525:
	ds_read2_b32 v[158:159], v186 offset0:56 offset1:65
	ds_read2_b32 v[160:161], v186 offset0:121 offset1:130
	ds_read2_b32 v[172:173], v186 offset0:186 offset1:195
	ds_read2_b32 v[174:175], v187 offset0:123 offset1:132
	ds_read2_b32 v[176:177], v185 offset0:60 offset1:69
	ds_read2_b32 v[178:179], v185 offset0:125 offset1:134
	ds_read2_b32 v[188:189], v185 offset0:190 offset1:199
	v_mov_b64_e32 v[190:191], s[8:9]
	ds_read2_b32 v[198:199], v186 offset0:8 offset1:16
	ds_read2_b32 v[200:201], v186 offset0:73 offset1:81
	ds_read2_b32 v[204:205], v186 offset0:138 offset1:146
	ds_read2_b32 v[206:207], v186 offset0:203 offset1:211
	ds_read2_b32 v[208:209], v185 offset0:12 offset1:20
	ds_read2_b32 v[210:211], v185 offset0:77 offset1:85
	ds_read2_b32 v[212:213], v185 offset0:142 offset1:150
	ds_read2_b32 v[214:215], v185 offset0:207 offset1:215
	v_mad_u64_u32 v[192:193], s[12:13], s55, v134, v[190:191]
	v_lshl_add_u64 v[192:193], v[192:193], 0, v[152:153]
	s_waitcnt lgkmcnt(14)
	v_cvt_pk_bf16_f32 v154, v132, v159
	s_waitcnt lgkmcnt(12)
	v_cvt_pk_bf16_f32 v155, v161, v173
	s_waitcnt lgkmcnt(10)
	v_cvt_pk_bf16_f32 v156, v175, v177
	s_waitcnt lgkmcnt(8)
	v_cvt_pk_bf16_f32 v157, v179, v189
	global_store_dwordx4 v[192:193], v[154:157], off nt
	v_mad_u64_u32 v[192:193], s[12:13], s55, v138, v[190:191]
	v_lshl_add_u64 v[192:193], v[192:193], 0, v[152:153]
	s_waitcnt lgkmcnt(6)
	v_cvt_pk_bf16_f32 v154, v198, v200
	s_waitcnt lgkmcnt(4)
	v_cvt_pk_bf16_f32 v155, v204, v206
	s_waitcnt lgkmcnt(2)
	v_cvt_pk_bf16_f32 v156, v208, v210
	s_waitcnt lgkmcnt(0)
	v_cvt_pk_bf16_f32 v157, v212, v214
	global_store_dwordx4 v[192:193], v[154:157], off nt
	v_mad_u64_u32 v[192:193], s[12:13], s55, v140, v[190:191]
	s_nop 0
	v_cvt_pk_bf16_f32 v154, v199, v201
	v_cvt_pk_bf16_f32 v155, v205, v207
	v_cvt_pk_bf16_f32 v156, v209, v211
	v_cvt_pk_bf16_f32 v157, v213, v215
	ds_read2_b32 v[198:199], v186 offset0:24 offset1:32
	ds_read2_b32 v[200:201], v186 offset0:89 offset1:97
	ds_read2_b32 v[204:205], v186 offset0:154 offset1:162
	ds_read2_b32 v[206:207], v186 offset0:219 offset1:227
	ds_read2_b32 v[208:209], v185 offset0:28 offset1:36
	ds_read2_b32 v[210:211], v185 offset0:93 offset1:101
	ds_read2_b32 v[212:213], v185 offset0:158 offset1:166
	ds_read2_b32 v[214:215], v185 offset0:223 offset1:231
	v_lshl_add_u64 v[192:193], v[192:193], 0, v[152:153]
	global_store_dwordx4 v[192:193], v[154:157], off nt
	v_mad_u64_u32 v[192:193], s[12:13], s55, v142, v[190:191]
	v_lshl_add_u64 v[192:193], v[192:193], 0, v[152:153]
	s_waitcnt lgkmcnt(6)
	v_cvt_pk_bf16_f32 v154, v198, v200
	s_waitcnt lgkmcnt(4)
	v_cvt_pk_bf16_f32 v155, v204, v206
	s_waitcnt lgkmcnt(2)
	v_cvt_pk_bf16_f32 v156, v208, v210
	s_waitcnt lgkmcnt(0)
	v_cvt_pk_bf16_f32 v157, v212, v214
	global_store_dwordx4 v[192:193], v[154:157], off nt
	v_mad_u64_u32 v[192:193], s[12:13], s55, v144, v[190:191]
	s_nop 0
	v_cvt_pk_bf16_f32 v154, v199, v201
	v_cvt_pk_bf16_f32 v155, v205, v207
	v_cvt_pk_bf16_f32 v156, v209, v211
	v_cvt_pk_bf16_f32 v157, v213, v215
	ds_read2_b32 v[198:199], v186 offset0:40 offset1:48
	ds_read2_b32 v[200:201], v186 offset0:105 offset1:113
	ds_read2_b32 v[204:205], v186 offset0:170 offset1:178
	ds_read2_b32 v[186:187], v186 offset0:235 offset1:243
	ds_read2_b32 v[206:207], v185 offset0:44 offset1:52
	ds_read2_b32 v[208:209], v185 offset0:109 offset1:117
	ds_read2_b32 v[210:211], v185 offset0:174 offset1:182
	ds_read2_b32 v[212:213], v185 offset0:239 offset1:247
	v_lshl_add_u64 v[192:193], v[192:193], 0, v[152:153]
	global_store_dwordx4 v[192:193], v[154:157], off nt
	v_mad_u64_u32 v[192:193], s[12:13], s55, v146, v[190:191]
	s_waitcnt lgkmcnt(4)
	v_cvt_pk_bf16_f32 v155, v204, v186
	v_lshl_add_u64 v[192:193], v[192:193], 0, v[152:153]
	v_cvt_pk_bf16_f32 v154, v198, v200
	s_waitcnt lgkmcnt(2)
	v_cvt_pk_bf16_f32 v156, v206, v208
	s_waitcnt lgkmcnt(0)
	v_cvt_pk_bf16_f32 v157, v210, v212
	global_store_dwordx4 v[192:193], v[154:157], off nt
	ds_read_b32 v132, v182 offset:18428
	s_nop 0
	v_cvt_pk_bf16_f32 v155, v205, v187
	v_mad_u64_u32 v[186:187], s[12:13], s55, v148, v[190:191]
	v_cvt_pk_bf16_f32 v154, v199, v201
	v_lshl_add_u64 v[186:187], v[186:187], 0, v[152:153]
	v_cvt_pk_bf16_f32 v156, v207, v209
	v_cvt_pk_bf16_f32 v157, v211, v213
	global_store_dwordx4 v[186:187], v[154:157], off nt
	s_nop 1
	v_cvt_pk_bf16_f32 v154, v158, v160
	v_mad_u64_u32 v[158:159], s[12:13], s55, v150, v[190:191]
	v_lshl_add_u64 v[158:159], v[158:159], 0, v[152:153]
	v_cvt_pk_bf16_f32 v155, v172, v174
	v_cvt_pk_bf16_f32 v156, v176, v178
	s_waitcnt lgkmcnt(0)
	v_cvt_pk_bf16_f32 v157, v188, v132
	global_store_dwordx4 v[158:159], v[154:157], off nt

.LBB0_558:
	v_mul_u32_u24_e32 v58, s14, v131
	v_mul_u32_u24_e32 v60, s14, v135
	v_mul_u32_u24_e32 v66, s14, v139
	v_mul_u32_u24_e32 v68, s14, v141
	v_mul_u32_u24_e32 v82, s14, v143
	v_mul_u32_u24_e32 v84, s14, v145
	v_mul_u32_u24_e32 v90, s14, v147
	v_mul_u32_u24_e32 v92, s14, v149
	v_mul_u32_u24_e32 v98, s14, v151
	v_mul_u32_u24_e32 v100, s14, v163
	v_mul_u32_u24_e32 v106, s14, v165
	v_mul_u32_u24_e32 v108, s14, v167
	v_mul_u32_u24_e32 v114, s14, v169
	v_mul_u32_u24_e32 v116, s14, v171
	v_mul_u32_u24_e32 v122, s14, v180
	v_mul_u32_u24_e32 v124, s14, v181
	s_waitcnt lgkmcnt(0)
	v_lshlrev_b32_e32 v132, 2, v58
	v_lshlrev_b32_e32 v60, 2, v60
	v_mov_b32_e32 v61, v133
	v_lshlrev_b32_e32 v66, 2, v66
	v_mov_b32_e32 v67, v133
	v_lshlrev_b32_e32 v68, 2, v68
	v_mov_b32_e32 v69, v133
	v_lshlrev_b32_e32 v82, 2, v82
	v_mov_b32_e32 v83, v133
	v_lshlrev_b32_e32 v84, 2, v84
	v_mov_b32_e32 v85, v133
	v_lshlrev_b32_e32 v90, 2, v90
	v_mov_b32_e32 v91, v133
	v_lshlrev_b32_e32 v92, 2, v92
	v_mov_b32_e32 v93, v133
	v_lshlrev_b32_e32 v98, 2, v98
	v_mov_b32_e32 v99, v133
	v_lshlrev_b32_e32 v100, 2, v100
	v_mov_b32_e32 v101, v133
	v_lshlrev_b32_e32 v106, 2, v106
	v_mov_b32_e32 v107, v133
	v_lshlrev_b32_e32 v108, 2, v108
	v_mov_b32_e32 v109, v133
	v_lshlrev_b32_e32 v114, 2, v114
	v_mov_b32_e32 v115, v133
	v_lshlrev_b32_e32 v116, 2, v116
	v_mov_b32_e32 v117, v133
	v_lshlrev_b32_e32 v122, 2, v122
	v_mov_b32_e32 v123, v133
	v_lshlrev_b32_e32 v124, 2, v124
	v_mov_b32_e32 v125, v133
	v_lshl_add_u64 v[58:59], s[12:13], 0, v[132:133]
	v_lshlrev_b32_e32 v132, 2, v130
	v_lshl_add_u64 v[60:61], s[12:13], 0, v[60:61]
	v_lshl_add_u64 v[66:67], s[12:13], 0, v[66:67]
	v_lshl_add_u64 v[68:69], s[12:13], 0, v[68:69]
	v_lshl_add_u64 v[82:83], s[12:13], 0, v[82:83]
	v_lshl_add_u64 v[84:85], s[12:13], 0, v[84:85]
	v_lshl_add_u64 v[90:91], s[12:13], 0, v[90:91]
	v_lshl_add_u64 v[92:93], s[12:13], 0, v[92:93]
	v_lshl_add_u64 v[98:99], s[12:13], 0, v[98:99]
	v_lshl_add_u64 v[100:101], s[12:13], 0, v[100:101]
	v_lshl_add_u64 v[106:107], s[12:13], 0, v[106:107]
	v_lshl_add_u64 v[108:109], s[12:13], 0, v[108:109]
	v_lshl_add_u64 v[114:115], s[12:13], 0, v[114:115]
	v_lshl_add_u64 v[116:117], s[12:13], 0, v[116:117]
	v_lshl_add_u64 v[122:123], s[12:13], 0, v[122:123]
	v_lshl_add_u64 v[124:125], s[12:13], 0, v[124:125]
	v_lshl_add_u64 v[58:59], v[58:59], 0, v[132:133]
	v_lshl_add_u64 v[60:61], v[60:61], 0, v[132:133]
	v_lshl_add_u64 v[66:67], v[66:67], 0, v[132:133]
	v_lshl_add_u64 v[68:69], v[68:69], 0, v[132:133]
	v_lshl_add_u64 v[82:83], v[82:83], 0, v[132:133]
	v_lshl_add_u64 v[84:85], v[84:85], 0, v[132:133]
	v_lshl_add_u64 v[90:91], v[90:91], 0, v[132:133]
	v_lshl_add_u64 v[92:93], v[92:93], 0, v[132:133]
	v_lshl_add_u64 v[98:99], v[98:99], 0, v[132:133]
	v_lshl_add_u64 v[100:101], v[100:101], 0, v[132:133]
	v_lshl_add_u64 v[106:107], v[106:107], 0, v[132:133]
	v_lshl_add_u64 v[108:109], v[108:109], 0, v[132:133]
	v_lshl_add_u64 v[114:115], v[114:115], 0, v[132:133]
	v_lshl_add_u64 v[116:117], v[116:117], 0, v[132:133]
	v_lshl_add_u64 v[122:123], v[122:123], 0, v[132:133]
	v_lshl_add_u64 v[124:125], v[124:125], 0, v[132:133]
	global_load_dwordx4 v[62:65], v[58:59], off nt
	s_nop 0
	global_load_dwordx4 v[58:61], v[60:61], off nt
	s_nop 0
	global_load_dwordx4 v[70:73], v[66:67], off nt
	s_nop 0
	global_load_dwordx4 v[66:69], v[68:69], off nt
	s_nop 0
	global_load_dwordx4 v[86:89], v[82:83], off nt
	s_nop 0
	global_load_dwordx4 v[82:85], v[84:85], off nt
	s_nop 0
	global_load_dwordx4 v[94:97], v[90:91], off nt
	s_nop 0
	global_load_dwordx4 v[90:93], v[92:93], off nt
	s_nop 0
	global_load_dwordx4 v[102:105], v[98:99], off nt
	s_nop 0
	global_load_dwordx4 v[98:101], v[100:101], off nt
	s_nop 0
	global_load_dwordx4 v[110:113], v[106:107], off nt
	s_nop 0
	global_load_dwordx4 v[106:109], v[108:109], off nt
	s_nop 0
	global_load_dwordx4 v[118:121], v[114:115], off nt
	s_nop 0
	global_load_dwordx4 v[114:117], v[116:117], off nt
	s_nop 0
	global_load_dwordx4 v[126:129], v[122:123], off nt
	s_nop 0
	global_load_dwordx4 v[122:125], v[124:125], off nt
.LBB0_559:
	v_add_u32_e32 v188, 0x4000, v183
	v_add_u32_e32 v189, 0x4008, v183
	v_add_u32_e32 v190, 0x4410, v183
	v_add_u32_e32 v191, 0x4418, v183
	v_add_u32_e32 v192, 0x4820, v183
	v_add_u32_e32 v193, 0x4828, v183
	v_add_u32_e32 v198, 0x4c30, v183
	v_add_u32_e32 v199, 0x4c38, v183
	v_add_u32_e32 v200, 0x5040, v183
	v_add_u32_e32 v201, 0x5048, v183
	v_add_u32_e32 v204, 0x5450, v183
	v_add_u32_e32 v205, 0x5458, v183
	v_add_u32_e32 v206, 0x5860, v183
	v_add_u32_e32 v207, 0x5868, v183
	v_add_u32_e32 v208, 0x5c70, v183
	v_add_u32_e32 v209, 0x5c78, v183
	v_add_u32_e32 v210, 0x6080, v183
	v_add_u32_e32 v211, 0x6088, v183
	v_add_u32_e32 v212, 0x6490, v183
	v_add_u32_e32 v213, 0x6498, v183
	v_add_u32_e32 v214, 0x68a0, v183
	v_add_u32_e32 v215, 0x68a8, v183
	v_add_u32_e32 v216, 0x6cb0, v183
	v_add_u32_e32 v217, 0x6cb8, v183
	v_add_u32_e32 v218, 0x70c0, v183
	v_add_u32_e32 v219, 0x70c8, v183
	v_add_u32_e32 v220, 0x74d0, v183
	v_add_u32_e32 v221, 0x74d8, v183
	v_add_u32_e32 v222, 0x78e0, v183
	v_add_u32_e32 v223, 0x78e8, v183
	v_add_u32_e32 v224, 0x7cf0, v183
	v_add_u32_e32 v225, 0x7cf8, v183
	s_waitcnt vmcnt(15)
	ds_write2_b32 v188, v2, v3 offset1:1
	ds_write2_b32 v189, v4, v5 offset1:1
	s_waitcnt vmcnt(14)
	ds_write2_b32 v190, v6, v7 offset1:1
	ds_write2_b32 v191, v8, v9 offset1:1
	s_waitcnt vmcnt(13)
	ds_write2_b32 v192, v10, v11 offset1:1
	ds_write2_b32 v193, v12, v13 offset1:1
	s_waitcnt vmcnt(12)
	ds_write2_b32 v198, v14, v15 offset1:1
	ds_write2_b32 v199, v16, v17 offset1:1
	s_waitcnt vmcnt(11)
	ds_write2_b32 v200, v18, v19 offset1:1
	ds_write2_b32 v201, v20, v21 offset1:1
	s_waitcnt vmcnt(10)
	ds_write2_b32 v204, v22, v23 offset1:1
	ds_write2_b32 v205, v24, v25 offset1:1
	s_waitcnt vmcnt(9)
	ds_write2_b32 v206, v26, v27 offset1:1
	ds_write2_b32 v207, v28, v29 offset1:1
	s_waitcnt vmcnt(8)
	ds_write2_b32 v208, v30, v31 offset1:1
	ds_write2_b32 v209, v32, v33 offset1:1
	s_waitcnt vmcnt(7)
	ds_write2_b32 v210, v34, v35 offset1:1
	ds_write2_b32 v211, v36, v37 offset1:1
	s_waitcnt vmcnt(6)
	ds_write2_b32 v212, v38, v39 offset1:1
	ds_write2_b32 v213, v40, v41 offset1:1
	s_waitcnt vmcnt(5)
	ds_write2_b32 v214, v42, v43 offset1:1
	ds_write2_b32 v215, v44, v45 offset1:1
	s_waitcnt vmcnt(4)
	ds_write2_b32 v216, v46, v47 offset1:1
	ds_write2_b32 v217, v48, v49 offset1:1
	s_waitcnt vmcnt(3)
	ds_write2_b32 v218, v50, v51 offset1:1
	ds_write2_b32 v219, v52, v53 offset1:1
	s_waitcnt vmcnt(2)
	ds_write2_b32 v220, v54, v55 offset1:1
	ds_write2_b32 v221, v56, v57 offset1:1
	s_waitcnt vmcnt(1)
	ds_write2_b32 v222, v74, v75 offset1:1
	ds_write2_b32 v223, v76, v77 offset1:1
	s_waitcnt vmcnt(0)
	ds_write2_b32 v224, v78, v79 offset1:1
	ds_write2_b32 v225, v80, v81 offset1:1
	s_waitcnt lgkmcnt(0)
	ds_read_b32 v132, v182 offset:16384
	v_cmp_eq_f32_e64 s[12:13], s24, 0
	s_and_b64 vcc, exec, s[12:13]
	v_add_u32_e32 v186, 0x4000, v182
	v_add_u32_e32 v187, 0x4200, v182
	v_add_u32_e32 v185, 0x4400, v182
	s_cbranch_vccnz .LBB0_580
	ds_read2_b32 v[154:155], v186 offset0:56 offset1:65
	ds_read2_b32 v[156:157], v186 offset0:121 offset1:130
	ds_read2_b32 v[158:159], v186 offset0:186 offset1:195
	s_waitcnt lgkmcnt(3)
	v_mul_f32_e32 v160, s24, v132
	v_med3_f32 v160, v160, s53, v184
	s_waitcnt lgkmcnt(2)
	v_mul_f32_e32 v155, s24, v155
	v_med3_f32 v155, v155, s53, v184
	v_mov_b32_e32 v226, v133
	v_cvt_pk_fp8_f32 v226, v160, v155
	ds_read2_b32 v[174:175], v187 offset0:123 offset1:132
	ds_read2_b32 v[160:161], v185 offset0:60 offset1:69
	ds_read2_b32 v[172:173], v185 offset0:125 offset1:134
	s_waitcnt lgkmcnt(4)
	v_mul_f32_e32 v157, s24, v157
	s_waitcnt lgkmcnt(3)
	v_mul_f32_e32 v159, s24, v159
	v_med3_f32 v157, v157, s53, v184
	v_med3_f32 v155, v159, s53, v184
	ds_read2_b32 v[178:179], v185 offset0:190 offset1:199
	v_cvt_pk_fp8_f32 v226, v157, v155 op_sel:[0,0,1]
	s_waitcnt lgkmcnt(3)
	v_mul_f32_e32 v155, s24, v175
	s_waitcnt lgkmcnt(2)
	v_mul_f32_e32 v157, s24, v161
	v_med3_f32 v155, v155, s53, v184
	v_med3_f32 v157, v157, s53, v184
	v_mov_b32_e32 v227, v133
	v_cvt_pk_fp8_f32 v227, v155, v157
	s_waitcnt lgkmcnt(1)
	v_mul_f32_e32 v159, s24, v173
	s_waitcnt lgkmcnt(0)
	v_mul_f32_e32 v155, s24, v179
	v_med3_f32 v157, v159, s53, v184
	v_med3_f32 v155, v155, s53, v184
	v_cvt_pk_fp8_f32 v227, v157, v155 op_sel:[0,0,1]
	ds_read2_b32 v[230:231], v186 offset0:8 offset1:16
	ds_read2_b32 v[232:233], v186 offset0:73 offset1:81
	ds_read2_b32 v[234:235], v186 offset0:138 offset1:146
	ds_read2_b32 v[236:237], v186 offset0:203 offset1:211
	v_mov_b64_e32 v[176:177], s[0:1]
	v_mad_u64_u32 v[228:229], s[12:13], s19, v134, v[176:177]
	v_lshl_add_u64 v[228:229], v[228:229], 0, v[136:137]
	s_waitcnt lgkmcnt(3)
	v_mul_f32_e32 v155, s24, v230
	s_waitcnt lgkmcnt(2)
	v_mul_f32_e32 v157, s24, v232
	global_store_dwordx2 v[228:229], v[226:227], off nt
	v_med3_f32 v155, v155, s53, v184
	v_med3_f32 v157, v157, s53, v184
	v_mov_b32_e32 v226, v133
	v_cvt_pk_fp8_f32 v226, v155, v157
	ds_read2_b32 v[228:229], v185 offset0:12 offset1:20
	ds_read2_b32 v[238:239], v185 offset0:77 offset1:85
	ds_read2_b32 v[240:241], v185 offset0:142 offset1:150
	s_waitcnt lgkmcnt(4)
	v_mul_f32_e32 v159, s24, v234
	s_waitcnt lgkmcnt(3)
	v_mul_f32_e32 v161, s24, v236
	v_med3_f32 v159, v159, s53, v184
	v_med3_f32 v155, v161, s53, v184
	ds_read2_b32 v[242:243], v185 offset0:207 offset1:215
	v_cvt_pk_fp8_f32 v226, v159, v155 op_sel:[0,0,1]
	s_waitcnt lgkmcnt(3)
	v_mul_f32_e32 v155, s24, v228
	s_waitcnt lgkmcnt(2)
	v_mul_f32_e32 v157, s24, v238
	v_med3_f32 v155, v155, s53, v184
	v_med3_f32 v157, v157, s53, v184
	v_mov_b32_e32 v227, v133
	v_cvt_pk_fp8_f32 v227, v155, v157
	s_waitcnt lgkmcnt(1)
	v_mul_f32_e32 v159, s24, v240
	s_waitcnt lgkmcnt(0)
	v_mul_f32_e32 v155, s24, v242
	v_med3_f32 v157, v159, s53, v184
	v_med3_f32 v155, v155, s53, v184
	v_cvt_pk_fp8_f32 v227, v157, v155 op_sel:[0,0,1]
	v_mad_u64_u32 v[244:245], s[12:13], s19, v138, v[176:177]
	v_lshl_add_u64 v[244:245], v[244:245], 0, v[136:137]
	v_mul_f32_e32 v155, s24, v231
	v_mul_f32_e32 v157, s24, v233
	global_store_dwordx2 v[244:245], v[226:227], off nt
	v_med3_f32 v155, v155, s53, v184
	v_med3_f32 v157, v157, s53, v184
	v_mov_b32_e32 v226, v133
	v_cvt_pk_fp8_f32 v226, v155, v157
	v_mul_f32_e32 v159, s24, v235
	v_mul_f32_e32 v155, s24, v237
	v_med3_f32 v157, v159, s53, v184
	v_med3_f32 v155, v155, s53, v184
	v_cvt_pk_fp8_f32 v226, v157, v155 op_sel:[0,0,1]
	v_mul_f32_e32 v155, s24, v229
	v_mul_f32_e32 v157, s24, v239
	v_med3_f32 v155, v155, s53, v184
	v_med3_f32 v157, v157, s53, v184
	v_mov_b32_e32 v227, v133
	v_cvt_pk_fp8_f32 v227, v155, v157
	v_mul_f32_e32 v159, s24, v241
	v_mul_f32_e32 v155, s24, v243
	v_med3_f32 v157, v159, s53, v184
	v_med3_f32 v155, v155, s53, v184
	v_cvt_pk_fp8_f32 v227, v157, v155 op_sel:[0,0,1]
	ds_read2_b32 v[230:231], v186 offset0:24 offset1:32
	ds_read2_b32 v[232:233], v186 offset0:89 offset1:97
	ds_read2_b32 v[234:235], v186 offset0:154 offset1:162
	ds_read2_b32 v[236:237], v186 offset0:219 offset1:227
	v_mad_u64_u32 v[228:229], s[12:13], s19, v140, v[176:177]
	v_lshl_add_u64 v[228:229], v[228:229], 0, v[136:137]
	s_waitcnt lgkmcnt(3)
	v_mul_f32_e32 v155, s24, v230
	s_waitcnt lgkmcnt(2)
	v_mul_f32_e32 v157, s24, v232
	global_store_dwordx2 v[228:229], v[226:227], off nt
	v_med3_f32 v155, v155, s53, v184
	v_med3_f32 v157, v157, s53, v184
	v_mov_b32_e32 v226, v133
	v_cvt_pk_fp8_f32 v226, v155, v157
	ds_read2_b32 v[228:229], v185 offset0:28 offset1:36
	ds_read2_b32 v[238:239], v185 offset0:93 offset1:101
	ds_read2_b32 v[240:241], v185 offset0:158 offset1:166
	s_waitcnt lgkmcnt(4)
	v_mul_f32_e32 v159, s24, v234
	s_waitcnt lgkmcnt(3)
	v_mul_f32_e32 v161, s24, v236
	v_med3_f32 v159, v159, s53, v184
	v_med3_f32 v155, v161, s53, v184
	ds_read2_b32 v[242:243], v185 offset0:223 offset1:231
	v_cvt_pk_fp8_f32 v226, v159, v155 op_sel:[0,0,1]
	s_waitcnt lgkmcnt(3)
	v_mul_f32_e32 v155, s24, v228
	s_waitcnt lgkmcnt(2)
	v_mul_f32_e32 v157, s24, v238
	v_med3_f32 v155, v155, s53, v184
	v_med3_f32 v157, v157, s53, v184
	v_mov_b32_e32 v227, v133
	v_cvt_pk_fp8_f32 v227, v155, v157
	s_waitcnt lgkmcnt(1)
	v_mul_f32_e32 v159, s24, v240
	s_waitcnt lgkmcnt(0)
	v_mul_f32_e32 v155, s24, v242
	v_med3_f32 v157, v159, s53, v184
	v_med3_f32 v155, v155, s53, v184
	v_cvt_pk_fp8_f32 v227, v157, v155 op_sel:[0,0,1]
	v_mad_u64_u32 v[244:245], s[12:13], s19, v142, v[176:177]
	v_lshl_add_u64 v[244:245], v[244:245], 0, v[136:137]
	v_mul_f32_e32 v155, s24, v231
	v_mul_f32_e32 v157, s24, v233
	global_store_dwordx2 v[244:245], v[226:227], off nt
	v_med3_f32 v155, v155, s53, v184
	v_med3_f32 v157, v157, s53, v184
	v_mov_b32_e32 v226, v133
	v_cvt_pk_fp8_f32 v226, v155, v157
	v_mul_f32_e32 v159, s24, v235
	v_mul_f32_e32 v155, s24, v237
	v_med3_f32 v157, v159, s53, v184
	v_med3_f32 v155, v155, s53, v184
	v_cvt_pk_fp8_f32 v226, v157, v155 op_sel:[0,0,1]
	v_mul_f32_e32 v155, s24, v229
	v_mul_f32_e32 v157, s24, v239
	v_med3_f32 v155, v155, s53, v184
	v_med3_f32 v157, v157, s53, v184
	v_mov_b32_e32 v227, v133
	v_cvt_pk_fp8_f32 v227, v155, v157
	v_mul_f32_e32 v159, s24, v241
	v_mul_f32_e32 v155, s24, v243
	v_med3_f32 v157, v159, s53, v184
	v_med3_f32 v155, v155, s53, v184
	v_cvt_pk_fp8_f32 v227, v157, v155 op_sel:[0,0,1]
	ds_read2_b32 v[230:231], v186 offset0:40 offset1:48
	ds_read2_b32 v[232:233], v186 offset0:105 offset1:113
	ds_read2_b32 v[234:235], v186 offset0:170 offset1:178
	ds_read2_b32 v[236:237], v186 offset0:235 offset1:243
	v_mad_u64_u32 v[228:229], s[12:13], s19, v144, v[176:177]
	v_lshl_add_u64 v[228:229], v[228:229], 0, v[136:137]
	s_waitcnt lgkmcnt(3)
	v_mul_f32_e32 v155, s24, v230
	s_waitcnt lgkmcnt(2)
	v_mul_f32_e32 v157, s24, v232
	global_store_dwordx2 v[228:229], v[226:227], off nt
	v_med3_f32 v155, v155, s53, v184
	v_med3_f32 v157, v157, s53, v184
	v_mov_b32_e32 v226, v133
	v_cvt_pk_fp8_f32 v226, v155, v157
	ds_read2_b32 v[228:229], v185 offset0:44 offset1:52
	ds_read2_b32 v[238:239], v185 offset0:109 offset1:117
	ds_read2_b32 v[240:241], v185 offset0:174 offset1:182
	s_waitcnt lgkmcnt(4)
	v_mul_f32_e32 v159, s24, v234
	s_waitcnt lgkmcnt(3)
	v_mul_f32_e32 v161, s24, v236
	v_med3_f32 v159, v159, s53, v184
	v_med3_f32 v155, v161, s53, v184
	ds_read2_b32 v[242:243], v185 offset0:239 offset1:247
	v_cvt_pk_fp8_f32 v226, v159, v155 op_sel:[0,0,1]
	s_waitcnt lgkmcnt(3)
	v_mul_f32_e32 v155, s24, v228
	s_waitcnt lgkmcnt(2)
	v_mul_f32_e32 v157, s24, v238
	v_med3_f32 v155, v155, s53, v184
	v_med3_f32 v157, v157, s53, v184
	v_mov_b32_e32 v227, v133
	v_cvt_pk_fp8_f32 v227, v155, v157
	s_waitcnt lgkmcnt(1)
	v_mul_f32_e32 v159, s24, v240
	s_waitcnt lgkmcnt(0)
	v_mul_f32_e32 v155, s24, v242
	v_med3_f32 v157, v159, s53, v184
	v_med3_f32 v155, v155, s53, v184
	v_cvt_pk_fp8_f32 v227, v157, v155 op_sel:[0,0,1]
	v_mad_u64_u32 v[244:245], s[12:13], s19, v146, v[176:177]
	v_lshl_add_u64 v[244:245], v[244:245], 0, v[136:137]
	v_mul_f32_e32 v155, s24, v231
	v_mul_f32_e32 v157, s24, v233
	global_store_dwordx2 v[244:245], v[226:227], off nt
	v_med3_f32 v155, v155, s53, v184
	v_med3_f32 v157, v157, s53, v184
	v_mov_b32_e32 v226, v133
	v_cvt_pk_fp8_f32 v226, v155, v157
	v_mul_f32_e32 v159, s24, v235
	v_mul_f32_e32 v155, s24, v237
	v_med3_f32 v157, v159, s53, v184
	v_med3_f32 v155, v155, s53, v184
	v_cvt_pk_fp8_f32 v226, v157, v155 op_sel:[0,0,1]
	v_mul_f32_e32 v155, s24, v229
	v_mul_f32_e32 v157, s24, v239
	v_med3_f32 v155, v155, s53, v184
	v_med3_f32 v157, v157, s53, v184
	v_mov_b32_e32 v227, v133
	v_cvt_pk_fp8_f32 v227, v155, v157
	v_mul_f32_e32 v159, s24, v241
	v_mul_f32_e32 v155, s24, v243
	v_med3_f32 v157, v159, s53, v184
	v_med3_f32 v155, v155, s53, v184
	v_cvt_pk_fp8_f32 v227, v157, v155 op_sel:[0,0,1]
	v_mul_f32_e32 v154, s24, v154
	v_mul_f32_e32 v155, s24, v156
	v_med3_f32 v157, v154, s53, v184
	v_med3_f32 v155, v155, s53, v184
	v_mov_b32_e32 v154, v133
	v_cvt_pk_fp8_f32 v154, v157, v155
	v_mul_f32_e32 v156, s24, v158
	v_mul_f32_e32 v155, s24, v174
	v_med3_f32 v156, v156, s53, v184
	v_med3_f32 v155, v155, s53, v184
	ds_read_b32 v158, v182 offset:18428
	v_cvt_pk_fp8_f32 v154, v156, v155 op_sel:[0,0,1]
	v_mul_f32_e32 v155, s24, v160
	v_mul_f32_e32 v156, s24, v172
	v_med3_f32 v159, v155, s53, v184
	v_med3_f32 v156, v156, s53, v184
	v_mov_b32_e32 v155, v133
	v_cvt_pk_fp8_f32 v155, v159, v156
	v_mul_f32_e32 v157, s24, v178
	s_waitcnt lgkmcnt(0)
	v_mul_f32_e32 v156, s24, v158
	v_med3_f32 v157, v157, s53, v184
	v_med3_f32 v156, v156, s53, v184
	v_cvt_pk_fp8_f32 v155, v157, v156 op_sel:[0,0,1]
	v_mad_u64_u32 v[228:229], s[12:13], s19, v148, v[176:177]
	v_mad_u64_u32 v[156:157], s[12:13], s19, v150, v[176:177]
	v_lshl_add_u64 v[228:229], v[228:229], 0, v[136:137]
	v_lshl_add_u64 v[156:157], v[156:157], 0, v[136:137]
	global_store_dwordx2 v[228:229], v[226:227], off nt
	global_store_dwordx2 v[156:157], v[154:155], off nt
	s_cbranch_execnz .LBB0_562
.LBB0_561:
	ds_read2_b32 v[158:159], v186 offset0:56 offset1:65
	ds_read2_b32 v[160:161], v186 offset0:121 offset1:130
	ds_read2_b32 v[172:173], v186 offset0:186 offset1:195
	ds_read2_b32 v[174:175], v187 offset0:123 offset1:132
	ds_read2_b32 v[176:177], v185 offset0:60 offset1:69
	ds_read2_b32 v[178:179], v185 offset0:125 offset1:134
	ds_read2_b32 v[226:227], v185 offset0:190 offset1:199
	v_mov_b64_e32 v[228:229], s[0:1]
	ds_read2_b32 v[232:233], v186 offset0:8 offset1:16
	ds_read2_b32 v[234:235], v186 offset0:73 offset1:81
	ds_read2_b32 v[236:237], v186 offset0:138 offset1:146
	ds_read2_b32 v[238:239], v186 offset0:203 offset1:211
	ds_read2_b32 v[240:241], v185 offset0:12 offset1:20
	ds_read2_b32 v[242:243], v185 offset0:77 offset1:85
	ds_read2_b32 v[244:245], v185 offset0:142 offset1:150
	ds_read2_b32 v[246:247], v185 offset0:207 offset1:215
	v_mad_u64_u32 v[230:231], s[12:13], s19, v134, v[228:229]
	v_lshl_add_u64 v[230:231], v[230:231], 0, v[152:153]
	s_waitcnt lgkmcnt(14)
	v_cvt_pk_bf16_f32 v154, v132, v159
	s_waitcnt lgkmcnt(12)
	v_cvt_pk_bf16_f32 v155, v161, v173
	s_waitcnt lgkmcnt(10)
	v_cvt_pk_bf16_f32 v156, v175, v177
	s_waitcnt lgkmcnt(8)
	v_cvt_pk_bf16_f32 v157, v179, v227
	global_store_dwordx4 v[230:231], v[154:157], off nt
	v_mad_u64_u32 v[230:231], s[12:13], s19, v138, v[228:229]
	v_lshl_add_u64 v[230:231], v[230:231], 0, v[152:153]
	s_waitcnt lgkmcnt(6)
	v_cvt_pk_bf16_f32 v154, v232, v234
	s_waitcnt lgkmcnt(4)
	v_cvt_pk_bf16_f32 v155, v236, v238
	s_waitcnt lgkmcnt(2)
	v_cvt_pk_bf16_f32 v156, v240, v242
	s_waitcnt lgkmcnt(0)
	v_cvt_pk_bf16_f32 v157, v244, v246
	global_store_dwordx4 v[230:231], v[154:157], off nt
	v_mad_u64_u32 v[230:231], s[12:13], s19, v140, v[228:229]
	s_nop 0
	v_cvt_pk_bf16_f32 v154, v233, v235
	v_cvt_pk_bf16_f32 v155, v237, v239
	v_cvt_pk_bf16_f32 v156, v241, v243
	v_cvt_pk_bf16_f32 v157, v245, v247
	ds_read2_b32 v[232:233], v186 offset0:24 offset1:32
	ds_read2_b32 v[234:235], v186 offset0:89 offset1:97
	ds_read2_b32 v[236:237], v186 offset0:154 offset1:162
	ds_read2_b32 v[238:239], v186 offset0:219 offset1:227
	ds_read2_b32 v[240:241], v185 offset0:28 offset1:36
	ds_read2_b32 v[242:243], v185 offset0:93 offset1:101
	ds_read2_b32 v[244:245], v185 offset0:158 offset1:166
	ds_read2_b32 v[246:247], v185 offset0:223 offset1:231
	v_lshl_add_u64 v[230:231], v[230:231], 0, v[152:153]
	global_store_dwordx4 v[230:231], v[154:157], off nt
	v_mad_u64_u32 v[230:231], s[12:13], s19, v142, v[228:229]
	v_lshl_add_u64 v[230:231], v[230:231], 0, v[152:153]
	s_waitcnt lgkmcnt(6)
	v_cvt_pk_bf16_f32 v154, v232, v234
	s_waitcnt lgkmcnt(4)
	v_cvt_pk_bf16_f32 v155, v236, v238
	s_waitcnt lgkmcnt(2)
	v_cvt_pk_bf16_f32 v156, v240, v242
	s_waitcnt lgkmcnt(0)
	v_cvt_pk_bf16_f32 v157, v244, v246
	global_store_dwordx4 v[230:231], v[154:157], off nt
	v_mad_u64_u32 v[230:231], s[12:13], s19, v144, v[228:229]
	s_nop 0
	v_cvt_pk_bf16_f32 v154, v233, v235
	v_cvt_pk_bf16_f32 v155, v237, v239
	v_cvt_pk_bf16_f32 v156, v241, v243
	v_cvt_pk_bf16_f32 v157, v245, v247
	ds_read2_b32 v[232:233], v186 offset0:40 offset1:48
	ds_read2_b32 v[234:235], v186 offset0:105 offset1:113
	ds_read2_b32 v[236:237], v186 offset0:170 offset1:178
	ds_read2_b32 v[238:239], v186 offset0:235 offset1:243
	ds_read2_b32 v[240:241], v185 offset0:44 offset1:52
	ds_read2_b32 v[242:243], v185 offset0:109 offset1:117
	ds_read2_b32 v[244:245], v185 offset0:174 offset1:182
	ds_read2_b32 v[246:247], v185 offset0:239 offset1:247
	v_lshl_add_u64 v[230:231], v[230:231], 0, v[152:153]
	global_store_dwordx4 v[230:231], v[154:157], off nt
	v_mad_u64_u32 v[230:231], s[12:13], s19, v146, v[228:229]
	v_lshl_add_u64 v[230:231], v[230:231], 0, v[152:153]
	s_waitcnt lgkmcnt(6)
	v_cvt_pk_bf16_f32 v154, v232, v234
	s_waitcnt lgkmcnt(4)
	v_cvt_pk_bf16_f32 v155, v236, v238
	s_waitcnt lgkmcnt(2)
	v_cvt_pk_bf16_f32 v156, v240, v242
	s_waitcnt lgkmcnt(0)
	v_cvt_pk_bf16_f32 v157, v244, v246
	global_store_dwordx4 v[230:231], v[154:157], off nt
	v_mad_u64_u32 v[230:231], s[12:13], s19, v148, v[228:229]
	s_nop 0
	v_cvt_pk_bf16_f32 v154, v233, v235
	v_lshl_add_u64 v[230:231], v[230:231], 0, v[152:153]
	v_cvt_pk_bf16_f32 v155, v237, v239
	v_cvt_pk_bf16_f32 v156, v241, v243
	v_cvt_pk_bf16_f32 v157, v245, v247
	global_store_dwordx4 v[230:231], v[154:157], off nt
	ds_read_b32 v132, v182 offset:18428
	s_nop 0
	v_cvt_pk_bf16_f32 v154, v158, v160
	v_mad_u64_u32 v[158:159], s[12:13], s19, v150, v[228:229]
	v_lshl_add_u64 v[158:159], v[158:159], 0, v[152:153]
	v_cvt_pk_bf16_f32 v155, v172, v174
	v_cvt_pk_bf16_f32 v156, v176, v178
	s_waitcnt lgkmcnt(0)
	v_cvt_pk_bf16_f32 v157, v226, v132
	global_store_dwordx4 v[158:159], v[154:157], off nt

.LBB0_595:
	ds_write2_b32 v188, v62, v63 offset1:1
	ds_write2_b32 v189, v64, v65 offset1:1
	ds_write2_b32 v190, v58, v59 offset1:1
	ds_write2_b32 v191, v60, v61 offset1:1
	ds_write2_b32 v192, v70, v71 offset1:1
	ds_write2_b32 v193, v72, v73 offset1:1
	ds_write2_b32 v198, v66, v67 offset1:1
	ds_write2_b32 v199, v68, v69 offset1:1
	ds_write2_b32 v200, v86, v87 offset1:1
	ds_write2_b32 v201, v88, v89 offset1:1
	ds_write2_b32 v204, v82, v83 offset1:1
	ds_write2_b32 v205, v84, v85 offset1:1
	ds_write2_b32 v206, v94, v95 offset1:1
	ds_write2_b32 v207, v96, v97 offset1:1
	ds_write2_b32 v208, v90, v91 offset1:1
	ds_write2_b32 v209, v92, v93 offset1:1
	ds_write2_b32 v210, v102, v103 offset1:1
	ds_write2_b32 v211, v104, v105 offset1:1
	ds_write2_b32 v212, v98, v99 offset1:1
	ds_write2_b32 v213, v100, v101 offset1:1
	ds_write2_b32 v214, v110, v111 offset1:1
	ds_write2_b32 v215, v112, v113 offset1:1
	ds_write2_b32 v216, v106, v107 offset1:1
	ds_write2_b32 v217, v108, v109 offset1:1
	ds_write2_b32 v218, v118, v119 offset1:1
	ds_write2_b32 v219, v120, v121 offset1:1
	ds_write2_b32 v220, v114, v115 offset1:1
	ds_write2_b32 v221, v116, v117 offset1:1
	ds_write2_b32 v222, v126, v127 offset1:1
	ds_write2_b32 v223, v128, v129 offset1:1
	ds_write2_b32 v224, v122, v123 offset1:1
	ds_write2_b32 v225, v124, v125 offset1:1
	s_waitcnt lgkmcnt(0)
	s_waitcnt lgkmcnt(14)
	ds_read_b32 v132, v182 offset:16384
	v_cmp_eq_f32_e64 s[12:13], s56, 0
	s_and_b64 vcc, exec, s[12:13]
	s_cbranch_vccnz .LBB0_597
	ds_read2_b32 v[154:155], v186 offset0:56 offset1:65
	ds_read2_b32 v[156:157], v186 offset0:121 offset1:130
	ds_read2_b32 v[158:159], v186 offset0:186 offset1:195
	s_waitcnt lgkmcnt(3)
	v_mul_f32_e32 v160, s56, v132
	v_med3_f32 v160, v160, s53, v184
	s_waitcnt lgkmcnt(2)
	v_mul_f32_e32 v155, s56, v155
	v_med3_f32 v155, v155, s53, v184
	v_mov_b32_e32 v188, v133
	v_cvt_pk_fp8_f32 v188, v160, v155
	ds_read2_b32 v[174:175], v187 offset0:123 offset1:132
	ds_read2_b32 v[160:161], v185 offset0:60 offset1:69
	ds_read2_b32 v[172:173], v185 offset0:125 offset1:134
	s_waitcnt lgkmcnt(4)
	v_mul_f32_e32 v157, s56, v157
	s_waitcnt lgkmcnt(3)
	v_mul_f32_e32 v159, s56, v159
	v_med3_f32 v157, v157, s53, v184
	v_med3_f32 v155, v159, s53, v184
	ds_read2_b32 v[178:179], v185 offset0:190 offset1:199
	v_cvt_pk_fp8_f32 v188, v157, v155 op_sel:[0,0,1]
	s_waitcnt lgkmcnt(3)
	v_mul_f32_e32 v155, s56, v175
	s_waitcnt lgkmcnt(2)
	v_mul_f32_e32 v157, s56, v161
	v_med3_f32 v155, v155, s53, v184
	v_med3_f32 v157, v157, s53, v184
	v_mov_b32_e32 v189, v133
	v_cvt_pk_fp8_f32 v189, v155, v157
	s_waitcnt lgkmcnt(1)
	v_mul_f32_e32 v159, s56, v173
	s_waitcnt lgkmcnt(0)
	v_mul_f32_e32 v155, s56, v179
	v_med3_f32 v157, v159, s53, v184
	v_med3_f32 v155, v155, s53, v184
	v_cvt_pk_fp8_f32 v189, v157, v155 op_sel:[0,0,1]
	ds_read2_b32 v[192:193], v186 offset0:8 offset1:16
	ds_read2_b32 v[198:199], v186 offset0:73 offset1:81
	ds_read2_b32 v[200:201], v186 offset0:138 offset1:146
	ds_read2_b32 v[204:205], v186 offset0:203 offset1:211
	v_mov_b64_e32 v[176:177], s[8:9]
	v_mad_u64_u32 v[190:191], s[12:13], s55, v134, v[176:177]
	v_lshl_add_u64 v[190:191], v[190:191], 0, v[136:137]
	s_waitcnt lgkmcnt(3)
	v_mul_f32_e32 v155, s56, v192
	s_waitcnt lgkmcnt(2)
	v_mul_f32_e32 v157, s56, v198
	global_store_dwordx2 v[190:191], v[188:189], off nt
	v_med3_f32 v155, v155, s53, v184
	v_med3_f32 v157, v157, s53, v184
	v_mov_b32_e32 v188, v133
	v_cvt_pk_fp8_f32 v188, v155, v157
	ds_read2_b32 v[190:191], v185 offset0:12 offset1:20
	ds_read2_b32 v[206:207], v185 offset0:77 offset1:85
	ds_read2_b32 v[208:209], v185 offset0:142 offset1:150
	s_waitcnt lgkmcnt(4)
	v_mul_f32_e32 v159, s56, v200
	s_waitcnt lgkmcnt(3)
	v_mul_f32_e32 v161, s56, v204
	v_med3_f32 v159, v159, s53, v184
	v_med3_f32 v155, v161, s53, v184
	ds_read2_b32 v[210:211], v185 offset0:207 offset1:215
	v_cvt_pk_fp8_f32 v188, v159, v155 op_sel:[0,0,1]
	s_waitcnt lgkmcnt(3)
	v_mul_f32_e32 v155, s56, v190
	s_waitcnt lgkmcnt(2)
	v_mul_f32_e32 v157, s56, v206
	v_med3_f32 v155, v155, s53, v184
	v_med3_f32 v157, v157, s53, v184
	v_mov_b32_e32 v189, v133
	v_cvt_pk_fp8_f32 v189, v155, v157
	s_waitcnt lgkmcnt(1)
	v_mul_f32_e32 v159, s56, v208
	s_waitcnt lgkmcnt(0)
	v_mul_f32_e32 v155, s56, v210
	v_med3_f32 v157, v159, s53, v184
	v_med3_f32 v155, v155, s53, v184
	v_cvt_pk_fp8_f32 v189, v157, v155 op_sel:[0,0,1]
	v_mad_u64_u32 v[212:213], s[12:13], s55, v138, v[176:177]
	v_lshl_add_u64 v[212:213], v[212:213], 0, v[136:137]
	v_mul_f32_e32 v155, s56, v193
	v_mul_f32_e32 v157, s56, v199
	global_store_dwordx2 v[212:213], v[188:189], off nt
	v_med3_f32 v155, v155, s53, v184
	v_med3_f32 v157, v157, s53, v184
	v_mov_b32_e32 v188, v133
	v_cvt_pk_fp8_f32 v188, v155, v157
	v_mul_f32_e32 v159, s56, v201
	v_mul_f32_e32 v155, s56, v205
	v_med3_f32 v157, v159, s53, v184
	v_med3_f32 v155, v155, s53, v184
	v_cvt_pk_fp8_f32 v188, v157, v155 op_sel:[0,0,1]
	v_mul_f32_e32 v155, s56, v191
	v_mul_f32_e32 v157, s56, v207
	v_med3_f32 v155, v155, s53, v184
	v_med3_f32 v157, v157, s53, v184
	v_mov_b32_e32 v189, v133
	v_cvt_pk_fp8_f32 v189, v155, v157
	v_mul_f32_e32 v159, s56, v209
	v_mul_f32_e32 v155, s56, v211
	v_med3_f32 v157, v159, s53, v184
	v_med3_f32 v155, v155, s53, v184
	v_cvt_pk_fp8_f32 v189, v157, v155 op_sel:[0,0,1]
	ds_read2_b32 v[192:193], v186 offset0:24 offset1:32
	ds_read2_b32 v[198:199], v186 offset0:89 offset1:97
	ds_read2_b32 v[200:201], v186 offset0:154 offset1:162
	ds_read2_b32 v[204:205], v186 offset0:219 offset1:227
	v_mad_u64_u32 v[190:191], s[12:13], s55, v140, v[176:177]
	v_lshl_add_u64 v[190:191], v[190:191], 0, v[136:137]
	s_waitcnt lgkmcnt(3)
	v_mul_f32_e32 v155, s56, v192
	s_waitcnt lgkmcnt(2)
	v_mul_f32_e32 v157, s56, v198
	global_store_dwordx2 v[190:191], v[188:189], off nt
	v_med3_f32 v155, v155, s53, v184
	v_med3_f32 v157, v157, s53, v184
	v_mov_b32_e32 v188, v133
	v_cvt_pk_fp8_f32 v188, v155, v157
	ds_read2_b32 v[190:191], v185 offset0:28 offset1:36
	ds_read2_b32 v[206:207], v185 offset0:93 offset1:101
	ds_read2_b32 v[208:209], v185 offset0:158 offset1:166
	s_waitcnt lgkmcnt(4)
	v_mul_f32_e32 v159, s56, v200
	s_waitcnt lgkmcnt(3)
	v_mul_f32_e32 v161, s56, v204
	v_med3_f32 v159, v159, s53, v184
	v_med3_f32 v155, v161, s53, v184
	ds_read2_b32 v[210:211], v185 offset0:223 offset1:231
	v_cvt_pk_fp8_f32 v188, v159, v155 op_sel:[0,0,1]
	s_waitcnt lgkmcnt(3)
	v_mul_f32_e32 v155, s56, v190
	s_waitcnt lgkmcnt(2)
	v_mul_f32_e32 v157, s56, v206
	v_med3_f32 v155, v155, s53, v184
	v_med3_f32 v157, v157, s53, v184
	v_mov_b32_e32 v189, v133
	v_cvt_pk_fp8_f32 v189, v155, v157
	s_waitcnt lgkmcnt(1)
	v_mul_f32_e32 v159, s56, v208
	s_waitcnt lgkmcnt(0)
	v_mul_f32_e32 v155, s56, v210
	v_med3_f32 v157, v159, s53, v184
	v_med3_f32 v155, v155, s53, v184
	v_cvt_pk_fp8_f32 v189, v157, v155 op_sel:[0,0,1]
	v_mad_u64_u32 v[212:213], s[12:13], s55, v142, v[176:177]
	v_lshl_add_u64 v[212:213], v[212:213], 0, v[136:137]
	v_mul_f32_e32 v155, s56, v193
	v_mul_f32_e32 v157, s56, v199
	global_store_dwordx2 v[212:213], v[188:189], off nt
	v_med3_f32 v155, v155, s53, v184
	v_med3_f32 v157, v157, s53, v184
	v_mov_b32_e32 v188, v133
	v_cvt_pk_fp8_f32 v188, v155, v157
	v_mul_f32_e32 v159, s56, v201
	v_mul_f32_e32 v155, s56, v205
	v_med3_f32 v157, v159, s53, v184
	v_med3_f32 v155, v155, s53, v184
	v_cvt_pk_fp8_f32 v188, v157, v155 op_sel:[0,0,1]
	v_mul_f32_e32 v155, s56, v191
	v_mul_f32_e32 v157, s56, v207
	v_med3_f32 v155, v155, s53, v184
	v_med3_f32 v157, v157, s53, v184
	v_mov_b32_e32 v189, v133
	v_cvt_pk_fp8_f32 v189, v155, v157
	v_mul_f32_e32 v159, s56, v209
	v_mul_f32_e32 v155, s56, v211
	v_med3_f32 v157, v159, s53, v184
	v_med3_f32 v155, v155, s53, v184
	v_cvt_pk_fp8_f32 v189, v157, v155 op_sel:[0,0,1]
	ds_read2_b32 v[192:193], v186 offset0:40 offset1:48
	ds_read2_b32 v[198:199], v186 offset0:105 offset1:113
	ds_read2_b32 v[200:201], v186 offset0:170 offset1:178
	ds_read2_b32 v[204:205], v186 offset0:235 offset1:243
	v_mad_u64_u32 v[190:191], s[12:13], s55, v144, v[176:177]
	v_lshl_add_u64 v[190:191], v[190:191], 0, v[136:137]
	s_waitcnt lgkmcnt(3)
	v_mul_f32_e32 v155, s56, v192
	s_waitcnt lgkmcnt(2)
	v_mul_f32_e32 v157, s56, v198
	global_store_dwordx2 v[190:191], v[188:189], off nt
	v_med3_f32 v155, v155, s53, v184
	v_med3_f32 v157, v157, s53, v184
	v_mov_b32_e32 v188, v133
	v_cvt_pk_fp8_f32 v188, v155, v157
	ds_read2_b32 v[190:191], v185 offset0:44 offset1:52
	ds_read2_b32 v[206:207], v185 offset0:109 offset1:117
	ds_read2_b32 v[208:209], v185 offset0:174 offset1:182
	s_waitcnt lgkmcnt(4)
	v_mul_f32_e32 v159, s56, v200
	s_waitcnt lgkmcnt(3)
	v_mul_f32_e32 v161, s56, v204
	v_med3_f32 v159, v159, s53, v184
	v_med3_f32 v155, v161, s53, v184
	ds_read2_b32 v[210:211], v185 offset0:239 offset1:247
	v_cvt_pk_fp8_f32 v188, v159, v155 op_sel:[0,0,1]
	s_waitcnt lgkmcnt(3)
	v_mul_f32_e32 v155, s56, v190
	s_waitcnt lgkmcnt(2)
	v_mul_f32_e32 v157, s56, v206
	v_med3_f32 v155, v155, s53, v184
	v_med3_f32 v157, v157, s53, v184
	v_mov_b32_e32 v189, v133
	v_cvt_pk_fp8_f32 v189, v155, v157
	s_waitcnt lgkmcnt(1)
	v_mul_f32_e32 v159, s56, v208
	s_waitcnt lgkmcnt(0)
	v_mul_f32_e32 v155, s56, v210
	v_med3_f32 v157, v159, s53, v184
	v_med3_f32 v155, v155, s53, v184
	v_cvt_pk_fp8_f32 v189, v157, v155 op_sel:[0,0,1]
	v_mad_u64_u32 v[212:213], s[12:13], s55, v146, v[176:177]
	v_lshl_add_u64 v[212:213], v[212:213], 0, v[136:137]
	v_mul_f32_e32 v155, s56, v193
	v_mul_f32_e32 v157, s56, v199
	global_store_dwordx2 v[212:213], v[188:189], off nt
	v_med3_f32 v155, v155, s53, v184
	v_med3_f32 v157, v157, s53, v184
	v_mov_b32_e32 v188, v133
	v_cvt_pk_fp8_f32 v188, v155, v157
	v_mul_f32_e32 v159, s56, v201
	v_mul_f32_e32 v155, s56, v205
	v_med3_f32 v157, v159, s53, v184
	v_med3_f32 v155, v155, s53, v184
	v_cvt_pk_fp8_f32 v188, v157, v155 op_sel:[0,0,1]
	v_mul_f32_e32 v155, s56, v191
	v_mul_f32_e32 v157, s56, v207
	v_med3_f32 v155, v155, s53, v184
	v_med3_f32 v157, v157, s53, v184
	v_mov_b32_e32 v189, v133
	v_cvt_pk_fp8_f32 v189, v155, v157
	v_mul_f32_e32 v159, s56, v209
	v_mul_f32_e32 v155, s56, v211
	v_med3_f32 v157, v159, s53, v184
	v_med3_f32 v155, v155, s53, v184
	v_cvt_pk_fp8_f32 v189, v157, v155 op_sel:[0,0,1]
	v_mul_f32_e32 v154, s56, v154
	v_mul_f32_e32 v155, s56, v156
	v_med3_f32 v157, v154, s53, v184
	v_med3_f32 v155, v155, s53, v184
	v_mov_b32_e32 v154, v133
	v_cvt_pk_fp8_f32 v154, v157, v155
	v_mul_f32_e32 v156, s56, v158
	v_mul_f32_e32 v155, s56, v174
	v_med3_f32 v156, v156, s53, v184
	v_med3_f32 v155, v155, s53, v184
	ds_read_b32 v158, v182 offset:18428
	v_cvt_pk_fp8_f32 v154, v156, v155 op_sel:[0,0,1]
	v_mul_f32_e32 v155, s56, v160
	v_mul_f32_e32 v156, s56, v172
	v_med3_f32 v159, v155, s53, v184
	v_med3_f32 v156, v156, s53, v184
	v_mov_b32_e32 v155, v133
	v_cvt_pk_fp8_f32 v155, v159, v156
	v_mul_f32_e32 v157, s56, v178
	s_waitcnt lgkmcnt(0)
	v_mul_f32_e32 v156, s56, v158
	v_med3_f32 v157, v157, s53, v184
	v_med3_f32 v156, v156, s53, v184
	v_cvt_pk_fp8_f32 v155, v157, v156 op_sel:[0,0,1]
	v_mad_u64_u32 v[190:191], s[12:13], s55, v148, v[176:177]
	v_mad_u64_u32 v[156:157], s[12:13], s55, v150, v[176:177]
	v_lshl_add_u64 v[190:191], v[190:191], 0, v[136:137]
	v_lshl_add_u64 v[156:157], v[156:157], 0, v[136:137]
	global_store_dwordx2 v[190:191], v[188:189], off nt
	global_store_dwordx2 v[156:157], v[154:155], off nt
	s_cbranch_execnz .LBB0_526
	s_branch .LBB0_525
